# speedup vs baseline: 1.0045x; 1.0035x over previous
.LBB6_32:
	s_or_b64 exec, exec, s[2:3]
	s_add_i32 s0, 0, 0x18000
	v_add_u32_e32 v48, s0, v39
	s_mov_b64 s[0:1], 0x80
	v_readfirstlane_b32 s22, v48
	v_add_u32_e32 v49, 0x2000, v48
	v_lshl_add_u64 v[2:3], v[30:31], 0, s[0:1]
	s_mov_b32 m0, s22
	v_readfirstlane_b32 s21, v49
	v_add_u32_e32 v46, 0x8000, v35
	s_waitcnt vmcnt(4)
	s_barrier
	global_load_lds_dwordx4 v[2:3], off
	v_lshl_add_u64 v[2:3], v[32:33], 0, s[0:1]
	s_mov_b32 m0, s21
	v_readfirstlane_b32 s19, v46
	v_add_u32_e32 v47, 0xa000, v35
	s_add_i32 s2, 0, 0x1c000
	global_load_lds_dwordx4 v[2:3], off
	v_lshl_add_u64 v[2:3], v[26:27], 0, s[0:1]
	s_mov_b32 m0, s19
	v_readfirstlane_b32 s17, v47
	v_add_u32_e32 v38, s2, v39
	global_load_lds_dwordx4 v[2:3], off
	v_lshl_add_u64 v[2:3], v[28:29], 0, s[0:1]
	s_mov_b32 m0, s17
	v_readfirstlane_b32 s4, v38
	v_add_u32_e32 v40, 0x2000, v38
	global_load_lds_dwordx4 v[2:3], off
	v_lshl_add_u64 v[2:3], v[22:23], 0, s[0:1]
	s_mov_b32 m0, s4
	v_readfirstlane_b32 s3, v40
	global_load_lds_dwordx4 v[2:3], off
	v_lshl_add_u64 v[2:3], v[24:25], 0, s[0:1]
	s_mov_b32 m0, s3
	v_and_b32_e32 v4, 48, v0
	global_load_lds_dwordx4 v[2:3], off
	v_lshlrev_b32_e32 v2, 6, v0
	v_and_b32_e32 v3, 0x3c0, v2
	v_and_b32_e32 v5, 32, v103
	v_bitop3_b32 v6, v3, v5, v4 bitop3:0x36
	v_and_b32_e32 v2, 0x3000, v2
	v_add3_u32 v234, 0, v2, v6
	v_add_u32_e32 v2, 0x10000, v234
	v_add_u32_e32 v4, 0x10800, v234
	s_waitcnt vmcnt(6)
	s_barrier
	v_add_u32_e32 v3, 0x10400, v234
	ds_read_b128 v[10:13], v2
	ds_read_b128 v[14:17], v3
	v_add_u32_e32 v5, 0x10c00, v234
	ds_read_b128 v[50:53], v4
	ds_read_b128 v[54:57], v5
	v_and_b32_e32 v1, 0x2000, v1
	v_add3_u32 v1, 0, v1, v6
	v_add_u32_e32 v37, 0xc000, v35
	v_add_u32_e32 v39, 0xe000, v35
	v_readfirstlane_b32 s7, v37
	v_lshl_add_u64 v[6:7], v[18:19], 0, s[0:1]
	s_mov_b32 m0, s7
	v_readfirstlane_b32 s2, v39
	global_load_lds_dwordx4 v[6:7], off
	v_lshl_add_u64 v[6:7], v[20:21], 0, s[0:1]
	s_mov_b32 m0, s2
	s_nop 0
	global_load_lds_dwordx4 v[6:7], off
	ds_read_b128 v[42:45], v1
	ds_read_b128 v[58:61], v1 offset:1024
	ds_read_b128 v[62:65], v1 offset:2048
	ds_read_b128 v[66:69], v1 offset:3072
	ds_read_b128 v[70:73], v1 offset:4096
	ds_read_b128 v[74:77], v1 offset:5120
	ds_read_b128 v[78:81], v1 offset:6144
	ds_read_b128 v[82:85], v1 offset:7168
	s_waitcnt lgkmcnt(8)
	s_barrier
	s_waitcnt lgkmcnt(0)
	s_setprio 1
	s_waitcnt lgkmcnt(0)
	v_mfma_f32_16x16x32_f16 v[6:9], v[10:13], v[42:45], 0
	v_mfma_f32_16x16x32_f16 v[86:89], v[14:17], v[58:61], v[6:9]
	v_mfma_f32_16x16x32_f16 v[6:9], v[50:53], v[42:45], 0
	v_mfma_f32_16x16x32_f16 v[90:93], v[54:57], v[58:61], v[6:9]
	v_mfma_f32_16x16x32_f16 v[6:9], v[10:13], v[62:65], 0
	v_mfma_f32_16x16x32_f16 v[94:97], v[14:17], v[66:69], v[6:9]
	v_mfma_f32_16x16x32_f16 v[6:9], v[50:53], v[62:65], 0
	v_mfma_f32_16x16x32_f16 v[98:101], v[54:57], v[66:69], v[6:9]
	v_mfma_f32_16x16x32_f16 v[6:9], v[10:13], v[70:73], 0
	v_mfma_f32_16x16x32_f16 v[102:105], v[14:17], v[74:77], v[6:9]
	v_mfma_f32_16x16x32_f16 v[6:9], v[50:53], v[70:73], 0
	v_mfma_f32_16x16x32_f16 v[106:109], v[54:57], v[74:77], v[6:9]
	v_mfma_f32_16x16x32_f16 v[6:9], v[10:13], v[78:81], 0
	v_mfma_f32_16x16x32_f16 v[110:113], v[14:17], v[82:85], v[6:9]
	v_mfma_f32_16x16x32_f16 v[6:9], v[50:53], v[78:81], 0
	v_mfma_f32_16x16x32_f16 v[114:117], v[54:57], v[82:85], v[6:9]
	s_setprio 0
	s_barrier
	s_mov_b64 s[0:1], 0x100
	v_readfirstlane_b32 s15, v36
	v_add_u32_e32 v41, 0x2000, v36
	s_nop 1
	v_add_u32_e32 v6, 0x14000, v234
	v_add_u32_e32 v8, 0x14800, v234
	v_lshl_add_u64 v[134:135], v[30:31], 0, s[0:1]
	s_mov_b32 m0, s15
	v_readfirstlane_b32 s5, v41
	v_add_u32_e32 v7, 0x14400, v234
	ds_read_b128 v[118:121], v6
	ds_read_b128 v[122:125], v7
	v_add_u32_e32 v9, 0x14c00, v234
	ds_read_b128 v[126:129], v8
	ds_read_b128 v[130:133], v9
	global_load_lds_dwordx4 v[134:135], off
	v_lshl_add_u64 v[134:135], v[32:33], 0, s[0:1]
	s_mov_b32 m0, s5
	s_nop 0
	global_load_lds_dwordx4 v[134:135], off
	s_barrier
	s_waitcnt lgkmcnt(0)
	s_setprio 1
	s_waitcnt lgkmcnt(0)
	v_mfma_f32_16x16x32_f16 v[134:137], v[118:121], v[42:45], 0
	v_mfma_f32_16x16x32_f16 v[42:45], v[126:129], v[42:45], 0
	v_mfma_f32_16x16x32_f16 v[134:137], v[122:125], v[58:61], v[134:137]
	v_mfma_f32_16x16x32_f16 v[58:61], v[130:133], v[58:61], v[42:45]
	v_mfma_f32_16x16x32_f16 v[42:45], v[118:121], v[62:65], 0
	v_mfma_f32_16x16x32_f16 v[138:141], v[122:125], v[66:69], v[42:45]
	v_mfma_f32_16x16x32_f16 v[42:45], v[126:129], v[62:65], 0
	v_mfma_f32_16x16x32_f16 v[62:65], v[130:133], v[66:69], v[42:45]
	v_mfma_f32_16x16x32_f16 v[42:45], v[118:121], v[70:73], 0
	v_mfma_f32_16x16x32_f16 v[66:69], v[122:125], v[74:77], v[42:45]
	v_mfma_f32_16x16x32_f16 v[42:45], v[126:129], v[70:73], 0
	v_mfma_f32_16x16x32_f16 v[70:73], v[130:133], v[74:77], v[42:45]
	v_mfma_f32_16x16x32_f16 v[42:45], v[118:121], v[78:81], 0
	v_mfma_f32_16x16x32_f16 v[74:77], v[122:125], v[82:85], v[42:45]
	v_mfma_f32_16x16x32_f16 v[42:45], v[126:129], v[78:81], 0
	v_mfma_f32_16x16x32_f16 v[78:81], v[130:133], v[82:85], v[42:45]
	s_setprio 0
	v_readfirstlane_b32 s16, v35
	s_nop 4
	v_lshl_add_u64 v[42:43], v[26:27], 0, s[0:1]
	s_mov_b32 m0, s16
	s_barrier
	ds_read_b128 v[82:85], v1 offset:16384
	ds_read_b128 v[142:145], v1 offset:17408
	ds_read_b128 v[146:149], v1 offset:18432
	ds_read_b128 v[150:153], v1 offset:19456
	ds_read_b128 v[154:157], v1 offset:20480
	ds_read_b128 v[158:161], v1 offset:21504
	ds_read_b128 v[162:165], v1 offset:22528
	ds_read_b128 v[166:169], v1 offset:23552
	global_load_lds_dwordx4 v[42:43], off
	v_add_u32_e32 v42, 0x2000, v35
	v_lshl_add_u64 v[44:45], v[28:29], 0, s[0:1]
	v_readfirstlane_b32 s10, v42
	s_mov_b32 m0, s10
	s_nop 0
	global_load_lds_dwordx4 v[44:45], off
	s_barrier
	s_waitcnt lgkmcnt(0)
	s_setprio 1
	s_waitcnt lgkmcnt(0)
	v_mfma_f32_16x16x32_f16 v[170:173], v[10:13], v[82:85], 0
	v_mfma_f32_16x16x32_f16 v[178:181], v[10:13], v[146:149], 0
	v_mfma_f32_16x16x32_f16 v[186:189], v[10:13], v[154:157], 0
	v_mfma_f32_16x16x32_f16 v[10:13], v[10:13], v[162:165], 0
	v_mfma_f32_16x16x32_f16 v[174:177], v[50:53], v[82:85], 0
	v_mfma_f32_16x16x32_f16 v[182:185], v[50:53], v[146:149], 0
	v_mfma_f32_16x16x32_f16 v[190:193], v[50:53], v[154:157], 0
	v_mfma_f32_16x16x32_f16 v[194:197], v[14:17], v[166:169], v[10:13]
	v_mfma_f32_16x16x32_f16 v[10:13], v[50:53], v[162:165], 0
	v_mfma_f32_16x16x32_f16 v[170:173], v[14:17], v[142:145], v[170:173]
	v_mfma_f32_16x16x32_f16 v[174:177], v[54:57], v[142:145], v[174:177]
	v_mfma_f32_16x16x32_f16 v[178:181], v[14:17], v[150:153], v[178:181]
	v_mfma_f32_16x16x32_f16 v[182:185], v[54:57], v[150:153], v[182:185]
	v_mfma_f32_16x16x32_f16 v[186:189], v[14:17], v[158:161], v[186:189]
	v_mfma_f32_16x16x32_f16 v[190:193], v[54:57], v[158:161], v[190:193]
	v_mfma_f32_16x16x32_f16 v[50:53], v[54:57], v[166:169], v[10:13]
	s_setprio 0
	s_barrier
	v_readfirstlane_b32 s14, v34
	v_add_u32_e32 v43, 0x2000, v34
	v_lshl_add_u64 v[10:11], v[22:23], 0, s[0:1]
	s_mov_b32 m0, s14
	v_readfirstlane_b32 s11, v43
	global_load_lds_dwordx4 v[10:11], off
	v_lshl_add_u64 v[10:11], v[24:25], 0, s[0:1]
	s_mov_b32 m0, s11
	s_nop 0
	global_load_lds_dwordx4 v[10:11], off
	s_waitcnt vmcnt(6)
	s_barrier
	s_setprio 1
	v_mfma_f32_16x16x32_f16 v[10:13], v[118:121], v[82:85], 0
	v_mfma_f32_16x16x32_f16 v[54:57], v[122:125], v[142:145], v[10:13]
	v_mfma_f32_16x16x32_f16 v[10:13], v[126:129], v[82:85], 0
	v_mfma_f32_16x16x32_f16 v[82:85], v[130:133], v[142:145], v[10:13]
	v_mfma_f32_16x16x32_f16 v[10:13], v[118:121], v[146:149], 0
	v_mfma_f32_16x16x32_f16 v[142:145], v[122:125], v[150:153], v[10:13]
	v_mfma_f32_16x16x32_f16 v[10:13], v[126:129], v[146:149], 0
	v_mfma_f32_16x16x32_f16 v[146:149], v[130:133], v[150:153], v[10:13]
	v_mfma_f32_16x16x32_f16 v[10:13], v[118:121], v[154:157], 0
	v_mfma_f32_16x16x32_f16 v[150:153], v[122:125], v[158:161], v[10:13]
	v_mfma_f32_16x16x32_f16 v[10:13], v[126:129], v[154:157], 0
	v_mfma_f32_16x16x32_f16 v[154:157], v[130:133], v[158:161], v[10:13]
	v_mfma_f32_16x16x32_f16 v[10:13], v[118:121], v[162:165], 0
	v_mfma_f32_16x16x32_f16 v[118:121], v[122:125], v[166:169], v[10:13]
	v_mfma_f32_16x16x32_f16 v[10:13], v[126:129], v[162:165], 0
	v_mfma_f32_16x16x32_f16 v[122:125], v[130:133], v[166:169], v[10:13]
	s_setprio 0
	s_nop 5
	v_add_u32_e32 v10, 0x18000, v234
	v_add_u32_e32 v12, 0x18800, v234
	s_barrier
	v_add_u32_e32 v11, 0x18400, v234
	ds_read_b128 v[126:129], v10
	ds_read_b128 v[130:133], v11
	v_add_u32_e32 v13, 0x18c00, v234
	ds_read_b128 v[158:161], v12
	ds_read_b128 v[162:165], v13
	v_add_u32_e32 v44, 0x4000, v35
	v_add_u32_e32 v45, 0x6000, v35
	v_readfirstlane_b32 s20, v44
	v_lshl_add_u64 v[14:15], v[18:19], 0, s[0:1]
	s_mov_b32 m0, s20
	v_readfirstlane_b32 s18, v45
	ds_read_b128 v[166:169], v1 offset:32768
	ds_read_b128 v[198:201], v1 offset:33792
	ds_read_b128 v[202:205], v1 offset:34816
	ds_read_b128 v[206:209], v1 offset:35840
	ds_read_b128 v[210:213], v1 offset:36864
	ds_read_b128 v[214:217], v1 offset:37888
	ds_read_b128 v[218:221], v1 offset:38912
	ds_read_b128 v[222:225], v1 offset:39936
	global_load_lds_dwordx4 v[14:15], off
	v_lshl_add_u64 v[14:15], v[20:21], 0, s[0:1]
	s_mov_b32 m0, s18
	s_nop 0
	global_load_lds_dwordx4 v[14:15], off
	s_waitcnt lgkmcnt(8)
	s_barrier
	s_waitcnt lgkmcnt(0)
	s_setprio 1
	s_waitcnt lgkmcnt(0)
	v_mfma_f32_16x16x32_f16 v[14:17], v[126:129], v[166:169], v[86:89]
	v_mfma_f32_16x16x32_f16 v[86:89], v[130:133], v[198:201], v[14:17]
	v_mfma_f32_16x16x32_f16 v[14:17], v[158:161], v[166:169], v[90:93]
	v_mfma_f32_16x16x32_f16 v[90:93], v[162:165], v[198:201], v[14:17]
	v_mfma_f32_16x16x32_f16 v[14:17], v[126:129], v[202:205], v[94:97]
	v_mfma_f32_16x16x32_f16 v[94:97], v[130:133], v[206:209], v[14:17]
	v_mfma_f32_16x16x32_f16 v[14:17], v[158:161], v[202:205], v[98:101]
	v_mfma_f32_16x16x32_f16 v[98:101], v[162:165], v[206:209], v[14:17]
	v_mfma_f32_16x16x32_f16 v[14:17], v[126:129], v[210:213], v[102:105]
	v_mfma_f32_16x16x32_f16 v[102:105], v[130:133], v[214:217], v[14:17]
	v_mfma_f32_16x16x32_f16 v[14:17], v[158:161], v[210:213], v[106:109]
	v_mfma_f32_16x16x32_f16 v[106:109], v[162:165], v[214:217], v[14:17]
	v_mfma_f32_16x16x32_f16 v[14:17], v[126:129], v[218:221], v[110:113]
	v_mfma_f32_16x16x32_f16 v[110:113], v[130:133], v[222:225], v[14:17]
	v_mfma_f32_16x16x32_f16 v[14:17], v[158:161], v[218:221], v[114:117]
	v_mfma_f32_16x16x32_f16 v[114:117], v[162:165], v[222:225], v[14:17]
	s_setprio 0
	s_barrier
	s_mov_b64 s[0:1], 0x180
	s_mov_b32 m0, s22
	s_nop 2
	v_add_u32_e32 v14, 0x1c000, v234
	v_add_u32_e32 v16, 0x1c800, v234
	v_lshl_add_u64 v[242:243], v[30:31], 0, s[0:1]
	v_add_u32_e32 v15, 0x1c400, v234
	ds_read_b128 v[226:229], v14
	ds_read_b128 v[230:233], v15
	v_add_u32_e32 v17, 0x1cc00, v234
	ds_read_b128 v[234:237], v16
	ds_read_b128 v[238:241], v17
	global_load_lds_dwordx4 v[242:243], off
	v_lshl_add_u64 v[242:243], v[32:33], 0, s[0:1]
	s_mov_b32 m0, s21
	s_nop 0
	global_load_lds_dwordx4 v[242:243], off
	s_barrier
	s_waitcnt lgkmcnt(0)
	s_setprio 1
	s_waitcnt lgkmcnt(0)
	v_mfma_f32_16x16x32_f16 v[134:137], v[226:229], v[166:169], v[134:137]
	v_mfma_f32_16x16x32_f16 v[138:141], v[226:229], v[202:205], v[138:141]
	v_mfma_f32_16x16x32_f16 v[66:69], v[226:229], v[210:213], v[66:69]
	v_mfma_f32_16x16x32_f16 v[70:73], v[234:237], v[210:213], v[70:73]
	v_mfma_f32_16x16x32_f16 v[74:77], v[226:229], v[218:221], v[74:77]
	v_mfma_f32_16x16x32_f16 v[78:81], v[234:237], v[218:221], v[78:81]
	v_mfma_f32_16x16x32_f16 v[134:137], v[230:233], v[198:201], v[134:137]
	v_mfma_f32_16x16x32_f16 v[58:61], v[234:237], v[166:169], v[58:61]
	v_mfma_f32_16x16x32_f16 v[138:141], v[230:233], v[206:209], v[138:141]
	v_mfma_f32_16x16x32_f16 v[62:65], v[234:237], v[202:205], v[62:65]
	v_mfma_f32_16x16x32_f16 v[66:69], v[230:233], v[214:217], v[66:69]
	v_mfma_f32_16x16x32_f16 v[70:73], v[238:241], v[214:217], v[70:73]
	v_mfma_f32_16x16x32_f16 v[74:77], v[230:233], v[222:225], v[74:77]
	v_mfma_f32_16x16x32_f16 v[78:81], v[238:241], v[222:225], v[78:81]
	v_mfma_f32_16x16x32_f16 v[58:61], v[238:241], v[198:201], v[58:61]
	v_mfma_f32_16x16x32_f16 v[62:65], v[238:241], v[206:209], v[62:65]
	s_setprio 0
	s_mov_b32 m0, s19
	v_lshl_add_u64 v[242:243], v[26:27], 0, s[0:1]
	s_barrier
	ds_read_b128 v[166:169], v1 offset:49152
	ds_read_b128 v[198:201], v1 offset:50176
	ds_read_b128 v[202:205], v1 offset:51200
	ds_read_b128 v[206:209], v1 offset:52224
	ds_read_b128 v[210:213], v1 offset:53248
	ds_read_b128 v[214:217], v1 offset:54272
	ds_read_b128 v[218:221], v1 offset:55296
	ds_read_b128 v[222:225], v1 offset:56320
	global_load_lds_dwordx4 v[242:243], off
	v_lshl_add_u64 v[242:243], v[28:29], 0, s[0:1]
	s_mov_b32 m0, s17
	s_nop 0
	global_load_lds_dwordx4 v[242:243], off
	s_barrier
	s_waitcnt lgkmcnt(0)
	s_setprio 1
	s_waitcnt lgkmcnt(0)
	v_mfma_f32_16x16x32_f16 v[170:173], v[126:129], v[166:169], v[170:173]
	v_mfma_f32_16x16x32_f16 v[178:181], v[126:129], v[202:205], v[178:181]
	v_mfma_f32_16x16x32_f16 v[186:189], v[126:129], v[210:213], v[186:189]
	v_mfma_f32_16x16x32_f16 v[126:129], v[126:129], v[218:221], v[194:197]
	v_mfma_f32_16x16x32_f16 v[174:177], v[158:161], v[166:169], v[174:177]
	v_mfma_f32_16x16x32_f16 v[182:185], v[158:161], v[202:205], v[182:185]
	v_mfma_f32_16x16x32_f16 v[190:193], v[158:161], v[210:213], v[190:193]
	v_mfma_f32_16x16x32_f16 v[126:129], v[130:133], v[222:225], v[126:129]
	v_mfma_f32_16x16x32_f16 v[50:53], v[158:161], v[218:221], v[50:53]
	v_mfma_f32_16x16x32_f16 v[170:173], v[130:133], v[198:201], v[170:173]
	v_mfma_f32_16x16x32_f16 v[174:177], v[162:165], v[198:201], v[174:177]
	v_mfma_f32_16x16x32_f16 v[178:181], v[130:133], v[206:209], v[178:181]
	v_mfma_f32_16x16x32_f16 v[182:185], v[162:165], v[206:209], v[182:185]
	v_mfma_f32_16x16x32_f16 v[186:189], v[130:133], v[214:217], v[186:189]
	v_mfma_f32_16x16x32_f16 v[190:193], v[162:165], v[214:217], v[190:193]
	v_mfma_f32_16x16x32_f16 v[50:53], v[162:165], v[222:225], v[50:53]
	s_setprio 0
	s_barrier
	s_mov_b32 m0, s4
	v_lshl_add_u64 v[130:131], v[22:23], 0, s[0:1]
	global_load_lds_dwordx4 v[130:131], off
	v_lshl_add_u64 v[130:131], v[24:25], 0, s[0:1]
	s_mov_b32 m0, s3
	s_nop 0
	global_load_lds_dwordx4 v[130:131], off
	s_waitcnt vmcnt(6)
	s_barrier
	s_setprio 1
	v_mfma_f32_16x16x32_f16 v[82:85], v[234:237], v[166:169], v[82:85]
	v_mfma_f32_16x16x32_f16 v[130:133], v[226:229], v[202:205], v[142:145]
	v_mfma_f32_16x16x32_f16 v[142:145], v[234:237], v[202:205], v[146:149]
	v_mfma_f32_16x16x32_f16 v[146:149], v[226:229], v[210:213], v[150:153]
	v_mfma_f32_16x16x32_f16 v[150:153], v[234:237], v[210:213], v[154:157]
	v_mfma_f32_16x16x32_f16 v[118:121], v[226:229], v[218:221], v[118:121]
	v_mfma_f32_16x16x32_f16 v[122:125], v[234:237], v[218:221], v[122:125]
	v_mfma_f32_16x16x32_f16 v[54:57], v[226:229], v[166:169], v[54:57]
	v_mfma_f32_16x16x32_f16 v[82:85], v[238:241], v[198:201], v[82:85]
	v_mfma_f32_16x16x32_f16 v[130:133], v[230:233], v[206:209], v[130:133]
	v_mfma_f32_16x16x32_f16 v[142:145], v[238:241], v[206:209], v[142:145]
	v_mfma_f32_16x16x32_f16 v[150:153], v[238:241], v[214:217], v[150:153]
	v_mfma_f32_16x16x32_f16 v[118:121], v[230:233], v[222:225], v[118:121]
	v_mfma_f32_16x16x32_f16 v[122:125], v[238:241], v[222:225], v[122:125]
	v_mfma_f32_16x16x32_f16 v[54:57], v[230:233], v[198:201], v[54:57]
	v_mfma_f32_16x16x32_f16 v[146:149], v[230:233], v[214:217], v[146:149]
	s_setprio 0
	s_barrier
	ds_read_b128 v[154:157], v2
	ds_read_b128 v[158:161], v3
	ds_read_b128 v[162:165], v4
	ds_read_b128 v[166:169], v5
	s_mov_b32 m0, s7
	v_lshl_add_u64 v[194:195], v[18:19], 0, s[0:1]
	global_load_lds_dwordx4 v[194:195], off
	v_lshl_add_u64 v[194:195], v[20:21], 0, s[0:1]
	s_mov_b32 m0, s2
	s_nop 0
	global_load_lds_dwordx4 v[194:195], off
	ds_read_b128 v[194:197], v1
	ds_read_b128 v[198:201], v1 offset:1024
	ds_read_b128 v[202:205], v1 offset:2048
	ds_read_b128 v[206:209], v1 offset:3072
	ds_read_b128 v[210:213], v1 offset:4096
	ds_read_b128 v[214:217], v1 offset:5120
	ds_read_b128 v[218:221], v1 offset:6144
	ds_read_b128 v[222:225], v1 offset:7168
	s_waitcnt lgkmcnt(8)
	s_barrier
	s_waitcnt lgkmcnt(0)
	s_setprio 1
	s_waitcnt lgkmcnt(0)
	v_mfma_f32_16x16x32_f16 v[86:89], v[154:157], v[194:197], v[86:89]
	v_mfma_f32_16x16x32_f16 v[90:93], v[162:165], v[194:197], v[90:93]
	v_mfma_f32_16x16x32_f16 v[94:97], v[154:157], v[202:205], v[94:97]
	v_mfma_f32_16x16x32_f16 v[98:101], v[162:165], v[202:205], v[98:101]
	v_mfma_f32_16x16x32_f16 v[102:105], v[154:157], v[210:213], v[102:105]
	v_mfma_f32_16x16x32_f16 v[106:109], v[162:165], v[210:213], v[106:109]
	v_mfma_f32_16x16x32_f16 v[110:113], v[154:157], v[218:221], v[110:113]
	v_mfma_f32_16x16x32_f16 v[114:117], v[162:165], v[218:221], v[114:117]
	v_mfma_f32_16x16x32_f16 v[86:89], v[158:161], v[198:201], v[86:89]
	v_mfma_f32_16x16x32_f16 v[90:93], v[166:169], v[198:201], v[90:93]
	v_mfma_f32_16x16x32_f16 v[94:97], v[158:161], v[206:209], v[94:97]
	v_mfma_f32_16x16x32_f16 v[98:101], v[166:169], v[206:209], v[98:101]
	v_mfma_f32_16x16x32_f16 v[102:105], v[158:161], v[214:217], v[102:105]
	v_mfma_f32_16x16x32_f16 v[106:109], v[166:169], v[214:217], v[106:109]
	v_mfma_f32_16x16x32_f16 v[110:113], v[158:161], v[222:225], v[110:113]
	v_mfma_f32_16x16x32_f16 v[114:117], v[166:169], v[222:225], v[114:117]
	s_setprio 0
	s_barrier
	s_mov_b64 s[0:1], 0x200
	s_mov_b32 m0, s15
	v_lshl_add_u64 v[242:243], v[30:31], 0, s[0:1]
	ds_read_b128 v[226:229], v6
	ds_read_b128 v[230:233], v7
	ds_read_b128 v[234:237], v8
	ds_read_b128 v[238:241], v9
	global_load_lds_dwordx4 v[242:243], off
	v_lshl_add_u64 v[242:243], v[32:33], 0, s[0:1]
	s_mov_b32 m0, s5
	s_nop 0
	global_load_lds_dwordx4 v[242:243], off
	s_barrier
	s_waitcnt lgkmcnt(0)
	s_setprio 1
	s_waitcnt lgkmcnt(0)
	v_mfma_f32_16x16x32_f16 v[134:137], v[226:229], v[194:197], v[134:137]
	v_mfma_f32_16x16x32_f16 v[138:141], v[226:229], v[202:205], v[138:141]
	v_mfma_f32_16x16x32_f16 v[66:69], v[226:229], v[210:213], v[66:69]
	v_mfma_f32_16x16x32_f16 v[70:73], v[234:237], v[210:213], v[70:73]
	v_mfma_f32_16x16x32_f16 v[74:77], v[226:229], v[218:221], v[74:77]
	v_mfma_f32_16x16x32_f16 v[78:81], v[234:237], v[218:221], v[78:81]
	v_mfma_f32_16x16x32_f16 v[134:137], v[230:233], v[198:201], v[134:137]
	v_mfma_f32_16x16x32_f16 v[58:61], v[234:237], v[194:197], v[58:61]
	v_mfma_f32_16x16x32_f16 v[138:141], v[230:233], v[206:209], v[138:141]
	v_mfma_f32_16x16x32_f16 v[62:65], v[234:237], v[202:205], v[62:65]
	v_mfma_f32_16x16x32_f16 v[66:69], v[230:233], v[214:217], v[66:69]
	v_mfma_f32_16x16x32_f16 v[70:73], v[238:241], v[214:217], v[70:73]
	v_mfma_f32_16x16x32_f16 v[74:77], v[230:233], v[222:225], v[74:77]
	v_mfma_f32_16x16x32_f16 v[78:81], v[238:241], v[222:225], v[78:81]
	v_mfma_f32_16x16x32_f16 v[58:61], v[238:241], v[198:201], v[58:61]
	v_mfma_f32_16x16x32_f16 v[62:65], v[238:241], v[206:209], v[62:65]
	s_setprio 0
	s_mov_b32 m0, s16
	v_lshl_add_u64 v[242:243], v[26:27], 0, s[0:1]
	s_barrier
	ds_read_b128 v[194:197], v1 offset:16384
	ds_read_b128 v[198:201], v1 offset:17408
	ds_read_b128 v[202:205], v1 offset:18432
	ds_read_b128 v[206:209], v1 offset:19456
	ds_read_b128 v[210:213], v1 offset:20480
	ds_read_b128 v[214:217], v1 offset:21504
	ds_read_b128 v[218:221], v1 offset:22528
	ds_read_b128 v[222:225], v1 offset:23552
	global_load_lds_dwordx4 v[242:243], off
	v_lshl_add_u64 v[242:243], v[28:29], 0, s[0:1]
	s_mov_b32 m0, s10
	s_nop 0
	global_load_lds_dwordx4 v[242:243], off
	s_barrier
	s_waitcnt lgkmcnt(0)
	s_setprio 1
	s_waitcnt lgkmcnt(0)
	v_mfma_f32_16x16x32_f16 v[126:129], v[154:157], v[218:221], v[126:129]
	v_mfma_f32_16x16x32_f16 v[170:173], v[154:157], v[194:197], v[170:173]
	v_mfma_f32_16x16x32_f16 v[174:177], v[162:165], v[194:197], v[174:177]
	v_mfma_f32_16x16x32_f16 v[178:181], v[154:157], v[202:205], v[178:181]
	v_mfma_f32_16x16x32_f16 v[182:185], v[162:165], v[202:205], v[182:185]
	v_mfma_f32_16x16x32_f16 v[186:189], v[154:157], v[210:213], v[186:189]
	v_mfma_f32_16x16x32_f16 v[190:193], v[162:165], v[210:213], v[190:193]
	v_mfma_f32_16x16x32_f16 v[126:129], v[158:161], v[222:225], v[126:129]
	v_mfma_f32_16x16x32_f16 v[50:53], v[162:165], v[218:221], v[50:53]
	v_mfma_f32_16x16x32_f16 v[170:173], v[158:161], v[198:201], v[170:173]
	v_mfma_f32_16x16x32_f16 v[174:177], v[166:169], v[198:201], v[174:177]
	v_mfma_f32_16x16x32_f16 v[178:181], v[158:161], v[206:209], v[178:181]
	v_mfma_f32_16x16x32_f16 v[182:185], v[166:169], v[206:209], v[182:185]
	v_mfma_f32_16x16x32_f16 v[186:189], v[158:161], v[214:217], v[186:189]
	v_mfma_f32_16x16x32_f16 v[190:193], v[166:169], v[214:217], v[190:193]
	v_mfma_f32_16x16x32_f16 v[50:53], v[166:169], v[222:225], v[50:53]
	s_setprio 0
	s_barrier
	s_mov_b32 m0, s14
	v_lshl_add_u64 v[154:155], v[22:23], 0, s[0:1]
	global_load_lds_dwordx4 v[154:155], off
	v_lshl_add_u64 v[154:155], v[24:25], 0, s[0:1]
	s_mov_b32 m0, s11
	s_nop 0
	global_load_lds_dwordx4 v[154:155], off
	s_waitcnt vmcnt(6)
	s_barrier
	s_setprio 1
	v_mfma_f32_16x16x32_f16 v[82:85], v[234:237], v[194:197], v[82:85]
	v_mfma_f32_16x16x32_f16 v[130:133], v[226:229], v[202:205], v[130:133]
	v_mfma_f32_16x16x32_f16 v[142:145], v[234:237], v[202:205], v[142:145]
	v_mfma_f32_16x16x32_f16 v[150:153], v[234:237], v[210:213], v[150:153]
	v_mfma_f32_16x16x32_f16 v[118:121], v[226:229], v[218:221], v[118:121]
	v_mfma_f32_16x16x32_f16 v[122:125], v[234:237], v[218:221], v[122:125]
	v_mfma_f32_16x16x32_f16 v[54:57], v[226:229], v[194:197], v[54:57]
	v_mfma_f32_16x16x32_f16 v[82:85], v[238:241], v[198:201], v[82:85]
	v_mfma_f32_16x16x32_f16 v[130:133], v[230:233], v[206:209], v[130:133]
	v_mfma_f32_16x16x32_f16 v[142:145], v[238:241], v[206:209], v[142:145]
	v_mfma_f32_16x16x32_f16 v[146:149], v[226:229], v[210:213], v[146:149]
	v_mfma_f32_16x16x32_f16 v[150:153], v[238:241], v[214:217], v[150:153]
	v_mfma_f32_16x16x32_f16 v[118:121], v[230:233], v[222:225], v[118:121]
	v_mfma_f32_16x16x32_f16 v[122:125], v[238:241], v[222:225], v[122:125]
	v_mfma_f32_16x16x32_f16 v[54:57], v[230:233], v[198:201], v[54:57]
	v_mfma_f32_16x16x32_f16 v[146:149], v[230:233], v[214:217], v[146:149]
	s_setprio 0
	s_barrier
	ds_read_b128 v[154:157], v10
	ds_read_b128 v[158:161], v11
	ds_read_b128 v[162:165], v12
	ds_read_b128 v[166:169], v13
	s_mov_b32 m0, s20
	v_lshl_add_u64 v[226:227], v[18:19], 0, s[0:1]
	ds_read_b128 v[194:197], v1 offset:32768
	ds_read_b128 v[198:201], v1 offset:33792
	ds_read_b128 v[202:205], v1 offset:34816
	ds_read_b128 v[206:209], v1 offset:35840
	ds_read_b128 v[210:213], v1 offset:36864
	ds_read_b128 v[214:217], v1 offset:37888
	ds_read_b128 v[218:221], v1 offset:38912
	ds_read_b128 v[222:225], v1 offset:39936
	global_load_lds_dwordx4 v[226:227], off
	v_lshl_add_u64 v[226:227], v[20:21], 0, s[0:1]
	s_mov_b32 m0, s18
	s_nop 0
	global_load_lds_dwordx4 v[226:227], off
	s_waitcnt lgkmcnt(8)
	s_barrier
	s_waitcnt lgkmcnt(0)
	s_setprio 1
	s_waitcnt lgkmcnt(0)
	v_mfma_f32_16x16x32_f16 v[86:89], v[154:157], v[194:197], v[86:89]
	v_mfma_f32_16x16x32_f16 v[90:93], v[162:165], v[194:197], v[90:93]
	v_mfma_f32_16x16x32_f16 v[94:97], v[154:157], v[202:205], v[94:97]
	v_mfma_f32_16x16x32_f16 v[98:101], v[162:165], v[202:205], v[98:101]
	v_mfma_f32_16x16x32_f16 v[102:105], v[154:157], v[210:213], v[102:105]
	v_mfma_f32_16x16x32_f16 v[106:109], v[162:165], v[210:213], v[106:109]
	v_mfma_f32_16x16x32_f16 v[110:113], v[154:157], v[218:221], v[110:113]
	v_mfma_f32_16x16x32_f16 v[114:117], v[162:165], v[218:221], v[114:117]
	v_mfma_f32_16x16x32_f16 v[86:89], v[158:161], v[198:201], v[86:89]
	v_mfma_f32_16x16x32_f16 v[90:93], v[166:169], v[198:201], v[90:93]
	v_mfma_f32_16x16x32_f16 v[94:97], v[158:161], v[206:209], v[94:97]
	v_mfma_f32_16x16x32_f16 v[98:101], v[166:169], v[206:209], v[98:101]
	v_mfma_f32_16x16x32_f16 v[102:105], v[158:161], v[214:217], v[102:105]
	v_mfma_f32_16x16x32_f16 v[106:109], v[166:169], v[214:217], v[106:109]
	v_mfma_f32_16x16x32_f16 v[110:113], v[158:161], v[222:225], v[110:113]
	v_mfma_f32_16x16x32_f16 v[114:117], v[166:169], v[222:225], v[114:117]
	s_setprio 0
	s_barrier
	s_mov_b64 s[0:1], 0x280
	v_readfirstlane_b32 s10, v48
	v_lshl_add_u64 v[242:243], v[30:31], 0, s[0:1]
	s_mov_b32 m0, s10
	v_readfirstlane_b32 s2, v49
	ds_read_b128 v[226:229], v14
	ds_read_b128 v[230:233], v15
	ds_read_b128 v[234:237], v16
	ds_read_b128 v[238:241], v17
	global_load_lds_dwordx4 v[242:243], off
	v_lshl_add_u64 v[242:243], v[32:33], 0, s[0:1]
	s_mov_b32 m0, s2
	s_nop 0
	global_load_lds_dwordx4 v[242:243], off
	s_barrier
	s_waitcnt lgkmcnt(0)
	s_setprio 1
	s_waitcnt lgkmcnt(0)
	v_mfma_f32_16x16x32_f16 v[134:137], v[226:229], v[194:197], v[134:137]
	v_mfma_f32_16x16x32_f16 v[138:141], v[226:229], v[202:205], v[138:141]
	v_mfma_f32_16x16x32_f16 v[66:69], v[226:229], v[210:213], v[66:69]
	v_mfma_f32_16x16x32_f16 v[70:73], v[234:237], v[210:213], v[70:73]
	v_mfma_f32_16x16x32_f16 v[74:77], v[226:229], v[218:221], v[74:77]
	v_mfma_f32_16x16x32_f16 v[78:81], v[234:237], v[218:221], v[78:81]
	v_mfma_f32_16x16x32_f16 v[134:137], v[230:233], v[198:201], v[134:137]
	v_mfma_f32_16x16x32_f16 v[58:61], v[234:237], v[194:197], v[58:61]
	v_mfma_f32_16x16x32_f16 v[138:141], v[230:233], v[206:209], v[138:141]
	v_mfma_f32_16x16x32_f16 v[62:65], v[234:237], v[202:205], v[62:65]
	v_mfma_f32_16x16x32_f16 v[66:69], v[230:233], v[214:217], v[66:69]
	v_mfma_f32_16x16x32_f16 v[70:73], v[238:241], v[214:217], v[70:73]
	v_mfma_f32_16x16x32_f16 v[74:77], v[230:233], v[222:225], v[74:77]
	v_mfma_f32_16x16x32_f16 v[78:81], v[238:241], v[222:225], v[78:81]
	v_mfma_f32_16x16x32_f16 v[58:61], v[238:241], v[198:201], v[58:61]
	v_mfma_f32_16x16x32_f16 v[62:65], v[238:241], v[206:209], v[62:65]
	s_setprio 0
	v_readfirstlane_b32 s11, v46
	v_lshl_add_u64 v[48:49], v[26:27], 0, s[0:1]
	s_mov_b32 m0, s11
	v_readfirstlane_b32 s3, v47
	s_barrier
	ds_read_b128 v[194:197], v1 offset:49152
	ds_read_b128 v[198:201], v1 offset:50176
	ds_read_b128 v[202:205], v1 offset:51200
	ds_read_b128 v[206:209], v1 offset:52224
	ds_read_b128 v[210:213], v1 offset:53248
	ds_read_b128 v[214:217], v1 offset:54272
	ds_read_b128 v[218:221], v1 offset:55296
	ds_read_b128 v[222:225], v1 offset:56320
	global_load_lds_dwordx4 v[48:49], off
	v_lshl_add_u64 v[48:49], v[28:29], 0, s[0:1]
	s_mov_b32 m0, s3
	s_nop 0
	global_load_lds_dwordx4 v[48:49], off
	s_barrier
	s_waitcnt lgkmcnt(0)
	s_setprio 1
	s_waitcnt lgkmcnt(0)
	v_mfma_f32_16x16x32_f16 v[126:129], v[154:157], v[218:221], v[126:129]
	v_mfma_f32_16x16x32_f16 v[46:49], v[154:157], v[194:197], v[170:173]
	v_mfma_f32_16x16x32_f16 v[170:173], v[162:165], v[194:197], v[174:177]
	v_mfma_f32_16x16x32_f16 v[174:177], v[154:157], v[202:205], v[178:181]
	v_mfma_f32_16x16x32_f16 v[178:181], v[162:165], v[202:205], v[182:185]
	v_mfma_f32_16x16x32_f16 v[182:185], v[154:157], v[210:213], v[186:189]
	v_mfma_f32_16x16x32_f16 v[186:189], v[162:165], v[210:213], v[190:193]
	v_mfma_f32_16x16x32_f16 v[126:129], v[158:161], v[222:225], v[126:129]
	v_mfma_f32_16x16x32_f16 v[50:53], v[162:165], v[218:221], v[50:53]
	v_mfma_f32_16x16x32_f16 v[46:49], v[158:161], v[198:201], v[46:49]
	v_mfma_f32_16x16x32_f16 v[170:173], v[166:169], v[198:201], v[170:173]
	v_mfma_f32_16x16x32_f16 v[174:177], v[158:161], v[206:209], v[174:177]
	v_mfma_f32_16x16x32_f16 v[178:181], v[166:169], v[206:209], v[178:181]
	v_mfma_f32_16x16x32_f16 v[182:185], v[158:161], v[214:217], v[182:185]
	v_mfma_f32_16x16x32_f16 v[186:189], v[166:169], v[214:217], v[186:189]
	v_mfma_f32_16x16x32_f16 v[50:53], v[166:169], v[222:225], v[50:53]
	s_setprio 0
	s_barrier
	v_readfirstlane_b32 s5, v38
	v_lshl_add_u64 v[154:155], v[22:23], 0, s[0:1]
	s_mov_b32 m0, s5
	v_readfirstlane_b32 s4, v40
	global_load_lds_dwordx4 v[154:155], off
	v_lshl_add_u64 v[154:155], v[24:25], 0, s[0:1]
	s_mov_b32 m0, s4
	s_nop 0
	global_load_lds_dwordx4 v[154:155], off
	s_waitcnt vmcnt(6)
	s_barrier
	s_setprio 1
	v_mfma_f32_16x16x32_f16 v[82:85], v[234:237], v[194:197], v[82:85]
	v_mfma_f32_16x16x32_f16 v[130:133], v[226:229], v[202:205], v[130:133]
	v_mfma_f32_16x16x32_f16 v[142:145], v[234:237], v[202:205], v[142:145]
	v_mfma_f32_16x16x32_f16 v[150:153], v[234:237], v[210:213], v[150:153]
	v_mfma_f32_16x16x32_f16 v[118:121], v[226:229], v[218:221], v[118:121]
	v_mfma_f32_16x16x32_f16 v[122:125], v[234:237], v[218:221], v[122:125]
	v_mfma_f32_16x16x32_f16 v[54:57], v[226:229], v[194:197], v[54:57]
	v_mfma_f32_16x16x32_f16 v[82:85], v[238:241], v[198:201], v[82:85]
	v_mfma_f32_16x16x32_f16 v[130:133], v[230:233], v[206:209], v[130:133]
	v_mfma_f32_16x16x32_f16 v[142:145], v[238:241], v[206:209], v[142:145]
	v_mfma_f32_16x16x32_f16 v[146:149], v[226:229], v[210:213], v[146:149]
	v_mfma_f32_16x16x32_f16 v[150:153], v[238:241], v[214:217], v[150:153]
	v_mfma_f32_16x16x32_f16 v[118:121], v[230:233], v[222:225], v[118:121]
	v_mfma_f32_16x16x32_f16 v[122:125], v[238:241], v[222:225], v[122:125]
	v_mfma_f32_16x16x32_f16 v[54:57], v[230:233], v[198:201], v[54:57]
	v_mfma_f32_16x16x32_f16 v[146:149], v[230:233], v[214:217], v[146:149]
	s_setprio 0
	s_barrier
	ds_read_b128 v[154:157], v2
	ds_read_b128 v[158:161], v3
	ds_read_b128 v[162:165], v4
	ds_read_b128 v[166:169], v5
	v_readfirstlane_b32 s14, v37
	v_lshl_add_u64 v[190:191], v[18:19], 0, s[0:1]
	s_mov_b32 m0, s14
	v_readfirstlane_b32 s7, v39
	global_load_lds_dwordx4 v[190:191], off
	v_lshl_add_u64 v[190:191], v[20:21], 0, s[0:1]
	s_mov_b32 m0, s7
	s_nop 0
	global_load_lds_dwordx4 v[190:191], off
	ds_read_b128 v[190:193], v1
	ds_read_b128 v[194:197], v1 offset:1024
	ds_read_b128 v[198:201], v1 offset:2048
	ds_read_b128 v[202:205], v1 offset:3072
	ds_read_b128 v[206:209], v1 offset:4096
	ds_read_b128 v[210:213], v1 offset:5120
	ds_read_b128 v[214:217], v1 offset:6144
	ds_read_b128 v[218:221], v1 offset:7168
	s_waitcnt lgkmcnt(8)
	s_barrier
	s_waitcnt lgkmcnt(0)
	s_setprio 1
	s_waitcnt lgkmcnt(0)
	v_mfma_f32_16x16x32_f16 v[86:89], v[154:157], v[190:193], v[86:89]
	v_mfma_f32_16x16x32_f16 v[90:93], v[162:165], v[190:193], v[90:93]
	v_mfma_f32_16x16x32_f16 v[94:97], v[154:157], v[198:201], v[94:97]
	v_mfma_f32_16x16x32_f16 v[98:101], v[162:165], v[198:201], v[98:101]
	v_mfma_f32_16x16x32_f16 v[102:105], v[154:157], v[206:209], v[102:105]
	v_mfma_f32_16x16x32_f16 v[106:109], v[162:165], v[206:209], v[106:109]
	v_mfma_f32_16x16x32_f16 v[110:113], v[154:157], v[214:217], v[110:113]
	v_mfma_f32_16x16x32_f16 v[114:117], v[162:165], v[214:217], v[114:117]
	v_mfma_f32_16x16x32_f16 v[86:89], v[158:161], v[194:197], v[86:89]
	v_mfma_f32_16x16x32_f16 v[90:93], v[166:169], v[194:197], v[90:93]
	v_mfma_f32_16x16x32_f16 v[94:97], v[158:161], v[202:205], v[94:97]
	v_mfma_f32_16x16x32_f16 v[98:101], v[166:169], v[202:205], v[98:101]
	v_mfma_f32_16x16x32_f16 v[102:105], v[158:161], v[210:213], v[102:105]
	v_mfma_f32_16x16x32_f16 v[106:109], v[166:169], v[210:213], v[106:109]
	v_mfma_f32_16x16x32_f16 v[110:113], v[158:161], v[218:221], v[110:113]
	v_mfma_f32_16x16x32_f16 v[114:117], v[166:169], v[218:221], v[114:117]
	s_setprio 0
	s_barrier
	s_mov_b64 s[0:1], 0x300
	v_readfirstlane_b32 s15, v36
	v_lshl_add_u64 v[38:39], v[30:31], 0, s[0:1]
	s_mov_b32 m0, s15
	v_readfirstlane_b32 s15, v41
	ds_read_b128 v[222:225], v6
	ds_read_b128 v[226:229], v7
	ds_read_b128 v[230:233], v8
	ds_read_b128 v[234:237], v9
	global_load_lds_dwordx4 v[38:39], off
	v_lshl_add_u64 v[36:37], v[32:33], 0, s[0:1]
	s_mov_b32 m0, s15
	s_nop 0
	global_load_lds_dwordx4 v[36:37], off
	s_barrier
	s_waitcnt lgkmcnt(0)
	s_setprio 1
	s_waitcnt lgkmcnt(0)
	v_mfma_f32_16x16x32_f16 v[36:39], v[222:225], v[190:193], v[134:137]
	v_mfma_f32_16x16x32_f16 v[134:137], v[222:225], v[198:201], v[138:141]
	v_mfma_f32_16x16x32_f16 v[66:69], v[222:225], v[206:209], v[66:69]
	v_mfma_f32_16x16x32_f16 v[70:73], v[230:233], v[206:209], v[70:73]
	v_mfma_f32_16x16x32_f16 v[74:77], v[222:225], v[214:217], v[74:77]
	v_mfma_f32_16x16x32_f16 v[78:81], v[230:233], v[214:217], v[78:81]
	v_mfma_f32_16x16x32_f16 v[58:61], v[230:233], v[190:193], v[58:61]
	v_mfma_f32_16x16x32_f16 v[134:137], v[226:229], v[202:205], v[134:137]
	v_mfma_f32_16x16x32_f16 v[62:65], v[230:233], v[198:201], v[62:65]
	v_mfma_f32_16x16x32_f16 v[66:69], v[226:229], v[210:213], v[66:69]
	v_mfma_f32_16x16x32_f16 v[70:73], v[234:237], v[210:213], v[70:73]
	v_mfma_f32_16x16x32_f16 v[74:77], v[226:229], v[218:221], v[74:77]
	v_mfma_f32_16x16x32_f16 v[78:81], v[234:237], v[218:221], v[78:81]
	v_mfma_f32_16x16x32_f16 v[36:39], v[226:229], v[194:197], v[36:39]
	v_mfma_f32_16x16x32_f16 v[58:61], v[234:237], v[194:197], v[58:61]
	v_mfma_f32_16x16x32_f16 v[62:65], v[234:237], v[202:205], v[62:65]
	s_setprio 0
	v_readfirstlane_b32 s15, v35
	v_lshl_add_u64 v[40:41], v[26:27], 0, s[0:1]
	s_mov_b32 m0, s15
	v_readfirstlane_b32 s15, v42
	s_barrier
	ds_read_b128 v[138:141], v1 offset:16384
	ds_read_b128 v[190:193], v1 offset:17408
	ds_read_b128 v[194:197], v1 offset:18432
	ds_read_b128 v[198:201], v1 offset:19456
	ds_read_b128 v[202:205], v1 offset:20480
	ds_read_b128 v[206:209], v1 offset:21504
	ds_read_b128 v[210:213], v1 offset:22528
	ds_read_b128 v[214:217], v1 offset:23552
	global_load_lds_dwordx4 v[40:41], off
	v_lshl_add_u64 v[40:41], v[28:29], 0, s[0:1]
	s_mov_b32 m0, s15
	s_nop 0
	global_load_lds_dwordx4 v[40:41], off
	s_barrier
	s_waitcnt lgkmcnt(0)
	s_setprio 1
	s_waitcnt lgkmcnt(0)
	v_mfma_f32_16x16x32_f16 v[126:129], v[154:157], v[210:213], v[126:129]
	v_mfma_f32_16x16x32_f16 v[46:49], v[154:157], v[138:141], v[46:49]
	v_mfma_f32_16x16x32_f16 v[170:173], v[162:165], v[138:141], v[170:173]
	v_mfma_f32_16x16x32_f16 v[174:177], v[154:157], v[194:197], v[174:177]
	v_mfma_f32_16x16x32_f16 v[178:181], v[162:165], v[194:197], v[178:181]
	v_mfma_f32_16x16x32_f16 v[182:185], v[154:157], v[202:205], v[182:185]
	v_mfma_f32_16x16x32_f16 v[186:189], v[162:165], v[202:205], v[186:189]
	v_mfma_f32_16x16x32_f16 v[126:129], v[158:161], v[214:217], v[126:129]
	v_mfma_f32_16x16x32_f16 v[50:53], v[162:165], v[210:213], v[50:53]
	v_mfma_f32_16x16x32_f16 v[46:49], v[158:161], v[190:193], v[46:49]
	v_mfma_f32_16x16x32_f16 v[170:173], v[166:169], v[190:193], v[170:173]
	v_mfma_f32_16x16x32_f16 v[174:177], v[158:161], v[198:201], v[174:177]
	v_mfma_f32_16x16x32_f16 v[178:181], v[166:169], v[198:201], v[178:181]
	v_mfma_f32_16x16x32_f16 v[182:185], v[158:161], v[206:209], v[182:185]
	v_mfma_f32_16x16x32_f16 v[186:189], v[166:169], v[206:209], v[186:189]
	v_mfma_f32_16x16x32_f16 v[50:53], v[166:169], v[214:217], v[50:53]
	s_setprio 0
	s_barrier
	v_readfirstlane_b32 s15, v34
	v_lshl_add_u64 v[40:41], v[22:23], 0, s[0:1]
	s_mov_b32 m0, s15
	v_readfirstlane_b32 s15, v43
	global_load_lds_dwordx4 v[40:41], off
	v_lshl_add_u64 v[34:35], v[24:25], 0, s[0:1]
	s_mov_b32 m0, s15
	s_nop 0
	global_load_lds_dwordx4 v[34:35], off
	s_waitcnt vmcnt(6)
	s_barrier
	s_setprio 1
	v_mfma_f32_16x16x32_f16 v[40:43], v[222:225], v[138:141], v[54:57]
	v_mfma_f32_16x16x32_f16 v[54:57], v[230:233], v[138:141], v[82:85]
	v_mfma_f32_16x16x32_f16 v[82:85], v[222:225], v[194:197], v[130:133]
	v_mfma_f32_16x16x32_f16 v[130:133], v[230:233], v[194:197], v[142:145]
	v_mfma_f32_16x16x32_f16 v[138:141], v[222:225], v[202:205], v[146:149]
	v_mfma_f32_16x16x32_f16 v[142:145], v[230:233], v[202:205], v[150:153]
	v_mfma_f32_16x16x32_f16 v[118:121], v[222:225], v[210:213], v[118:121]
	v_mfma_f32_16x16x32_f16 v[122:125], v[230:233], v[210:213], v[122:125]
	v_mfma_f32_16x16x32_f16 v[82:85], v[226:229], v[198:201], v[82:85]
	v_mfma_f32_16x16x32_f16 v[130:133], v[234:237], v[198:201], v[130:133]
	v_mfma_f32_16x16x32_f16 v[138:141], v[226:229], v[206:209], v[138:141]
	v_mfma_f32_16x16x32_f16 v[142:145], v[234:237], v[206:209], v[142:145]
	v_mfma_f32_16x16x32_f16 v[118:121], v[226:229], v[214:217], v[118:121]
	v_mfma_f32_16x16x32_f16 v[122:125], v[234:237], v[214:217], v[122:125]
	v_mfma_f32_16x16x32_f16 v[40:43], v[226:229], v[190:193], v[40:43]
	v_mfma_f32_16x16x32_f16 v[54:57], v[234:237], v[190:193], v[54:57]
	s_setprio 0
	s_barrier
	ds_read_b128 v[146:149], v10
	ds_read_b128 v[150:153], v11
	ds_read_b128 v[154:157], v12
	ds_read_b128 v[158:161], v13
	v_readfirstlane_b32 s15, v44
	v_lshl_add_u64 v[34:35], v[18:19], 0, s[0:1]
	s_mov_b32 m0, s15
	ds_read_b128 v[162:165], v1 offset:32768
	ds_read_b128 v[166:169], v1 offset:33792
	ds_read_b128 v[190:193], v1 offset:34816
	ds_read_b128 v[194:197], v1 offset:35840
	ds_read_b128 v[198:201], v1 offset:36864
	ds_read_b128 v[202:205], v1 offset:37888
	ds_read_b128 v[206:209], v1 offset:38912
	ds_read_b128 v[210:213], v1 offset:39936
	global_load_lds_dwordx4 v[34:35], off
	v_lshl_add_u64 v[34:35], v[20:21], 0, s[0:1]
	v_readfirstlane_b32 s0, v45
	s_mov_b32 m0, s0
	s_nop 0
	global_load_lds_dwordx4 v[34:35], off
	s_waitcnt lgkmcnt(8)
	s_barrier
	s_waitcnt lgkmcnt(0)
	s_setprio 1
	s_waitcnt lgkmcnt(0)
	v_mfma_f32_16x16x32_f16 v[86:89], v[146:149], v[162:165], v[86:89]
	v_mfma_f32_16x16x32_f16 v[90:93], v[154:157], v[162:165], v[90:93]
	v_mfma_f32_16x16x32_f16 v[94:97], v[146:149], v[190:193], v[94:97]
	v_mfma_f32_16x16x32_f16 v[98:101], v[154:157], v[190:193], v[98:101]
	v_mfma_f32_16x16x32_f16 v[102:105], v[146:149], v[198:201], v[102:105]
	v_mfma_f32_16x16x32_f16 v[106:109], v[154:157], v[198:201], v[106:109]
	v_mfma_f32_16x16x32_f16 v[110:113], v[146:149], v[206:209], v[110:113]
	v_mfma_f32_16x16x32_f16 v[114:117], v[154:157], v[206:209], v[114:117]
	v_mfma_f32_16x16x32_f16 v[86:89], v[150:153], v[166:169], v[86:89]
	v_mfma_f32_16x16x32_f16 v[90:93], v[158:161], v[166:169], v[90:93]
	v_mfma_f32_16x16x32_f16 v[94:97], v[150:153], v[194:197], v[94:97]
	v_mfma_f32_16x16x32_f16 v[98:101], v[158:161], v[194:197], v[98:101]
	v_mfma_f32_16x16x32_f16 v[102:105], v[150:153], v[202:205], v[102:105]
	v_mfma_f32_16x16x32_f16 v[106:109], v[158:161], v[202:205], v[106:109]
	v_mfma_f32_16x16x32_f16 v[110:113], v[150:153], v[210:213], v[110:113]
	v_mfma_f32_16x16x32_f16 v[114:117], v[158:161], v[210:213], v[114:117]
	s_setprio 0
	s_barrier
	s_mov_b64 s[0:1], 0x380
	s_mov_b32 m0, s10
	v_lshl_add_u64 v[30:31], v[30:31], 0, s[0:1]
	ds_read_b128 v[214:217], v14
	ds_read_b128 v[218:221], v15
	ds_read_b128 v[222:225], v16
	ds_read_b128 v[226:229], v17
	global_load_lds_dwordx4 v[30:31], off
	v_lshl_add_u64 v[30:31], v[32:33], 0, s[0:1]
	s_mov_b32 m0, s2
	s_nop 0
	global_load_lds_dwordx4 v[30:31], off
	s_barrier
	s_waitcnt lgkmcnt(0)
	s_setprio 1
	s_waitcnt lgkmcnt(0)
	v_mfma_f32_16x16x32_f16 v[30:33], v[214:217], v[162:165], v[36:39]
	v_mfma_f32_16x16x32_f16 v[66:69], v[214:217], v[198:201], v[66:69]
	v_mfma_f32_16x16x32_f16 v[70:73], v[222:225], v[198:201], v[70:73]
	v_mfma_f32_16x16x32_f16 v[74:77], v[214:217], v[206:209], v[74:77]
	v_mfma_f32_16x16x32_f16 v[78:81], v[222:225], v[206:209], v[78:81]
	v_mfma_f32_16x16x32_f16 v[30:33], v[218:221], v[166:169], v[30:33]
	v_mfma_f32_16x16x32_f16 v[34:37], v[222:225], v[162:165], v[58:61]
	v_mfma_f32_16x16x32_f16 v[58:61], v[214:217], v[190:193], v[134:137]
	v_mfma_f32_16x16x32_f16 v[62:65], v[222:225], v[190:193], v[62:65]
	v_mfma_f32_16x16x32_f16 v[66:69], v[218:221], v[202:205], v[66:69]
	v_mfma_f32_16x16x32_f16 v[70:73], v[226:229], v[202:205], v[70:73]
	v_mfma_f32_16x16x32_f16 v[74:77], v[218:221], v[210:213], v[74:77]
	v_mfma_f32_16x16x32_f16 v[78:81], v[226:229], v[210:213], v[78:81]
	v_mfma_f32_16x16x32_f16 v[34:37], v[226:229], v[166:169], v[34:37]
	v_mfma_f32_16x16x32_f16 v[58:61], v[218:221], v[194:197], v[58:61]
	v_mfma_f32_16x16x32_f16 v[62:65], v[226:229], v[194:197], v[62:65]
	s_setprio 0
	s_mov_b32 m0, s11
	v_lshl_add_u64 v[26:27], v[26:27], 0, s[0:1]
	s_barrier
	ds_read_b128 v[134:137], v1 offset:49152
	ds_read_b128 v[162:165], v1 offset:50176
	ds_read_b128 v[166:169], v1 offset:51200
	ds_read_b128 v[190:193], v1 offset:52224
	ds_read_b128 v[194:197], v1 offset:53248
	ds_read_b128 v[198:201], v1 offset:54272
	ds_read_b128 v[202:205], v1 offset:55296
	ds_read_b128 v[206:209], v1 offset:56320
	global_load_lds_dwordx4 v[26:27], off
	v_lshl_add_u64 v[26:27], v[28:29], 0, s[0:1]
	s_mov_b32 m0, s3
	s_nop 0
	global_load_lds_dwordx4 v[26:27], off
	s_barrier
	s_waitcnt lgkmcnt(0)
	s_setprio 1
	s_waitcnt lgkmcnt(0)
	v_mfma_f32_16x16x32_f16 v[26:29], v[146:149], v[134:137], v[46:49]
	v_mfma_f32_16x16x32_f16 v[126:129], v[146:149], v[202:205], v[126:129]
	v_mfma_f32_16x16x32_f16 v[26:29], v[150:153], v[162:165], v[26:29]
	v_mfma_f32_16x16x32_f16 v[44:47], v[154:157], v[134:137], v[170:173]
	v_mfma_f32_16x16x32_f16 v[170:173], v[146:149], v[166:169], v[174:177]
	v_mfma_f32_16x16x32_f16 v[174:177], v[154:157], v[166:169], v[178:181]
	v_mfma_f32_16x16x32_f16 v[178:181], v[146:149], v[194:197], v[182:185]
	v_mfma_f32_16x16x32_f16 v[182:185], v[154:157], v[194:197], v[186:189]
	v_mfma_f32_16x16x32_f16 v[126:129], v[150:153], v[206:209], v[126:129]
	v_mfma_f32_16x16x32_f16 v[48:51], v[154:157], v[202:205], v[50:53]
	v_mfma_f32_16x16x32_f16 v[44:47], v[158:161], v[162:165], v[44:47]
	v_mfma_f32_16x16x32_f16 v[170:173], v[150:153], v[190:193], v[170:173]
	v_mfma_f32_16x16x32_f16 v[174:177], v[158:161], v[190:193], v[174:177]
	v_mfma_f32_16x16x32_f16 v[178:181], v[150:153], v[198:201], v[178:181]
	v_mfma_f32_16x16x32_f16 v[182:185], v[158:161], v[198:201], v[182:185]
	v_mfma_f32_16x16x32_f16 v[48:51], v[158:161], v[206:209], v[48:51]
	s_setprio 0
	s_barrier
	s_mov_b32 m0, s5
	v_lshl_add_u64 v[22:23], v[22:23], 0, s[0:1]
	global_load_lds_dwordx4 v[22:23], off
	v_lshl_add_u64 v[22:23], v[24:25], 0, s[0:1]
	s_mov_b32 m0, s4
	s_nop 0
	global_load_lds_dwordx4 v[22:23], off
	s_waitcnt vmcnt(6)
	s_barrier
	s_setprio 1
	v_mfma_f32_16x16x32_f16 v[22:25], v[214:217], v[134:137], v[40:43]
	v_mfma_f32_16x16x32_f16 v[38:41], v[222:225], v[134:137], v[54:57]
	v_mfma_f32_16x16x32_f16 v[52:55], v[214:217], v[166:169], v[82:85]
	v_mfma_f32_16x16x32_f16 v[82:85], v[222:225], v[166:169], v[130:133]
	v_mfma_f32_16x16x32_f16 v[130:133], v[214:217], v[194:197], v[138:141]
	v_mfma_f32_16x16x32_f16 v[134:137], v[222:225], v[194:197], v[142:145]
	v_mfma_f32_16x16x32_f16 v[118:121], v[214:217], v[202:205], v[118:121]
	v_mfma_f32_16x16x32_f16 v[122:125], v[222:225], v[202:205], v[122:125]
	v_mfma_f32_16x16x32_f16 v[22:25], v[218:221], v[162:165], v[22:25]
	v_mfma_f32_16x16x32_f16 v[82:85], v[226:229], v[190:193], v[82:85]
	v_mfma_f32_16x16x32_f16 v[130:133], v[218:221], v[198:201], v[130:133]
	v_mfma_f32_16x16x32_f16 v[134:137], v[226:229], v[198:201], v[134:137]
	v_mfma_f32_16x16x32_f16 v[118:121], v[218:221], v[206:209], v[118:121]
	v_mfma_f32_16x16x32_f16 v[122:125], v[226:229], v[206:209], v[122:125]
	v_mfma_f32_16x16x32_f16 v[38:41], v[226:229], v[162:165], v[38:41]
	v_mfma_f32_16x16x32_f16 v[52:55], v[218:221], v[190:193], v[52:55]
	s_setprio 0
	s_mov_b32 m0, s14
	v_lshl_add_u64 v[18:19], v[18:19], 0, s[0:1]
	s_barrier
	ds_read_b128 v[138:141], v2
	ds_read_b128 v[142:145], v3
	ds_read_b128 v[146:149], v4
	ds_read_b128 v[2:5], v5
	global_load_lds_dwordx4 v[18:19], off
	v_lshl_add_u64 v[18:19], v[20:21], 0, s[0:1]
	s_mov_b32 m0, s7
	s_nop 0
	global_load_lds_dwordx4 v[18:19], off
	ds_read_b128 v[18:21], v1
	ds_read_b128 v[150:153], v1 offset:1024
	ds_read_b128 v[154:157], v1 offset:2048
	ds_read_b128 v[158:161], v1 offset:3072
	ds_read_b128 v[162:165], v1 offset:4096
	ds_read_b128 v[166:169], v1 offset:5120
	ds_read_b128 v[186:189], v1 offset:6144
	ds_read_b128 v[190:193], v1 offset:7168
	s_barrier
	s_waitcnt lgkmcnt(0)
	s_setprio 1
	s_waitcnt lgkmcnt(0)
	v_mfma_f32_16x16x32_f16 v[86:89], v[138:141], v[18:21], v[86:89]
	v_mfma_f32_16x16x32_f16 v[90:93], v[146:149], v[18:21], v[90:93]
	v_mfma_f32_16x16x32_f16 v[94:97], v[138:141], v[154:157], v[94:97]
	v_mfma_f32_16x16x32_f16 v[98:101], v[146:149], v[154:157], v[98:101]
	v_mfma_f32_16x16x32_f16 v[102:105], v[138:141], v[162:165], v[102:105]
	v_mfma_f32_16x16x32_f16 v[106:109], v[146:149], v[162:165], v[106:109]
	v_mfma_f32_16x16x32_f16 v[110:113], v[138:141], v[186:189], v[110:113]
	v_mfma_f32_16x16x32_f16 v[86:89], v[142:145], v[150:153], v[86:89]
	v_mfma_f32_16x16x32_f16 v[90:93], v[2:5], v[150:153], v[90:93]
	v_mfma_f32_16x16x32_f16 v[94:97], v[142:145], v[158:161], v[94:97]
	v_mfma_f32_16x16x32_f16 v[98:101], v[2:5], v[158:161], v[98:101]
	v_mfma_f32_16x16x32_f16 v[102:105], v[142:145], v[166:169], v[102:105]
	v_mfma_f32_16x16x32_f16 v[106:109], v[2:5], v[166:169], v[106:109]
	v_mfma_f32_16x16x32_f16 v[110:113], v[142:145], v[190:193], v[110:113]
	v_mfma_f32_16x16x32_f16 v[114:117], v[146:149], v[186:189], v[114:117]
	v_mfma_f32_16x16x32_f16 v[194:197], v[2:5], v[190:193], v[114:117]
	s_setprio 0
	s_barrier
	s_nop 4
	ds_read_b128 v[114:117], v6
	ds_read_b128 v[198:201], v7
	ds_read_b128 v[202:205], v8
	ds_read_b128 v[6:9], v9
	s_barrier
	s_waitcnt lgkmcnt(0)
	s_setprio 1
	s_waitcnt lgkmcnt(0)
	v_mfma_f32_16x16x32_f16 v[30:33], v[114:117], v[18:21], v[30:33]
	v_mfma_f32_16x16x32_f16 v[18:21], v[202:205], v[18:21], v[34:37]
	v_mfma_f32_16x16x32_f16 v[34:37], v[114:117], v[154:157], v[58:61]
	v_mfma_f32_16x16x32_f16 v[56:59], v[202:205], v[154:157], v[62:65]
	v_mfma_f32_16x16x32_f16 v[60:63], v[114:117], v[162:165], v[66:69]
	v_mfma_f32_16x16x32_f16 v[64:67], v[202:205], v[162:165], v[70:73]
	v_mfma_f32_16x16x32_f16 v[68:71], v[114:117], v[186:189], v[74:77]
	v_mfma_f32_16x16x32_f16 v[72:75], v[202:205], v[186:189], v[78:81]
	v_mfma_f32_16x16x32_f16 v[30:33], v[198:201], v[150:153], v[30:33]
	v_mfma_f32_16x16x32_f16 v[18:21], v[6:9], v[150:153], v[18:21]
	v_mfma_f32_16x16x32_f16 v[64:67], v[6:9], v[166:169], v[64:67]
	v_mfma_f32_16x16x32_f16 v[68:71], v[198:201], v[190:193], v[68:71]
	v_mfma_f32_16x16x32_f16 v[72:75], v[6:9], v[190:193], v[72:75]
	v_mfma_f32_16x16x32_f16 v[34:37], v[198:201], v[158:161], v[34:37]
	v_mfma_f32_16x16x32_f16 v[56:59], v[6:9], v[158:161], v[56:59]
	v_mfma_f32_16x16x32_f16 v[60:63], v[198:201], v[166:169], v[60:63]
	s_setprio 0
	s_barrier
	ds_read_b128 v[76:79], v1 offset:16384
	ds_read_b128 v[150:153], v1 offset:17408
	ds_read_b128 v[154:157], v1 offset:18432
	ds_read_b128 v[158:161], v1 offset:19456
	ds_read_b128 v[162:165], v1 offset:20480
	ds_read_b128 v[166:169], v1 offset:21504
	ds_read_b128 v[186:189], v1 offset:22528
	ds_read_b128 v[190:193], v1 offset:23552
	s_waitcnt vmcnt(4)
	s_barrier
	s_waitcnt lgkmcnt(0)
	s_setprio 1
	s_waitcnt lgkmcnt(0)
	v_mfma_f32_16x16x32_f16 v[26:29], v[138:141], v[76:79], v[26:29]
	v_mfma_f32_16x16x32_f16 v[42:45], v[146:149], v[76:79], v[44:47]
	v_mfma_f32_16x16x32_f16 v[174:177], v[146:149], v[154:157], v[174:177]
	v_mfma_f32_16x16x32_f16 v[182:185], v[146:149], v[162:165], v[182:185]
	v_mfma_f32_16x16x32_f16 v[46:49], v[146:149], v[186:189], v[48:51]
	v_mfma_f32_16x16x32_f16 v[26:29], v[142:145], v[150:153], v[26:29]
	v_mfma_f32_16x16x32_f16 v[42:45], v[2:5], v[150:153], v[42:45]
	v_mfma_f32_16x16x32_f16 v[170:173], v[138:141], v[154:157], v[170:173]
	v_mfma_f32_16x16x32_f16 v[174:177], v[2:5], v[158:161], v[174:177]
	v_mfma_f32_16x16x32_f16 v[178:181], v[138:141], v[162:165], v[178:181]
	v_mfma_f32_16x16x32_f16 v[182:185], v[2:5], v[166:169], v[182:185]
	v_mfma_f32_16x16x32_f16 v[126:129], v[138:141], v[186:189], v[126:129]
	v_mfma_f32_16x16x32_f16 v[2:5], v[2:5], v[190:193], v[46:49]
	v_mfma_f32_16x16x32_f16 v[170:173], v[142:145], v[158:161], v[170:173]
	v_mfma_f32_16x16x32_f16 v[178:181], v[142:145], v[166:169], v[178:181]
	v_mfma_f32_16x16x32_f16 v[206:209], v[142:145], v[190:193], v[126:129]
	s_setprio 0
	s_setprio 1
	v_mfma_f32_16x16x32_f16 v[22:25], v[114:117], v[76:79], v[22:25]
	v_mfma_f32_16x16x32_f16 v[46:49], v[198:201], v[150:153], v[22:25]
	v_mfma_f32_16x16x32_f16 v[22:25], v[202:205], v[76:79], v[38:41]
	v_mfma_f32_16x16x32_f16 v[38:41], v[6:9], v[150:153], v[22:25]
	v_mfma_f32_16x16x32_f16 v[22:25], v[114:117], v[154:157], v[52:55]
	v_mfma_f32_16x16x32_f16 v[50:53], v[198:201], v[158:161], v[22:25]
	v_mfma_f32_16x16x32_f16 v[22:25], v[202:205], v[154:157], v[82:85]
	v_mfma_f32_16x16x32_f16 v[146:149], v[6:9], v[158:161], v[22:25]
	v_mfma_f32_16x16x32_f16 v[22:25], v[114:117], v[162:165], v[130:133]
	v_mfma_f32_16x16x32_f16 v[210:213], v[198:201], v[166:169], v[22:25]
	v_mfma_f32_16x16x32_f16 v[22:25], v[202:205], v[162:165], v[134:137]
	v_mfma_f32_16x16x32_f16 v[166:169], v[6:9], v[166:169], v[22:25]
	v_mfma_f32_16x16x32_f16 v[22:25], v[114:117], v[186:189], v[118:121]
	v_mfma_f32_16x16x32_f16 v[198:201], v[198:201], v[190:193], v[22:25]
	v_mfma_f32_16x16x32_f16 v[22:25], v[202:205], v[186:189], v[122:125]
	v_mfma_f32_16x16x32_f16 v[186:189], v[6:9], v[190:193], v[22:25]
	s_setprio 0
	s_barrier
	ds_read_b128 v[6:9], v10
	ds_read_b128 v[76:79], v11
	ds_read_b128 v[190:193], v12
	ds_read_b128 v[10:13], v13
	s_nop 0
	ds_read_b128 v[22:25], v1 offset:32768
	ds_read_b128 v[122:125], v1 offset:33792
	ds_read_b128 v[126:129], v1 offset:34816
	ds_read_b128 v[138:141], v1 offset:35840
	ds_read_b128 v[202:205], v1 offset:36864
	ds_read_b128 v[214:217], v1 offset:37888
	ds_read_b128 v[218:221], v1 offset:38912
	ds_read_b128 v[222:225], v1 offset:39936
	s_waitcnt vmcnt(2)
	s_barrier
	s_waitcnt lgkmcnt(0)
	s_setprio 1
	s_waitcnt lgkmcnt(0)
	v_mfma_f32_16x16x32_f16 v[80:83], v[6:9], v[22:25], v[86:89]
	v_mfma_f32_16x16x32_f16 v[162:165], v[76:79], v[122:125], v[80:83]
	v_mfma_f32_16x16x32_f16 v[80:83], v[190:193], v[22:25], v[90:93]
	v_mfma_f32_16x16x32_f16 v[154:157], v[10:13], v[122:125], v[80:83]
	v_mfma_f32_16x16x32_f16 v[80:83], v[6:9], v[126:129], v[94:97]
	v_mfma_f32_16x16x32_f16 v[134:137], v[76:79], v[138:141], v[80:83]
	v_mfma_f32_16x16x32_f16 v[80:83], v[190:193], v[126:129], v[98:101]
	v_mfma_f32_16x16x32_f16 v[130:133], v[10:13], v[138:141], v[80:83]
	v_mfma_f32_16x16x32_f16 v[80:83], v[6:9], v[202:205], v[102:105]
	v_mfma_f32_16x16x32_f16 v[118:121], v[76:79], v[214:217], v[80:83]
	v_mfma_f32_16x16x32_f16 v[80:83], v[190:193], v[202:205], v[106:109]
	v_mfma_f32_16x16x32_f16 v[114:117], v[10:13], v[214:217], v[80:83]
	v_mfma_f32_16x16x32_f16 v[80:83], v[6:9], v[218:221], v[110:113]
	v_mfma_f32_16x16x32_f16 v[86:89], v[76:79], v[222:225], v[80:83]
	v_mfma_f32_16x16x32_f16 v[80:83], v[190:193], v[218:221], v[194:197]
	v_mfma_f32_16x16x32_f16 v[82:85], v[10:13], v[222:225], v[80:83]
	s_setprio 0
	s_barrier
	ds_read_b128 v[194:197], v14
	ds_read_b128 v[226:229], v15
	ds_read_b128 v[230:233], v16
	ds_read_b128 v[234:237], v17
	s_waitcnt vmcnt(0)
	s_barrier
	s_waitcnt lgkmcnt(0)
	s_setprio 1
	s_waitcnt lgkmcnt(0)
	v_mfma_f32_16x16x32_f16 v[14:17], v[194:197], v[22:25], v[30:33]
	v_mfma_f32_16x16x32_f16 v[158:161], v[226:229], v[122:125], v[14:17]
	v_mfma_f32_16x16x32_f16 v[14:17], v[230:233], v[22:25], v[18:21]
	v_mfma_f32_16x16x32_f16 v[150:153], v[234:237], v[122:125], v[14:17]
	v_mfma_f32_16x16x32_f16 v[14:17], v[194:197], v[126:129], v[34:37]
	v_mfma_f32_16x16x32_f16 v[142:145], v[226:229], v[138:141], v[14:17]
	v_mfma_f32_16x16x32_f16 v[14:17], v[230:233], v[126:129], v[56:59]
	v_mfma_f32_16x16x32_f16 v[138:141], v[234:237], v[138:141], v[14:17]
	v_mfma_f32_16x16x32_f16 v[14:17], v[194:197], v[202:205], v[60:63]
	v_mfma_f32_16x16x32_f16 v[126:129], v[226:229], v[214:217], v[14:17]
	v_mfma_f32_16x16x32_f16 v[14:17], v[230:233], v[202:205], v[64:67]
	v_mfma_f32_16x16x32_f16 v[122:125], v[234:237], v[214:217], v[14:17]
	v_mfma_f32_16x16x32_f16 v[14:17], v[194:197], v[218:221], v[68:71]
	v_mfma_f32_16x16x32_f16 v[98:101], v[226:229], v[222:225], v[14:17]
	v_mfma_f32_16x16x32_f16 v[14:17], v[230:233], v[218:221], v[72:75]
	v_mfma_f32_16x16x32_f16 v[90:93], v[234:237], v[222:225], v[14:17]
	s_setprio 0
	s_barrier
	ds_read_b128 v[30:33], v1 offset:49152
	ds_read_b128 v[34:37], v1 offset:50176
	ds_read_b128 v[54:57], v1 offset:51200
	ds_read_b128 v[58:61], v1 offset:52224
	ds_read_b128 v[62:65], v1 offset:53248
	ds_read_b128 v[202:205], v1 offset:54272
	ds_read_b128 v[214:217], v1 offset:55296
	ds_read_b128 v[218:221], v1 offset:56320
	s_barrier
	s_waitcnt lgkmcnt(0)
	s_setprio 1
	s_waitcnt lgkmcnt(0)
	v_mfma_f32_16x16x32_f16 v[14:17], v[6:9], v[30:33], v[26:29]
	v_mfma_f32_16x16x32_f16 v[102:105], v[76:79], v[34:37], v[14:17]
	v_mfma_f32_16x16x32_f16 v[14:17], v[190:193], v[30:33], v[42:45]
	v_mfma_f32_16x16x32_f16 v[94:97], v[10:13], v[34:37], v[14:17]
	v_mfma_f32_16x16x32_f16 v[14:17], v[6:9], v[54:57], v[170:173]
	v_mfma_f32_16x16x32_f16 v[70:73], v[76:79], v[58:61], v[14:17]
	v_mfma_f32_16x16x32_f16 v[14:17], v[190:193], v[54:57], v[174:177]
	v_mfma_f32_16x16x32_f16 v[66:69], v[10:13], v[58:61], v[14:17]
	v_mfma_f32_16x16x32_f16 v[14:17], v[6:9], v[62:65], v[178:181]
	v_mfma_f32_16x16x32_f16 v[22:25], v[76:79], v[202:205], v[14:17]
	v_mfma_f32_16x16x32_f16 v[14:17], v[190:193], v[62:65], v[182:185]
	v_mfma_f32_16x16x32_f16 v[6:9], v[6:9], v[214:217], v[206:209]
	v_mfma_f32_16x16x32_f16 v[2:5], v[190:193], v[214:217], v[2:5]
	v_mfma_f32_16x16x32_f16 v[18:21], v[10:13], v[202:205], v[14:17]
	v_mfma_f32_16x16x32_f16 v[14:17], v[76:79], v[218:221], v[6:9]
	v_mfma_f32_16x16x32_f16 v[6:9], v[10:13], v[218:221], v[2:5]
	s_setprio 0
	s_setprio 1
	v_mfma_f32_16x16x32_f16 v[2:5], v[194:197], v[30:33], v[46:49]
	v_mfma_f32_16x16x32_f16 v[110:113], v[226:229], v[34:37], v[2:5]
	v_mfma_f32_16x16x32_f16 v[2:5], v[230:233], v[30:33], v[38:41]
	v_mfma_f32_16x16x32_f16 v[106:109], v[234:237], v[34:37], v[2:5]
	v_mfma_f32_16x16x32_f16 v[2:5], v[194:197], v[54:57], v[50:53]
	v_mfma_f32_16x16x32_f16 v[78:81], v[226:229], v[58:61], v[2:5]
	v_mfma_f32_16x16x32_f16 v[2:5], v[230:233], v[54:57], v[146:149]
	v_mfma_f32_16x16x32_f16 v[74:77], v[234:237], v[58:61], v[2:5]
	v_mfma_f32_16x16x32_f16 v[2:5], v[194:197], v[62:65], v[210:213]
	v_mfma_f32_16x16x32_f16 v[30:33], v[226:229], v[202:205], v[2:5]
	v_mfma_f32_16x16x32_f16 v[2:5], v[230:233], v[62:65], v[166:169]
	v_mfma_f32_16x16x32_f16 v[26:29], v[234:237], v[202:205], v[2:5]
	v_mfma_f32_16x16x32_f16 v[2:5], v[194:197], v[214:217], v[198:201]
	v_mfma_f32_16x16x32_f16 v[10:13], v[226:229], v[218:221], v[2:5]
	v_mfma_f32_16x16x32_f16 v[2:5], v[230:233], v[214:217], v[186:189]
	v_mfma_f32_16x16x32_f16 v[2:5], v[234:237], v[218:221], v[2:5]
	s_setprio 0
	s_barrier
	s_add_i32 s0, 0, 0x20800
	v_bfe_u32 v166, v0, 4, 2
	v_bfe_u32 v1, v0, 6, 2
	v_lshlrev_b32_e32 v34, 5, v166
	v_lshl_or_b32 v34, v1, 7, v34
	v_add_u32_e32 v35, s0, v34
	s_add_i32 s1, 0, 0x20c00
	v_add_u32_e32 v36, s1, v34
	ds_read_b128 v[58:61], v35
	ds_read_b128 v[62:65], v36
	v_or_b32_e32 v35, 16, v34
	v_add_u32_e32 v36, s0, v35
	v_add_u32_e32 v35, s1, v35
	ds_read_b128 v[50:53], v36
	ds_read_b128 v[54:57], v35
	v_or_b32_e32 v35, 0x200, v34
	v_add_u32_e32 v36, s0, v35
	v_add_u32_e32 v35, s1, v35
	v_or_b32_e32 v34, 0x210, v34
	ds_read_b128 v[42:45], v36
	ds_read_b128 v[46:49], v35
	v_add_u32_e32 v35, s0, v34
	v_and_b32_e32 v146, 15, v0
	v_ashrrev_i32_e32 v0, 2, v0
	s_movk_i32 s0, 0xffc0
	v_and_or_b32 v168, v0, s0, v146
	s_add_i32 s0, 0, 0x20000
	v_add_u32_e32 v38, s1, v34
	v_lshl_add_u32 v169, v168, 3, s0
	ds_read_b128 v[34:37], v35
	ds_read_b128 v[38:41], v38
	s_waitcnt vmcnt(0)
	ds_read2st64_b64 v[146:149], v169 offset1:2
	v_lshlrev_b32_e32 v0, 5, v1
	v_lshlrev_b32_e32 v1, 3, v166
	v_or3_b32 v166, v0, v1, s13
	v_add_u32_e32 v167, s12, v168
	s_waitcnt lgkmcnt(0)
	v_pk_fma_f32 v[0:1], v[146:147], v[58:59], v[162:163] op_sel_hi:[0,1,1] neg_lo:[1,0,0] neg_hi:[1,0,0]
	v_pk_fma_f32 v[0:1], v[146:147], v[0:1], v[62:63] op_sel:[1,0,0]
	v_mul_lo_u32 v170, v167, s6
	v_cvt_pk_f16_f32 v162, v0, v1
	v_pk_fma_f32 v[0:1], v[146:147], v[60:61], v[164:165] op_sel_hi:[0,1,1] neg_lo:[1,0,0] neg_hi:[1,0,0]
	v_pk_fma_f32 v[0:1], v[146:147], v[0:1], v[64:65] op_sel:[1,0,0]
	s_and_b32 s9, s9, 0xffff
	v_cvt_pk_f16_f32 v163, v0, v1
	v_pk_fma_f32 v[0:1], v[146:147], v[50:51], v[154:155] op_sel_hi:[0,1,1] neg_lo:[1,0,0] neg_hi:[1,0,0]
	v_pk_fma_f32 v[0:1], v[146:147], v[0:1], v[54:55] op_sel:[1,0,0]
	s_mov_b32 s11, 0x20000
	v_cvt_pk_f16_f32 v164, v0, v1
	v_pk_fma_f32 v[0:1], v[146:147], v[52:53], v[156:157] op_sel_hi:[0,1,1] neg_lo:[1,0,0] neg_hi:[1,0,0]
	v_pk_fma_f32 v[0:1], v[146:147], v[0:1], v[56:57] op_sel:[1,0,0]
	s_mov_b32 s10, 0x7ffffff0
	v_cvt_pk_f16_f32 v165, v0, v1
	v_pk_fma_f32 v[0:1], v[146:147], v[42:43], v[158:159] op_sel_hi:[0,1,1] neg_lo:[1,0,0] neg_hi:[1,0,0]
	v_pk_fma_f32 v[0:1], v[146:147], v[0:1], v[46:47] op_sel:[1,0,0]
	v_add_lshl_u32 v170, v166, v170, 1
	v_cvt_pk_f16_f32 v154, v0, v1
	v_pk_fma_f32 v[0:1], v[146:147], v[44:45], v[160:161] op_sel_hi:[0,1,1] neg_lo:[1,0,0] neg_hi:[1,0,0]
	v_pk_fma_f32 v[0:1], v[146:147], v[0:1], v[48:49] op_sel:[1,0,0]
	buffer_store_dwordx4 v[162:165], v170, s[8:11], 0 offen sc1
	v_cvt_pk_f16_f32 v155, v0, v1
	v_pk_fma_f32 v[0:1], v[146:147], v[34:35], v[150:151] op_sel_hi:[0,1,1] neg_lo:[1,0,0] neg_hi:[1,0,0]
	v_pk_fma_f32 v[0:1], v[146:147], v[0:1], v[38:39] op_sel:[1,0,0]
	s_nop 0
	v_cvt_pk_f16_f32 v156, v0, v1
	v_pk_fma_f32 v[0:1], v[146:147], v[36:37], v[152:153] op_sel_hi:[0,1,1] neg_lo:[1,0,0] neg_hi:[1,0,0]
	v_pk_fma_f32 v[0:1], v[146:147], v[0:1], v[40:41] op_sel:[1,0,0]
	s_nop 0
	v_cvt_pk_f16_f32 v157, v0, v1
	v_or_b32_e32 v0, 16, v168
	v_add_u32_e32 v146, s12, v0
	v_lshl_add_u32 v0, v0, 3, s0
	ds_read_b64 v[0:1], v0
	buffer_store_dwordx4 v[154:157], v170, s[8:11], 0 offen offset:256 sc1
	s_waitcnt lgkmcnt(0)
	v_pk_fma_f32 v[134:135], v[0:1], v[58:59], v[134:135] op_sel_hi:[0,1,1] neg_lo:[1,0,0] neg_hi:[1,0,0]
	v_pk_fma_f32 v[136:137], v[0:1], v[60:61], v[136:137] op_sel_hi:[0,1,1] neg_lo:[1,0,0] neg_hi:[1,0,0]
	v_pk_fma_f32 v[130:131], v[0:1], v[50:51], v[130:131] op_sel_hi:[0,1,1] neg_lo:[1,0,0] neg_hi:[1,0,0]
	v_pk_fma_f32 v[134:135], v[0:1], v[134:135], v[62:63] op_sel:[1,0,0]
	v_pk_fma_f32 v[136:137], v[0:1], v[136:137], v[64:65] op_sel:[1,0,0]
	v_pk_fma_f32 v[130:131], v[0:1], v[130:131], v[54:55] op_sel:[1,0,0]
	v_cvt_pk_f16_f32 v134, v134, v135
	v_cvt_pk_f16_f32 v135, v136, v137
	v_cvt_pk_f16_f32 v136, v130, v131
	v_pk_fma_f32 v[130:131], v[0:1], v[52:53], v[132:133] op_sel_hi:[0,1,1] neg_lo:[1,0,0] neg_hi:[1,0,0]
	v_pk_fma_f32 v[130:131], v[0:1], v[130:131], v[56:57] op_sel:[1,0,0]
	v_mul_lo_u32 v154, v146, s6
	v_or_b32_e32 v155, 32, v168
	v_or_b32_e32 v156, 48, v168
	v_cvt_pk_f16_f32 v137, v130, v131
	v_pk_fma_f32 v[130:131], v[0:1], v[42:43], v[142:143] op_sel_hi:[0,1,1] neg_lo:[1,0,0] neg_hi:[1,0,0]
	v_pk_fma_f32 v[132:133], v[0:1], v[44:45], v[144:145] op_sel_hi:[0,1,1] neg_lo:[1,0,0] neg_hi:[1,0,0]
	v_lshl_add_u32 v146, v155, 3, s0
	v_lshl_add_u32 v147, v156, 3, s0
	v_add_lshl_u32 v154, v166, v154, 1
	v_pk_fma_f32 v[130:131], v[0:1], v[130:131], v[46:47] op_sel:[1,0,0]
	v_pk_fma_f32 v[132:133], v[0:1], v[132:133], v[48:49] op_sel:[1,0,0]
	ds_read_b64 v[150:151], v146
	ds_read_b64 v[146:147], v147
	ds_read_b64 v[152:153], v169 offset:1408
	buffer_store_dwordx4 v[134:137], v154, s[8:11], 0 offen sc1
	s_and_saveexec_b64 s[44:45], vcc
	s_cbranch_execz .LBB6_34
	s_barrier
.LBB6_34:
	s_or_b64 exec, exec, s[44:45]
	v_cvt_pk_f16_f32 v130, v130, v131
	v_cvt_pk_f16_f32 v131, v132, v133
	v_pk_fma_f32 v[132:133], v[0:1], v[34:35], v[138:139] op_sel_hi:[0,1,1] neg_lo:[1,0,0] neg_hi:[1,0,0]
	v_pk_fma_f32 v[134:135], v[0:1], v[36:37], v[140:141] op_sel_hi:[0,1,1] neg_lo:[1,0,0] neg_hi:[1,0,0]
	v_pk_fma_f32 v[132:133], v[0:1], v[132:133], v[38:39] op_sel:[1,0,0]
	v_pk_fma_f32 v[0:1], v[0:1], v[134:135], v[40:41] op_sel:[1,0,0]
	v_cvt_pk_f16_f32 v132, v132, v133
	v_cvt_pk_f16_f32 v133, v0, v1
	v_add_u32_e32 v0, s12, v155
	buffer_store_dwordx4 v[130:133], v154, s[8:11], 0 offen offset:256 sc1
	s_waitcnt lgkmcnt(0)
	v_pk_fma_f32 v[2:3], v[152:153], v[34:35], v[2:3] op_sel_hi:[0,1,1] neg_lo:[1,0,0] neg_hi:[1,0,0]
	v_pk_fma_f32 v[4:5], v[152:153], v[36:37], v[4:5] op_sel_hi:[0,1,1] neg_lo:[1,0,0] neg_hi:[1,0,0]
	v_mul_lo_u32 v130, v0, s6
	v_pk_fma_f32 v[0:1], v[150:151], v[58:59], v[118:119] op_sel_hi:[0,1,1] neg_lo:[1,0,0] neg_hi:[1,0,0]
	v_pk_fma_f32 v[0:1], v[150:151], v[0:1], v[62:63] op_sel:[1,0,0]
	v_add_lshl_u32 v130, v166, v130, 1
	v_cvt_pk_f16_f32 v118, v0, v1
	v_pk_fma_f32 v[0:1], v[150:151], v[60:61], v[120:121] op_sel_hi:[0,1,1] neg_lo:[1,0,0] neg_hi:[1,0,0]
	v_pk_fma_f32 v[0:1], v[150:151], v[0:1], v[64:65] op_sel:[1,0,0]
	v_pk_fma_f32 v[2:3], v[152:153], v[2:3], v[38:39] op_sel:[1,0,0]
	v_cvt_pk_f16_f32 v119, v0, v1
	v_pk_fma_f32 v[0:1], v[150:151], v[50:51], v[114:115] op_sel_hi:[0,1,1] neg_lo:[1,0,0] neg_hi:[1,0,0]
	v_pk_fma_f32 v[0:1], v[150:151], v[0:1], v[54:55] op_sel:[1,0,0]
	v_pk_fma_f32 v[4:5], v[152:153], v[4:5], v[40:41] op_sel:[1,0,0]
	v_cvt_pk_f16_f32 v120, v0, v1
	v_pk_fma_f32 v[0:1], v[150:151], v[52:53], v[116:117] op_sel_hi:[0,1,1] neg_lo:[1,0,0] neg_hi:[1,0,0]
	v_pk_fma_f32 v[0:1], v[150:151], v[0:1], v[56:57] op_sel:[1,0,0]
	v_cvt_pk_f16_f32 v2, v2, v3
	v_cvt_pk_f16_f32 v121, v0, v1
	v_pk_fma_f32 v[0:1], v[150:151], v[42:43], v[126:127] op_sel_hi:[0,1,1] neg_lo:[1,0,0] neg_hi:[1,0,0]
	v_pk_fma_f32 v[0:1], v[150:151], v[0:1], v[46:47] op_sel:[1,0,0]
	buffer_store_dwordx4 v[118:121], v130, s[8:11], 0 offen sc1
	v_cvt_pk_f16_f32 v114, v0, v1
	v_pk_fma_f32 v[0:1], v[150:151], v[44:45], v[128:129] op_sel_hi:[0,1,1] neg_lo:[1,0,0] neg_hi:[1,0,0]
	v_pk_fma_f32 v[0:1], v[150:151], v[0:1], v[48:49] op_sel:[1,0,0]
	v_cvt_pk_f16_f32 v3, v4, v5
	v_cvt_pk_f16_f32 v115, v0, v1
	v_pk_fma_f32 v[0:1], v[150:151], v[34:35], v[122:123] op_sel_hi:[0,1,1] neg_lo:[1,0,0] neg_hi:[1,0,0]
	v_pk_fma_f32 v[0:1], v[150:151], v[0:1], v[38:39] op_sel:[1,0,0]
	s_nop 0
	v_cvt_pk_f16_f32 v116, v0, v1
	v_pk_fma_f32 v[0:1], v[150:151], v[36:37], v[124:125] op_sel_hi:[0,1,1] neg_lo:[1,0,0] neg_hi:[1,0,0]
	v_pk_fma_f32 v[0:1], v[150:151], v[0:1], v[40:41] op_sel:[1,0,0]
	s_nop 0
	v_cvt_pk_f16_f32 v117, v0, v1
	v_add_u32_e32 v0, s12, v156
	buffer_store_dwordx4 v[114:117], v130, s[8:11], 0 offen offset:256 sc1
	s_nop 1
	v_mul_lo_u32 v114, v0, s6
	v_pk_fma_f32 v[0:1], v[146:147], v[58:59], v[86:87] op_sel_hi:[0,1,1] neg_lo:[1,0,0] neg_hi:[1,0,0]
	v_pk_fma_f32 v[0:1], v[146:147], v[0:1], v[62:63] op_sel:[1,0,0]
	v_add_lshl_u32 v114, v166, v114, 1
	v_cvt_pk_f16_f32 v86, v0, v1
	v_pk_fma_f32 v[0:1], v[146:147], v[60:61], v[88:89] op_sel_hi:[0,1,1] neg_lo:[1,0,0] neg_hi:[1,0,0]
	v_pk_fma_f32 v[0:1], v[146:147], v[0:1], v[64:65] op_sel:[1,0,0]
	s_nop 0
	v_cvt_pk_f16_f32 v87, v0, v1
	v_pk_fma_f32 v[0:1], v[146:147], v[50:51], v[82:83] op_sel_hi:[0,1,1] neg_lo:[1,0,0] neg_hi:[1,0,0]
	v_pk_fma_f32 v[0:1], v[146:147], v[0:1], v[54:55] op_sel:[1,0,0]
	s_nop 0
	v_cvt_pk_f16_f32 v88, v0, v1
	v_pk_fma_f32 v[0:1], v[146:147], v[52:53], v[84:85] op_sel_hi:[0,1,1] neg_lo:[1,0,0] neg_hi:[1,0,0]
	v_pk_fma_f32 v[0:1], v[146:147], v[0:1], v[56:57] op_sel:[1,0,0]
	s_nop 0
	v_cvt_pk_f16_f32 v89, v0, v1
	v_pk_fma_f32 v[0:1], v[146:147], v[42:43], v[98:99] op_sel_hi:[0,1,1] neg_lo:[1,0,0] neg_hi:[1,0,0]
	v_pk_fma_f32 v[0:1], v[146:147], v[0:1], v[46:47] op_sel:[1,0,0]
	buffer_store_dwordx4 v[86:89], v114, s[8:11], 0 offen sc1
	v_cvt_pk_f16_f32 v82, v0, v1
	v_pk_fma_f32 v[0:1], v[146:147], v[44:45], v[100:101] op_sel_hi:[0,1,1] neg_lo:[1,0,0] neg_hi:[1,0,0]
	v_pk_fma_f32 v[0:1], v[146:147], v[0:1], v[48:49] op_sel:[1,0,0]
	s_nop 0
	v_cvt_pk_f16_f32 v83, v0, v1
	v_pk_fma_f32 v[0:1], v[146:147], v[34:35], v[90:91] op_sel_hi:[0,1,1] neg_lo:[1,0,0] neg_hi:[1,0,0]
	v_pk_fma_f32 v[0:1], v[146:147], v[0:1], v[38:39] op_sel:[1,0,0]
	s_nop 0
	v_cvt_pk_f16_f32 v84, v0, v1
	v_pk_fma_f32 v[0:1], v[146:147], v[36:37], v[92:93] op_sel_hi:[0,1,1] neg_lo:[1,0,0] neg_hi:[1,0,0]
	v_pk_fma_f32 v[0:1], v[146:147], v[0:1], v[40:41] op_sel:[1,0,0]
	s_nop 0
	v_cvt_pk_f16_f32 v85, v0, v1
	v_add_u32_e32 v0, 0x80, v167
	v_mul_lo_u32 v86, v0, s6
	v_pk_fma_f32 v[0:1], v[148:149], v[58:59], v[102:103] op_sel_hi:[0,1,1] neg_lo:[1,0,0] neg_hi:[1,0,0]
	v_pk_fma_f32 v[0:1], v[148:149], v[0:1], v[62:63] op_sel:[1,0,0]
	buffer_store_dwordx4 v[82:85], v114, s[8:11], 0 offen offset:256 sc1
	v_add_lshl_u32 v90, v166, v86, 1
	ds_read2_b64 v[86:89], v169 offset0:144 offset1:160
	v_cvt_pk_f16_f32 v82, v0, v1
	v_pk_fma_f32 v[0:1], v[148:149], v[60:61], v[104:105] op_sel_hi:[0,1,1] neg_lo:[1,0,0] neg_hi:[1,0,0]
	v_pk_fma_f32 v[0:1], v[148:149], v[0:1], v[64:65] op_sel:[1,0,0]
	s_nop 0
	v_cvt_pk_f16_f32 v83, v0, v1
	v_pk_fma_f32 v[0:1], v[148:149], v[50:51], v[94:95] op_sel_hi:[0,1,1] neg_lo:[1,0,0] neg_hi:[1,0,0]
	v_pk_fma_f32 v[0:1], v[148:149], v[0:1], v[54:55] op_sel:[1,0,0]
	s_nop 0
	v_cvt_pk_f16_f32 v84, v0, v1
	v_pk_fma_f32 v[0:1], v[148:149], v[52:53], v[96:97] op_sel_hi:[0,1,1] neg_lo:[1,0,0] neg_hi:[1,0,0]
	v_pk_fma_f32 v[0:1], v[148:149], v[0:1], v[56:57] op_sel:[1,0,0]
	s_nop 0
	v_cvt_pk_f16_f32 v85, v0, v1
	v_pk_fma_f32 v[0:1], v[148:149], v[42:43], v[110:111] op_sel_hi:[0,1,1] neg_lo:[1,0,0] neg_hi:[1,0,0]
	v_pk_fma_f32 v[0:1], v[148:149], v[0:1], v[46:47] op_sel:[1,0,0]
	buffer_store_dwordx4 v[82:85], v90, s[8:11], 0 offen sc1
	s_nop 1
	v_cvt_pk_f16_f32 v82, v0, v1
	v_pk_fma_f32 v[0:1], v[148:149], v[44:45], v[112:113] op_sel_hi:[0,1,1] neg_lo:[1,0,0] neg_hi:[1,0,0]
	v_pk_fma_f32 v[0:1], v[148:149], v[0:1], v[48:49] op_sel:[1,0,0]
	s_nop 0
	v_cvt_pk_f16_f32 v83, v0, v1
	v_pk_fma_f32 v[0:1], v[148:149], v[34:35], v[106:107] op_sel_hi:[0,1,1] neg_lo:[1,0,0] neg_hi:[1,0,0]
	v_pk_fma_f32 v[0:1], v[148:149], v[0:1], v[38:39] op_sel:[1,0,0]
	s_nop 0
	v_cvt_pk_f16_f32 v84, v0, v1
	v_pk_fma_f32 v[0:1], v[148:149], v[36:37], v[108:109] op_sel_hi:[0,1,1] neg_lo:[1,0,0] neg_hi:[1,0,0]
	v_pk_fma_f32 v[0:1], v[148:149], v[0:1], v[40:41] op_sel:[1,0,0]
	s_nop 0
	v_cvt_pk_f16_f32 v85, v0, v1
	v_add_u32_e32 v0, 0x90, v167
	buffer_store_dwordx4 v[82:85], v90, s[8:11], 0 offen offset:256 sc1
	s_nop 1
	v_mul_lo_u32 v82, v0, s6
	s_waitcnt lgkmcnt(0)
	v_pk_fma_f32 v[0:1], v[86:87], v[58:59], v[70:71] op_sel_hi:[0,1,1] neg_lo:[1,0,0] neg_hi:[1,0,0]
	v_pk_fma_f32 v[0:1], v[86:87], v[0:1], v[62:63] op_sel:[1,0,0]
	v_add_lshl_u32 v82, v166, v82, 1
	v_cvt_pk_f16_f32 v70, v0, v1
	v_pk_fma_f32 v[0:1], v[86:87], v[60:61], v[72:73] op_sel_hi:[0,1,1] neg_lo:[1,0,0] neg_hi:[1,0,0]
	v_pk_fma_f32 v[0:1], v[86:87], v[0:1], v[64:65] op_sel:[1,0,0]
	s_nop 0
	v_cvt_pk_f16_f32 v71, v0, v1
	v_pk_fma_f32 v[0:1], v[86:87], v[50:51], v[66:67] op_sel_hi:[0,1,1] neg_lo:[1,0,0] neg_hi:[1,0,0]
	v_pk_fma_f32 v[0:1], v[86:87], v[0:1], v[54:55] op_sel:[1,0,0]
	s_nop 0
	v_cvt_pk_f16_f32 v72, v0, v1
	v_pk_fma_f32 v[0:1], v[86:87], v[52:53], v[68:69] op_sel_hi:[0,1,1] neg_lo:[1,0,0] neg_hi:[1,0,0]
	v_pk_fma_f32 v[0:1], v[86:87], v[0:1], v[56:57] op_sel:[1,0,0]
	s_nop 0
	v_cvt_pk_f16_f32 v73, v0, v1
	v_pk_fma_f32 v[0:1], v[86:87], v[42:43], v[78:79] op_sel_hi:[0,1,1] neg_lo:[1,0,0] neg_hi:[1,0,0]
	v_pk_fma_f32 v[0:1], v[86:87], v[0:1], v[46:47] op_sel:[1,0,0]
	buffer_store_dwordx4 v[70:73], v82, s[8:11], 0 offen sc1
	v_cvt_pk_f16_f32 v66, v0, v1
	v_pk_fma_f32 v[0:1], v[86:87], v[44:45], v[80:81] op_sel_hi:[0,1,1] neg_lo:[1,0,0] neg_hi:[1,0,0]
	v_pk_fma_f32 v[0:1], v[86:87], v[0:1], v[48:49] op_sel:[1,0,0]
	s_nop 0
	v_cvt_pk_f16_f32 v67, v0, v1
	v_pk_fma_f32 v[0:1], v[86:87], v[34:35], v[74:75] op_sel_hi:[0,1,1] neg_lo:[1,0,0] neg_hi:[1,0,0]
	v_pk_fma_f32 v[0:1], v[86:87], v[0:1], v[38:39] op_sel:[1,0,0]
	s_nop 0
	v_cvt_pk_f16_f32 v68, v0, v1
	v_pk_fma_f32 v[0:1], v[86:87], v[36:37], v[76:77] op_sel_hi:[0,1,1] neg_lo:[1,0,0] neg_hi:[1,0,0]
	v_pk_fma_f32 v[0:1], v[86:87], v[0:1], v[40:41] op_sel:[1,0,0]
	s_nop 0
	v_cvt_pk_f16_f32 v69, v0, v1
	v_add_u32_e32 v0, 0xa0, v167
	buffer_store_dwordx4 v[66:69], v82, s[8:11], 0 offen offset:256 sc1
	s_nop 1
	v_mul_lo_u32 v66, v0, s6
	v_pk_fma_f32 v[0:1], v[88:89], v[58:59], v[22:23] op_sel_hi:[0,1,1] neg_lo:[1,0,0] neg_hi:[1,0,0]
	v_pk_fma_f32 v[0:1], v[88:89], v[0:1], v[62:63] op_sel:[1,0,0]
	v_add_lshl_u32 v66, v166, v66, 1
	v_cvt_pk_f16_f32 v22, v0, v1
	v_pk_fma_f32 v[0:1], v[88:89], v[60:61], v[24:25] op_sel_hi:[0,1,1] neg_lo:[1,0,0] neg_hi:[1,0,0]
	v_pk_fma_f32 v[0:1], v[88:89], v[0:1], v[64:65] op_sel:[1,0,0]
	s_nop 0
	v_cvt_pk_f16_f32 v23, v0, v1
	v_pk_fma_f32 v[0:1], v[88:89], v[50:51], v[18:19] op_sel_hi:[0,1,1] neg_lo:[1,0,0] neg_hi:[1,0,0]
	v_pk_fma_f32 v[0:1], v[88:89], v[0:1], v[54:55] op_sel:[1,0,0]
	s_nop 0
	v_cvt_pk_f16_f32 v24, v0, v1
	v_pk_fma_f32 v[0:1], v[88:89], v[52:53], v[20:21] op_sel_hi:[0,1,1] neg_lo:[1,0,0] neg_hi:[1,0,0]
	v_pk_fma_f32 v[0:1], v[88:89], v[0:1], v[56:57] op_sel:[1,0,0]
	s_nop 0
	v_cvt_pk_f16_f32 v25, v0, v1
	v_pk_fma_f32 v[0:1], v[88:89], v[42:43], v[30:31] op_sel_hi:[0,1,1] neg_lo:[1,0,0] neg_hi:[1,0,0]
	v_pk_fma_f32 v[0:1], v[88:89], v[0:1], v[46:47] op_sel:[1,0,0]
	buffer_store_dwordx4 v[22:25], v66, s[8:11], 0 offen sc1
	v_cvt_pk_f16_f32 v18, v0, v1
	v_pk_fma_f32 v[0:1], v[88:89], v[44:45], v[32:33] op_sel_hi:[0,1,1] neg_lo:[1,0,0] neg_hi:[1,0,0]
	v_pk_fma_f32 v[0:1], v[88:89], v[0:1], v[48:49] op_sel:[1,0,0]
	s_nop 0
	v_cvt_pk_f16_f32 v19, v0, v1
	v_pk_fma_f32 v[0:1], v[88:89], v[34:35], v[26:27] op_sel_hi:[0,1,1] neg_lo:[1,0,0] neg_hi:[1,0,0]
	v_pk_fma_f32 v[0:1], v[88:89], v[0:1], v[38:39] op_sel:[1,0,0]
	s_nop 0
	v_cvt_pk_f16_f32 v20, v0, v1
	v_pk_fma_f32 v[0:1], v[88:89], v[36:37], v[28:29] op_sel_hi:[0,1,1] neg_lo:[1,0,0] neg_hi:[1,0,0]
	v_pk_fma_f32 v[0:1], v[88:89], v[0:1], v[40:41] op_sel:[1,0,0]
	s_nop 0
	v_cvt_pk_f16_f32 v21, v0, v1
	v_add_u32_e32 v0, 0xb0, v167
	buffer_store_dwordx4 v[18:21], v66, s[8:11], 0 offen offset:256 sc1
	s_nop 1
	v_mul_lo_u32 v18, v0, s6
	v_pk_fma_f32 v[0:1], v[152:153], v[58:59], v[14:15] op_sel_hi:[0,1,1] neg_lo:[1,0,0] neg_hi:[1,0,0]
	v_pk_fma_f32 v[0:1], v[152:153], v[0:1], v[62:63] op_sel:[1,0,0]
	s_nop 0
	v_cvt_pk_f16_f32 v14, v0, v1
	v_pk_fma_f32 v[0:1], v[152:153], v[60:61], v[16:17] op_sel_hi:[0,1,1] neg_lo:[1,0,0] neg_hi:[1,0,0]
	v_pk_fma_f32 v[0:1], v[152:153], v[0:1], v[64:65] op_sel:[1,0,0]
	s_nop 0
	v_cvt_pk_f16_f32 v15, v0, v1
	v_pk_fma_f32 v[0:1], v[152:153], v[50:51], v[6:7] op_sel_hi:[0,1,1] neg_lo:[1,0,0] neg_hi:[1,0,0]
	v_pk_fma_f32 v[0:1], v[152:153], v[0:1], v[54:55] op_sel:[1,0,0]
	v_pk_fma_f32 v[6:7], v[152:153], v[44:45], v[12:13] op_sel_hi:[0,1,1] neg_lo:[1,0,0] neg_hi:[1,0,0]
	v_cvt_pk_f16_f32 v16, v0, v1
	v_pk_fma_f32 v[0:1], v[152:153], v[52:53], v[8:9] op_sel_hi:[0,1,1] neg_lo:[1,0,0] neg_hi:[1,0,0]
	v_pk_fma_f32 v[0:1], v[152:153], v[0:1], v[56:57] op_sel:[1,0,0]
	v_pk_fma_f32 v[6:7], v[152:153], v[6:7], v[48:49] op_sel:[1,0,0]
	v_cvt_pk_f16_f32 v17, v0, v1
	v_pk_fma_f32 v[0:1], v[152:153], v[42:43], v[10:11] op_sel_hi:[0,1,1] neg_lo:[1,0,0] neg_hi:[1,0,0]
	v_pk_fma_f32 v[0:1], v[152:153], v[0:1], v[46:47] op_sel:[1,0,0]
	v_add_lshl_u32 v8, v166, v18, 1
	v_cvt_pk_f16_f32 v0, v0, v1
	v_cvt_pk_f16_f32 v1, v6, v7
	buffer_store_dwordx4 v[14:17], v8, s[8:11], 0 offen sc1
	buffer_store_dwordx4 v[0:3], v8, s[8:11], 0 offen offset:256 sc1
	s_endpgm

.LBB8_6:
	s_or_b64 exec, exec, s[2:3]
	s_add_i32 s0, 0, 0x18000
	v_add_u32_e32 v48, s0, v38
	s_mov_b64 s[0:1], 0x80
	v_readfirstlane_b32 s22, v48
	v_add_u32_e32 v49, 0x2000, v48
	v_lshl_add_u64 v[2:3], v[30:31], 0, s[0:1]
	s_mov_b32 m0, s22
	v_readfirstlane_b32 s21, v49
	v_add_u32_e32 v46, 0x8000, v35
	s_waitcnt vmcnt(4)
	s_barrier
	global_load_lds_dwordx4 v[2:3], off
	v_lshl_add_u64 v[2:3], v[32:33], 0, s[0:1]
	s_mov_b32 m0, s21
	v_readfirstlane_b32 s19, v46
	v_add_u32_e32 v47, 0xa000, v35
	s_add_i32 s2, 0, 0x1c000
	global_load_lds_dwordx4 v[2:3], off
	v_lshl_add_u64 v[2:3], v[26:27], 0, s[0:1]
	s_mov_b32 m0, s19
	v_readfirstlane_b32 s16, v47
	v_add_u32_e32 v37, s2, v38
	global_load_lds_dwordx4 v[2:3], off
	v_lshl_add_u64 v[2:3], v[28:29], 0, s[0:1]
	s_mov_b32 m0, s16
	v_readfirstlane_b32 s3, v37
	v_add_u32_e32 v39, 0x2000, v37
	global_load_lds_dwordx4 v[2:3], off
	v_lshl_add_u64 v[2:3], v[22:23], 0, s[0:1]
	s_mov_b32 m0, s3
	v_readfirstlane_b32 s2, v39
	global_load_lds_dwordx4 v[2:3], off
	v_lshl_add_u64 v[2:3], v[24:25], 0, s[0:1]
	s_mov_b32 m0, s2
	v_lshlrev_b32_e32 v1, 6, v0
	global_load_lds_dwordx4 v[2:3], off
	v_lshlrev_b32_e32 v4, 2, v0
	v_and_b32_e32 v2, 0x3c0, v1
	v_and_b32_e32 v3, 48, v0
	v_and_b32_e32 v4, 32, v4
	v_bitop3_b32 v6, v2, v4, v3 bitop3:0x36
	v_and_b32_e32 v1, 0x3000, v1
	v_add3_u32 v234, 0, v1, v6
	v_add_u32_e32 v2, 0x10000, v234
	v_add_u32_e32 v4, 0x10800, v234
	s_waitcnt vmcnt(6)
	s_barrier
	v_add_u32_e32 v3, 0x10400, v234
	ds_read_b128 v[10:13], v2
	ds_read_b128 v[14:17], v3
	v_add_u32_e32 v5, 0x10c00, v234
	ds_read_b128 v[50:53], v4
	ds_read_b128 v[54:57], v5
	v_lshlrev_b32_e32 v1, 5, v0
	v_and_b32_e32 v1, 0x2000, v1
	v_add3_u32 v1, 0, v1, v6
	v_add_u32_e32 v38, 0xc000, v35
	v_add_u32_e32 v40, 0xe000, v35
	v_readfirstlane_b32 s7, v38
	v_lshl_add_u64 v[6:7], v[18:19], 0, s[0:1]
	s_mov_b32 m0, s7
	v_readfirstlane_b32 s4, v40
	global_load_lds_dwordx4 v[6:7], off
	v_lshl_add_u64 v[6:7], v[20:21], 0, s[0:1]
	s_mov_b32 m0, s4
	s_nop 0
	global_load_lds_dwordx4 v[6:7], off
	ds_read_b128 v[42:45], v1
	ds_read_b128 v[58:61], v1 offset:1024
	ds_read_b128 v[62:65], v1 offset:2048
	ds_read_b128 v[66:69], v1 offset:3072
	ds_read_b128 v[70:73], v1 offset:4096
	ds_read_b128 v[74:77], v1 offset:5120
	ds_read_b128 v[78:81], v1 offset:6144
	ds_read_b128 v[82:85], v1 offset:7168
	s_waitcnt lgkmcnt(8)
	s_barrier
	s_waitcnt lgkmcnt(0)
	s_setprio 1
	s_waitcnt lgkmcnt(0)
	v_mfma_f32_16x16x32_f16 v[6:9], v[10:13], v[42:45], 0
	v_mfma_f32_16x16x32_f16 v[86:89], v[14:17], v[58:61], v[6:9]
	v_mfma_f32_16x16x32_f16 v[6:9], v[50:53], v[42:45], 0
	v_mfma_f32_16x16x32_f16 v[90:93], v[54:57], v[58:61], v[6:9]
	v_mfma_f32_16x16x32_f16 v[6:9], v[10:13], v[62:65], 0
	v_mfma_f32_16x16x32_f16 v[94:97], v[14:17], v[66:69], v[6:9]
	v_mfma_f32_16x16x32_f16 v[6:9], v[50:53], v[62:65], 0
	v_mfma_f32_16x16x32_f16 v[98:101], v[54:57], v[66:69], v[6:9]
	v_mfma_f32_16x16x32_f16 v[6:9], v[10:13], v[70:73], 0
	v_mfma_f32_16x16x32_f16 v[102:105], v[14:17], v[74:77], v[6:9]
	v_mfma_f32_16x16x32_f16 v[6:9], v[50:53], v[70:73], 0
	v_mfma_f32_16x16x32_f16 v[106:109], v[54:57], v[74:77], v[6:9]
	v_mfma_f32_16x16x32_f16 v[6:9], v[10:13], v[78:81], 0
	v_mfma_f32_16x16x32_f16 v[110:113], v[14:17], v[82:85], v[6:9]
	v_mfma_f32_16x16x32_f16 v[6:9], v[50:53], v[78:81], 0
	v_mfma_f32_16x16x32_f16 v[114:117], v[54:57], v[82:85], v[6:9]
	s_setprio 0
	s_barrier
	s_mov_b64 s[0:1], 0x100
	v_readfirstlane_b32 s15, v36
	v_add_u32_e32 v41, 0x2000, v36
	s_nop 1
	v_add_u32_e32 v6, 0x14000, v234
	v_add_u32_e32 v8, 0x14800, v234
	v_lshl_add_u64 v[134:135], v[30:31], 0, s[0:1]
	s_mov_b32 m0, s15
	v_readfirstlane_b32 s5, v41
	v_add_u32_e32 v7, 0x14400, v234
	ds_read_b128 v[118:121], v6
	ds_read_b128 v[122:125], v7
	v_add_u32_e32 v9, 0x14c00, v234
	ds_read_b128 v[126:129], v8
	ds_read_b128 v[130:133], v9
	global_load_lds_dwordx4 v[134:135], off
	v_lshl_add_u64 v[134:135], v[32:33], 0, s[0:1]
	s_mov_b32 m0, s5
	s_nop 0
	global_load_lds_dwordx4 v[134:135], off
	s_barrier
	s_waitcnt lgkmcnt(0)
	s_setprio 1
	s_waitcnt lgkmcnt(0)
	v_mfma_f32_16x16x32_f16 v[134:137], v[118:121], v[42:45], 0
	v_mfma_f32_16x16x32_f16 v[42:45], v[126:129], v[42:45], 0
	v_mfma_f32_16x16x32_f16 v[134:137], v[122:125], v[58:61], v[134:137]
	v_mfma_f32_16x16x32_f16 v[58:61], v[130:133], v[58:61], v[42:45]
	v_mfma_f32_16x16x32_f16 v[42:45], v[118:121], v[62:65], 0
	v_mfma_f32_16x16x32_f16 v[138:141], v[122:125], v[66:69], v[42:45]
	v_mfma_f32_16x16x32_f16 v[42:45], v[126:129], v[62:65], 0
	v_mfma_f32_16x16x32_f16 v[62:65], v[130:133], v[66:69], v[42:45]
	v_mfma_f32_16x16x32_f16 v[42:45], v[118:121], v[70:73], 0
	v_mfma_f32_16x16x32_f16 v[66:69], v[122:125], v[74:77], v[42:45]
	v_mfma_f32_16x16x32_f16 v[42:45], v[126:129], v[70:73], 0
	v_mfma_f32_16x16x32_f16 v[70:73], v[130:133], v[74:77], v[42:45]
	v_mfma_f32_16x16x32_f16 v[42:45], v[118:121], v[78:81], 0
	v_mfma_f32_16x16x32_f16 v[74:77], v[122:125], v[82:85], v[42:45]
	v_mfma_f32_16x16x32_f16 v[42:45], v[126:129], v[78:81], 0
	v_mfma_f32_16x16x32_f16 v[78:81], v[130:133], v[82:85], v[42:45]
	s_setprio 0
	v_readfirstlane_b32 s17, v35
	s_nop 4
	v_lshl_add_u64 v[42:43], v[26:27], 0, s[0:1]
	s_mov_b32 m0, s17
	s_barrier
	ds_read_b128 v[82:85], v1 offset:16384
	ds_read_b128 v[142:145], v1 offset:17408
	ds_read_b128 v[146:149], v1 offset:18432
	ds_read_b128 v[150:153], v1 offset:19456
	ds_read_b128 v[154:157], v1 offset:20480
	ds_read_b128 v[158:161], v1 offset:21504
	ds_read_b128 v[162:165], v1 offset:22528
	ds_read_b128 v[166:169], v1 offset:23552
	global_load_lds_dwordx4 v[42:43], off
	v_add_u32_e32 v42, 0x2000, v35
	v_lshl_add_u64 v[44:45], v[28:29], 0, s[0:1]
	v_readfirstlane_b32 s10, v42
	s_mov_b32 m0, s10
	s_nop 0
	global_load_lds_dwordx4 v[44:45], off
	s_barrier
	s_waitcnt lgkmcnt(0)
	s_setprio 1
	s_waitcnt lgkmcnt(0)
	v_mfma_f32_16x16x32_f16 v[170:173], v[10:13], v[82:85], 0
	v_mfma_f32_16x16x32_f16 v[178:181], v[10:13], v[146:149], 0
	v_mfma_f32_16x16x32_f16 v[186:189], v[10:13], v[154:157], 0
	v_mfma_f32_16x16x32_f16 v[10:13], v[10:13], v[162:165], 0
	v_mfma_f32_16x16x32_f16 v[194:197], v[14:17], v[166:169], v[10:13]
	v_mfma_f32_16x16x32_f16 v[10:13], v[50:53], v[162:165], 0
	v_mfma_f32_16x16x32_f16 v[174:177], v[50:53], v[82:85], 0
	v_mfma_f32_16x16x32_f16 v[182:185], v[50:53], v[146:149], 0
	v_mfma_f32_16x16x32_f16 v[190:193], v[50:53], v[154:157], 0
	v_mfma_f32_16x16x32_f16 v[50:53], v[54:57], v[166:169], v[10:13]
	v_mfma_f32_16x16x32_f16 v[170:173], v[14:17], v[142:145], v[170:173]
	v_mfma_f32_16x16x32_f16 v[174:177], v[54:57], v[142:145], v[174:177]
	v_mfma_f32_16x16x32_f16 v[178:181], v[14:17], v[150:153], v[178:181]
	v_mfma_f32_16x16x32_f16 v[182:185], v[54:57], v[150:153], v[182:185]
	v_mfma_f32_16x16x32_f16 v[186:189], v[14:17], v[158:161], v[186:189]
	v_mfma_f32_16x16x32_f16 v[190:193], v[54:57], v[158:161], v[190:193]
	s_setprio 0
	s_barrier
	v_readfirstlane_b32 s14, v34
	v_add_u32_e32 v43, 0x2000, v34
	v_lshl_add_u64 v[10:11], v[22:23], 0, s[0:1]
	s_mov_b32 m0, s14
	v_readfirstlane_b32 s11, v43
	global_load_lds_dwordx4 v[10:11], off
	v_lshl_add_u64 v[10:11], v[24:25], 0, s[0:1]
	s_mov_b32 m0, s11
	s_nop 0
	global_load_lds_dwordx4 v[10:11], off
	s_waitcnt vmcnt(6)
	s_barrier
	s_setprio 1
	v_mfma_f32_16x16x32_f16 v[10:13], v[118:121], v[82:85], 0
	v_mfma_f32_16x16x32_f16 v[54:57], v[122:125], v[142:145], v[10:13]
	v_mfma_f32_16x16x32_f16 v[10:13], v[126:129], v[82:85], 0
	v_mfma_f32_16x16x32_f16 v[82:85], v[130:133], v[142:145], v[10:13]
	v_mfma_f32_16x16x32_f16 v[10:13], v[118:121], v[146:149], 0
	v_mfma_f32_16x16x32_f16 v[142:145], v[122:125], v[150:153], v[10:13]
	v_mfma_f32_16x16x32_f16 v[10:13], v[126:129], v[146:149], 0
	v_mfma_f32_16x16x32_f16 v[146:149], v[130:133], v[150:153], v[10:13]
	v_mfma_f32_16x16x32_f16 v[10:13], v[118:121], v[154:157], 0
	v_mfma_f32_16x16x32_f16 v[150:153], v[122:125], v[158:161], v[10:13]
	v_mfma_f32_16x16x32_f16 v[10:13], v[126:129], v[154:157], 0
	v_mfma_f32_16x16x32_f16 v[154:157], v[130:133], v[158:161], v[10:13]
	v_mfma_f32_16x16x32_f16 v[10:13], v[118:121], v[162:165], 0
	v_mfma_f32_16x16x32_f16 v[118:121], v[122:125], v[166:169], v[10:13]
	v_mfma_f32_16x16x32_f16 v[10:13], v[126:129], v[162:165], 0
	v_mfma_f32_16x16x32_f16 v[122:125], v[130:133], v[166:169], v[10:13]
	s_setprio 0
	s_nop 5
	v_add_u32_e32 v10, 0x18000, v234
	v_add_u32_e32 v12, 0x18800, v234
	s_barrier
	v_add_u32_e32 v11, 0x18400, v234
	ds_read_b128 v[126:129], v10
	ds_read_b128 v[130:133], v11
	v_add_u32_e32 v13, 0x18c00, v234
	ds_read_b128 v[158:161], v12
	ds_read_b128 v[162:165], v13
	v_add_u32_e32 v44, 0x4000, v35
	v_add_u32_e32 v45, 0x6000, v35
	v_readfirstlane_b32 s20, v44
	v_lshl_add_u64 v[14:15], v[18:19], 0, s[0:1]
	s_mov_b32 m0, s20
	v_readfirstlane_b32 s18, v45
	ds_read_b128 v[166:169], v1 offset:32768
	ds_read_b128 v[198:201], v1 offset:33792
	ds_read_b128 v[202:205], v1 offset:34816
	ds_read_b128 v[206:209], v1 offset:35840
	ds_read_b128 v[210:213], v1 offset:36864
	ds_read_b128 v[214:217], v1 offset:37888
	ds_read_b128 v[218:221], v1 offset:38912
	ds_read_b128 v[222:225], v1 offset:39936
	global_load_lds_dwordx4 v[14:15], off
	v_lshl_add_u64 v[14:15], v[20:21], 0, s[0:1]
	s_mov_b32 m0, s18
	s_nop 0
	global_load_lds_dwordx4 v[14:15], off
	s_waitcnt lgkmcnt(8)
	s_barrier
	s_waitcnt lgkmcnt(0)
	s_setprio 1
	s_waitcnt lgkmcnt(0)
	v_mfma_f32_16x16x32_f16 v[14:17], v[126:129], v[166:169], v[86:89]
	v_mfma_f32_16x16x32_f16 v[86:89], v[130:133], v[198:201], v[14:17]
	v_mfma_f32_16x16x32_f16 v[14:17], v[158:161], v[166:169], v[90:93]
	v_mfma_f32_16x16x32_f16 v[90:93], v[162:165], v[198:201], v[14:17]
	v_mfma_f32_16x16x32_f16 v[14:17], v[126:129], v[202:205], v[94:97]
	v_mfma_f32_16x16x32_f16 v[94:97], v[130:133], v[206:209], v[14:17]
	v_mfma_f32_16x16x32_f16 v[14:17], v[158:161], v[202:205], v[98:101]
	v_mfma_f32_16x16x32_f16 v[98:101], v[162:165], v[206:209], v[14:17]
	v_mfma_f32_16x16x32_f16 v[14:17], v[126:129], v[210:213], v[102:105]
	v_mfma_f32_16x16x32_f16 v[102:105], v[130:133], v[214:217], v[14:17]
	v_mfma_f32_16x16x32_f16 v[14:17], v[158:161], v[210:213], v[106:109]
	v_mfma_f32_16x16x32_f16 v[106:109], v[162:165], v[214:217], v[14:17]
	v_mfma_f32_16x16x32_f16 v[14:17], v[126:129], v[218:221], v[110:113]
	v_mfma_f32_16x16x32_f16 v[110:113], v[130:133], v[222:225], v[14:17]
	v_mfma_f32_16x16x32_f16 v[14:17], v[158:161], v[218:221], v[114:117]
	v_mfma_f32_16x16x32_f16 v[114:117], v[162:165], v[222:225], v[14:17]
	s_setprio 0
	s_barrier
	s_mov_b64 s[0:1], 0x180
	s_mov_b32 m0, s22
	s_nop 2
	v_add_u32_e32 v14, 0x1c000, v234
	v_add_u32_e32 v16, 0x1c800, v234
	v_lshl_add_u64 v[242:243], v[30:31], 0, s[0:1]
	v_add_u32_e32 v15, 0x1c400, v234
	ds_read_b128 v[226:229], v14
	ds_read_b128 v[230:233], v15
	v_add_u32_e32 v17, 0x1cc00, v234
	ds_read_b128 v[234:237], v16
	ds_read_b128 v[238:241], v17
	global_load_lds_dwordx4 v[242:243], off
	v_lshl_add_u64 v[242:243], v[32:33], 0, s[0:1]
	s_mov_b32 m0, s21
	s_nop 0
	global_load_lds_dwordx4 v[242:243], off
	s_barrier
	s_waitcnt lgkmcnt(0)
	s_setprio 1
	s_waitcnt lgkmcnt(0)
	v_mfma_f32_16x16x32_f16 v[134:137], v[226:229], v[166:169], v[134:137]
	v_mfma_f32_16x16x32_f16 v[58:61], v[234:237], v[166:169], v[58:61]
	v_mfma_f32_16x16x32_f16 v[138:141], v[226:229], v[202:205], v[138:141]
	v_mfma_f32_16x16x32_f16 v[62:65], v[234:237], v[202:205], v[62:65]
	v_mfma_f32_16x16x32_f16 v[66:69], v[226:229], v[210:213], v[66:69]
	v_mfma_f32_16x16x32_f16 v[70:73], v[234:237], v[210:213], v[70:73]
	v_mfma_f32_16x16x32_f16 v[74:77], v[226:229], v[218:221], v[74:77]
	v_mfma_f32_16x16x32_f16 v[78:81], v[234:237], v[218:221], v[78:81]
	v_mfma_f32_16x16x32_f16 v[134:137], v[230:233], v[198:201], v[134:137]
	v_mfma_f32_16x16x32_f16 v[58:61], v[238:241], v[198:201], v[58:61]
	v_mfma_f32_16x16x32_f16 v[138:141], v[230:233], v[206:209], v[138:141]
	v_mfma_f32_16x16x32_f16 v[62:65], v[238:241], v[206:209], v[62:65]
	v_mfma_f32_16x16x32_f16 v[66:69], v[230:233], v[214:217], v[66:69]
	v_mfma_f32_16x16x32_f16 v[70:73], v[238:241], v[214:217], v[70:73]
	v_mfma_f32_16x16x32_f16 v[74:77], v[230:233], v[222:225], v[74:77]
	v_mfma_f32_16x16x32_f16 v[78:81], v[238:241], v[222:225], v[78:81]
	s_setprio 0
	s_mov_b32 m0, s19
	v_lshl_add_u64 v[242:243], v[26:27], 0, s[0:1]
	s_barrier
	ds_read_b128 v[166:169], v1 offset:49152
	ds_read_b128 v[198:201], v1 offset:50176
	ds_read_b128 v[202:205], v1 offset:51200
	ds_read_b128 v[206:209], v1 offset:52224
	ds_read_b128 v[210:213], v1 offset:53248
	ds_read_b128 v[214:217], v1 offset:54272
	ds_read_b128 v[218:221], v1 offset:55296
	ds_read_b128 v[222:225], v1 offset:56320
	global_load_lds_dwordx4 v[242:243], off
	v_lshl_add_u64 v[242:243], v[28:29], 0, s[0:1]
	s_mov_b32 m0, s16
	s_nop 0
	global_load_lds_dwordx4 v[242:243], off
	s_barrier
	s_waitcnt lgkmcnt(0)
	s_setprio 1
	s_waitcnt lgkmcnt(0)
	v_mfma_f32_16x16x32_f16 v[170:173], v[126:129], v[166:169], v[170:173]
	v_mfma_f32_16x16x32_f16 v[178:181], v[126:129], v[202:205], v[178:181]
	v_mfma_f32_16x16x32_f16 v[186:189], v[126:129], v[210:213], v[186:189]
	v_mfma_f32_16x16x32_f16 v[126:129], v[126:129], v[218:221], v[194:197]
	v_mfma_f32_16x16x32_f16 v[50:53], v[158:161], v[218:221], v[50:53]
	v_mfma_f32_16x16x32_f16 v[174:177], v[158:161], v[166:169], v[174:177]
	v_mfma_f32_16x16x32_f16 v[182:185], v[158:161], v[202:205], v[182:185]
	v_mfma_f32_16x16x32_f16 v[190:193], v[158:161], v[210:213], v[190:193]
	v_mfma_f32_16x16x32_f16 v[126:129], v[130:133], v[222:225], v[126:129]
	v_mfma_f32_16x16x32_f16 v[50:53], v[162:165], v[222:225], v[50:53]
	v_mfma_f32_16x16x32_f16 v[170:173], v[130:133], v[198:201], v[170:173]
	v_mfma_f32_16x16x32_f16 v[174:177], v[162:165], v[198:201], v[174:177]
	v_mfma_f32_16x16x32_f16 v[178:181], v[130:133], v[206:209], v[178:181]
	v_mfma_f32_16x16x32_f16 v[182:185], v[162:165], v[206:209], v[182:185]
	v_mfma_f32_16x16x32_f16 v[186:189], v[130:133], v[214:217], v[186:189]
	v_mfma_f32_16x16x32_f16 v[190:193], v[162:165], v[214:217], v[190:193]
	s_setprio 0
	s_barrier
	s_mov_b32 m0, s3
	v_lshl_add_u64 v[130:131], v[22:23], 0, s[0:1]
	global_load_lds_dwordx4 v[130:131], off
	v_lshl_add_u64 v[130:131], v[24:25], 0, s[0:1]
	s_mov_b32 m0, s2
	s_nop 0
	global_load_lds_dwordx4 v[130:131], off
	s_waitcnt vmcnt(6)
	s_barrier
	s_setprio 1
	v_mfma_f32_16x16x32_f16 v[82:85], v[234:237], v[166:169], v[82:85]
	v_mfma_f32_16x16x32_f16 v[130:133], v[226:229], v[202:205], v[142:145]
	v_mfma_f32_16x16x32_f16 v[142:145], v[234:237], v[202:205], v[146:149]
	v_mfma_f32_16x16x32_f16 v[146:149], v[226:229], v[210:213], v[150:153]
	v_mfma_f32_16x16x32_f16 v[150:153], v[234:237], v[210:213], v[154:157]
	v_mfma_f32_16x16x32_f16 v[118:121], v[226:229], v[218:221], v[118:121]
	v_mfma_f32_16x16x32_f16 v[122:125], v[234:237], v[218:221], v[122:125]
	v_mfma_f32_16x16x32_f16 v[54:57], v[226:229], v[166:169], v[54:57]
	v_mfma_f32_16x16x32_f16 v[82:85], v[238:241], v[198:201], v[82:85]
	v_mfma_f32_16x16x32_f16 v[130:133], v[230:233], v[206:209], v[130:133]
	v_mfma_f32_16x16x32_f16 v[142:145], v[238:241], v[206:209], v[142:145]
	v_mfma_f32_16x16x32_f16 v[146:149], v[230:233], v[214:217], v[146:149]
	v_mfma_f32_16x16x32_f16 v[150:153], v[238:241], v[214:217], v[150:153]
	v_mfma_f32_16x16x32_f16 v[118:121], v[230:233], v[222:225], v[118:121]
	v_mfma_f32_16x16x32_f16 v[122:125], v[238:241], v[222:225], v[122:125]
	v_mfma_f32_16x16x32_f16 v[54:57], v[230:233], v[198:201], v[54:57]
	s_setprio 0
	s_barrier
	ds_read_b128 v[154:157], v2
	ds_read_b128 v[158:161], v3
	ds_read_b128 v[162:165], v4
	ds_read_b128 v[166:169], v5
	s_mov_b32 m0, s7
	v_lshl_add_u64 v[194:195], v[18:19], 0, s[0:1]
	global_load_lds_dwordx4 v[194:195], off
	v_lshl_add_u64 v[194:195], v[20:21], 0, s[0:1]
	s_mov_b32 m0, s4
	s_nop 0
	global_load_lds_dwordx4 v[194:195], off
	ds_read_b128 v[194:197], v1
	ds_read_b128 v[198:201], v1 offset:1024
	ds_read_b128 v[202:205], v1 offset:2048
	ds_read_b128 v[206:209], v1 offset:3072
	ds_read_b128 v[210:213], v1 offset:4096
	ds_read_b128 v[214:217], v1 offset:5120
	ds_read_b128 v[218:221], v1 offset:6144
	ds_read_b128 v[222:225], v1 offset:7168
	s_waitcnt lgkmcnt(8)
	s_barrier
	s_waitcnt lgkmcnt(0)
	s_setprio 1
	s_waitcnt lgkmcnt(0)
	v_mfma_f32_16x16x32_f16 v[86:89], v[154:157], v[194:197], v[86:89]
	v_mfma_f32_16x16x32_f16 v[90:93], v[162:165], v[194:197], v[90:93]
	v_mfma_f32_16x16x32_f16 v[94:97], v[154:157], v[202:205], v[94:97]
	v_mfma_f32_16x16x32_f16 v[98:101], v[162:165], v[202:205], v[98:101]
	v_mfma_f32_16x16x32_f16 v[102:105], v[154:157], v[210:213], v[102:105]
	v_mfma_f32_16x16x32_f16 v[106:109], v[162:165], v[210:213], v[106:109]
	v_mfma_f32_16x16x32_f16 v[110:113], v[154:157], v[218:221], v[110:113]
	v_mfma_f32_16x16x32_f16 v[86:89], v[158:161], v[198:201], v[86:89]
	v_mfma_f32_16x16x32_f16 v[90:93], v[166:169], v[198:201], v[90:93]
	v_mfma_f32_16x16x32_f16 v[94:97], v[158:161], v[206:209], v[94:97]
	v_mfma_f32_16x16x32_f16 v[98:101], v[166:169], v[206:209], v[98:101]
	v_mfma_f32_16x16x32_f16 v[102:105], v[158:161], v[214:217], v[102:105]
	v_mfma_f32_16x16x32_f16 v[106:109], v[166:169], v[214:217], v[106:109]
	v_mfma_f32_16x16x32_f16 v[110:113], v[158:161], v[222:225], v[110:113]
	v_mfma_f32_16x16x32_f16 v[114:117], v[162:165], v[218:221], v[114:117]
	v_mfma_f32_16x16x32_f16 v[114:117], v[166:169], v[222:225], v[114:117]
	s_setprio 0
	s_barrier
	s_mov_b64 s[0:1], 0x200
	s_mov_b32 m0, s15
	v_lshl_add_u64 v[242:243], v[30:31], 0, s[0:1]
	ds_read_b128 v[226:229], v6
	ds_read_b128 v[230:233], v7
	ds_read_b128 v[234:237], v8
	ds_read_b128 v[238:241], v9
	global_load_lds_dwordx4 v[242:243], off
	v_lshl_add_u64 v[242:243], v[32:33], 0, s[0:1]
	s_mov_b32 m0, s5
	s_nop 0
	global_load_lds_dwordx4 v[242:243], off
	s_barrier
	s_waitcnt lgkmcnt(0)
	s_setprio 1
	s_waitcnt lgkmcnt(0)
	v_mfma_f32_16x16x32_f16 v[134:137], v[226:229], v[194:197], v[134:137]
	v_mfma_f32_16x16x32_f16 v[58:61], v[234:237], v[194:197], v[58:61]
	v_mfma_f32_16x16x32_f16 v[138:141], v[226:229], v[202:205], v[138:141]
	v_mfma_f32_16x16x32_f16 v[62:65], v[234:237], v[202:205], v[62:65]
	v_mfma_f32_16x16x32_f16 v[66:69], v[226:229], v[210:213], v[66:69]
	v_mfma_f32_16x16x32_f16 v[70:73], v[234:237], v[210:213], v[70:73]
	v_mfma_f32_16x16x32_f16 v[74:77], v[226:229], v[218:221], v[74:77]
	v_mfma_f32_16x16x32_f16 v[78:81], v[234:237], v[218:221], v[78:81]
	v_mfma_f32_16x16x32_f16 v[134:137], v[230:233], v[198:201], v[134:137]
	v_mfma_f32_16x16x32_f16 v[58:61], v[238:241], v[198:201], v[58:61]
	v_mfma_f32_16x16x32_f16 v[138:141], v[230:233], v[206:209], v[138:141]
	v_mfma_f32_16x16x32_f16 v[62:65], v[238:241], v[206:209], v[62:65]
	v_mfma_f32_16x16x32_f16 v[66:69], v[230:233], v[214:217], v[66:69]
	v_mfma_f32_16x16x32_f16 v[70:73], v[238:241], v[214:217], v[70:73]
	v_mfma_f32_16x16x32_f16 v[74:77], v[230:233], v[222:225], v[74:77]
	v_mfma_f32_16x16x32_f16 v[78:81], v[238:241], v[222:225], v[78:81]
	s_setprio 0
	s_mov_b32 m0, s17
	v_lshl_add_u64 v[242:243], v[26:27], 0, s[0:1]
	s_barrier
	ds_read_b128 v[194:197], v1 offset:16384
	ds_read_b128 v[198:201], v1 offset:17408
	ds_read_b128 v[202:205], v1 offset:18432
	ds_read_b128 v[206:209], v1 offset:19456
	ds_read_b128 v[210:213], v1 offset:20480
	ds_read_b128 v[214:217], v1 offset:21504
	ds_read_b128 v[218:221], v1 offset:22528
	ds_read_b128 v[222:225], v1 offset:23552
	global_load_lds_dwordx4 v[242:243], off
	v_lshl_add_u64 v[242:243], v[28:29], 0, s[0:1]
	s_mov_b32 m0, s10
	s_nop 0
	global_load_lds_dwordx4 v[242:243], off
	s_barrier
	s_waitcnt lgkmcnt(0)
	s_setprio 1
	s_waitcnt lgkmcnt(0)
	v_mfma_f32_16x16x32_f16 v[126:129], v[154:157], v[218:221], v[126:129]
	v_mfma_f32_16x16x32_f16 v[50:53], v[162:165], v[218:221], v[50:53]
	v_mfma_f32_16x16x32_f16 v[170:173], v[154:157], v[194:197], v[170:173]
	v_mfma_f32_16x16x32_f16 v[174:177], v[162:165], v[194:197], v[174:177]
	v_mfma_f32_16x16x32_f16 v[178:181], v[154:157], v[202:205], v[178:181]
	v_mfma_f32_16x16x32_f16 v[182:185], v[162:165], v[202:205], v[182:185]
	v_mfma_f32_16x16x32_f16 v[186:189], v[154:157], v[210:213], v[186:189]
	v_mfma_f32_16x16x32_f16 v[190:193], v[162:165], v[210:213], v[190:193]
	v_mfma_f32_16x16x32_f16 v[126:129], v[158:161], v[222:225], v[126:129]
	v_mfma_f32_16x16x32_f16 v[50:53], v[166:169], v[222:225], v[50:53]
	v_mfma_f32_16x16x32_f16 v[170:173], v[158:161], v[198:201], v[170:173]
	v_mfma_f32_16x16x32_f16 v[174:177], v[166:169], v[198:201], v[174:177]
	v_mfma_f32_16x16x32_f16 v[178:181], v[158:161], v[206:209], v[178:181]
	v_mfma_f32_16x16x32_f16 v[182:185], v[166:169], v[206:209], v[182:185]
	v_mfma_f32_16x16x32_f16 v[186:189], v[158:161], v[214:217], v[186:189]
	v_mfma_f32_16x16x32_f16 v[190:193], v[166:169], v[214:217], v[190:193]
	s_setprio 0
	s_barrier
	s_mov_b32 m0, s14
	v_lshl_add_u64 v[154:155], v[22:23], 0, s[0:1]
	global_load_lds_dwordx4 v[154:155], off
	v_lshl_add_u64 v[154:155], v[24:25], 0, s[0:1]
	s_mov_b32 m0, s11
	s_nop 0
	global_load_lds_dwordx4 v[154:155], off
	s_waitcnt vmcnt(6)
	s_barrier
	s_setprio 1
	v_mfma_f32_16x16x32_f16 v[82:85], v[234:237], v[194:197], v[82:85]
	v_mfma_f32_16x16x32_f16 v[130:133], v[226:229], v[202:205], v[130:133]
	v_mfma_f32_16x16x32_f16 v[142:145], v[234:237], v[202:205], v[142:145]
	v_mfma_f32_16x16x32_f16 v[146:149], v[226:229], v[210:213], v[146:149]
	v_mfma_f32_16x16x32_f16 v[150:153], v[234:237], v[210:213], v[150:153]
	v_mfma_f32_16x16x32_f16 v[118:121], v[226:229], v[218:221], v[118:121]
	v_mfma_f32_16x16x32_f16 v[122:125], v[234:237], v[218:221], v[122:125]
	v_mfma_f32_16x16x32_f16 v[54:57], v[226:229], v[194:197], v[54:57]
	v_mfma_f32_16x16x32_f16 v[82:85], v[238:241], v[198:201], v[82:85]
	v_mfma_f32_16x16x32_f16 v[130:133], v[230:233], v[206:209], v[130:133]
	v_mfma_f32_16x16x32_f16 v[142:145], v[238:241], v[206:209], v[142:145]
	v_mfma_f32_16x16x32_f16 v[146:149], v[230:233], v[214:217], v[146:149]
	v_mfma_f32_16x16x32_f16 v[150:153], v[238:241], v[214:217], v[150:153]
	v_mfma_f32_16x16x32_f16 v[118:121], v[230:233], v[222:225], v[118:121]
	v_mfma_f32_16x16x32_f16 v[122:125], v[238:241], v[222:225], v[122:125]
	v_mfma_f32_16x16x32_f16 v[54:57], v[230:233], v[198:201], v[54:57]
	s_setprio 0
	s_barrier
	ds_read_b128 v[154:157], v10
	ds_read_b128 v[158:161], v11
	ds_read_b128 v[162:165], v12
	ds_read_b128 v[166:169], v13
	s_mov_b32 m0, s20
	v_lshl_add_u64 v[226:227], v[18:19], 0, s[0:1]
	ds_read_b128 v[194:197], v1 offset:32768
	ds_read_b128 v[198:201], v1 offset:33792
	ds_read_b128 v[202:205], v1 offset:34816
	ds_read_b128 v[206:209], v1 offset:35840
	ds_read_b128 v[210:213], v1 offset:36864
	ds_read_b128 v[214:217], v1 offset:37888
	ds_read_b128 v[218:221], v1 offset:38912
	ds_read_b128 v[222:225], v1 offset:39936
	global_load_lds_dwordx4 v[226:227], off
	v_lshl_add_u64 v[226:227], v[20:21], 0, s[0:1]
	s_mov_b32 m0, s18
	s_nop 0
	global_load_lds_dwordx4 v[226:227], off
	s_waitcnt lgkmcnt(8)
	s_barrier
	s_waitcnt lgkmcnt(0)
	s_setprio 1
	s_waitcnt lgkmcnt(0)
	v_mfma_f32_16x16x32_f16 v[86:89], v[154:157], v[194:197], v[86:89]
	v_mfma_f32_16x16x32_f16 v[90:93], v[162:165], v[194:197], v[90:93]
	v_mfma_f32_16x16x32_f16 v[94:97], v[154:157], v[202:205], v[94:97]
	v_mfma_f32_16x16x32_f16 v[98:101], v[162:165], v[202:205], v[98:101]
	v_mfma_f32_16x16x32_f16 v[102:105], v[154:157], v[210:213], v[102:105]
	v_mfma_f32_16x16x32_f16 v[106:109], v[162:165], v[210:213], v[106:109]
	v_mfma_f32_16x16x32_f16 v[110:113], v[154:157], v[218:221], v[110:113]
	v_mfma_f32_16x16x32_f16 v[86:89], v[158:161], v[198:201], v[86:89]
	v_mfma_f32_16x16x32_f16 v[90:93], v[166:169], v[198:201], v[90:93]
	v_mfma_f32_16x16x32_f16 v[94:97], v[158:161], v[206:209], v[94:97]
	v_mfma_f32_16x16x32_f16 v[98:101], v[166:169], v[206:209], v[98:101]
	v_mfma_f32_16x16x32_f16 v[102:105], v[158:161], v[214:217], v[102:105]
	v_mfma_f32_16x16x32_f16 v[106:109], v[166:169], v[214:217], v[106:109]
	v_mfma_f32_16x16x32_f16 v[110:113], v[158:161], v[222:225], v[110:113]
	v_mfma_f32_16x16x32_f16 v[114:117], v[162:165], v[218:221], v[114:117]
	v_mfma_f32_16x16x32_f16 v[114:117], v[166:169], v[222:225], v[114:117]
	s_setprio 0
	s_barrier
	s_mov_b64 s[0:1], 0x280
	v_readfirstlane_b32 s10, v48
	v_lshl_add_u64 v[242:243], v[30:31], 0, s[0:1]
	s_mov_b32 m0, s10
	v_readfirstlane_b32 s2, v49
	ds_read_b128 v[226:229], v14
	ds_read_b128 v[230:233], v15
	ds_read_b128 v[234:237], v16
	ds_read_b128 v[238:241], v17
	global_load_lds_dwordx4 v[242:243], off
	v_lshl_add_u64 v[242:243], v[32:33], 0, s[0:1]
	s_mov_b32 m0, s2
	s_nop 0
	global_load_lds_dwordx4 v[242:243], off
	s_barrier
	s_waitcnt lgkmcnt(0)
	s_setprio 1
	s_waitcnt lgkmcnt(0)
	v_mfma_f32_16x16x32_f16 v[134:137], v[226:229], v[194:197], v[134:137]
	v_mfma_f32_16x16x32_f16 v[58:61], v[234:237], v[194:197], v[58:61]
	v_mfma_f32_16x16x32_f16 v[138:141], v[226:229], v[202:205], v[138:141]
	v_mfma_f32_16x16x32_f16 v[62:65], v[234:237], v[202:205], v[62:65]
	v_mfma_f32_16x16x32_f16 v[66:69], v[226:229], v[210:213], v[66:69]
	v_mfma_f32_16x16x32_f16 v[70:73], v[234:237], v[210:213], v[70:73]
	v_mfma_f32_16x16x32_f16 v[74:77], v[226:229], v[218:221], v[74:77]
	v_mfma_f32_16x16x32_f16 v[78:81], v[234:237], v[218:221], v[78:81]
	v_mfma_f32_16x16x32_f16 v[134:137], v[230:233], v[198:201], v[134:137]
	v_mfma_f32_16x16x32_f16 v[58:61], v[238:241], v[198:201], v[58:61]
	v_mfma_f32_16x16x32_f16 v[138:141], v[230:233], v[206:209], v[138:141]
	v_mfma_f32_16x16x32_f16 v[62:65], v[238:241], v[206:209], v[62:65]
	v_mfma_f32_16x16x32_f16 v[66:69], v[230:233], v[214:217], v[66:69]
	v_mfma_f32_16x16x32_f16 v[70:73], v[238:241], v[214:217], v[70:73]
	v_mfma_f32_16x16x32_f16 v[74:77], v[230:233], v[222:225], v[74:77]
	v_mfma_f32_16x16x32_f16 v[78:81], v[238:241], v[222:225], v[78:81]
	s_setprio 0
	v_readfirstlane_b32 s11, v46
	v_lshl_add_u64 v[48:49], v[26:27], 0, s[0:1]
	s_mov_b32 m0, s11
	v_readfirstlane_b32 s3, v47
	s_barrier
	ds_read_b128 v[194:197], v1 offset:49152
	ds_read_b128 v[198:201], v1 offset:50176
	ds_read_b128 v[202:205], v1 offset:51200
	ds_read_b128 v[206:209], v1 offset:52224
	ds_read_b128 v[210:213], v1 offset:53248
	ds_read_b128 v[214:217], v1 offset:54272
	ds_read_b128 v[218:221], v1 offset:55296
	ds_read_b128 v[222:225], v1 offset:56320
	global_load_lds_dwordx4 v[48:49], off
	v_lshl_add_u64 v[48:49], v[28:29], 0, s[0:1]
	s_mov_b32 m0, s3
	s_nop 0
	global_load_lds_dwordx4 v[48:49], off
	s_barrier
	s_waitcnt lgkmcnt(0)
	s_setprio 1
	s_waitcnt lgkmcnt(0)
	v_mfma_f32_16x16x32_f16 v[126:129], v[154:157], v[218:221], v[126:129]
	v_mfma_f32_16x16x32_f16 v[50:53], v[162:165], v[218:221], v[50:53]
	v_mfma_f32_16x16x32_f16 v[46:49], v[154:157], v[194:197], v[170:173]
	v_mfma_f32_16x16x32_f16 v[170:173], v[162:165], v[194:197], v[174:177]
	v_mfma_f32_16x16x32_f16 v[174:177], v[154:157], v[202:205], v[178:181]
	v_mfma_f32_16x16x32_f16 v[178:181], v[162:165], v[202:205], v[182:185]
	v_mfma_f32_16x16x32_f16 v[182:185], v[154:157], v[210:213], v[186:189]
	v_mfma_f32_16x16x32_f16 v[186:189], v[162:165], v[210:213], v[190:193]
	v_mfma_f32_16x16x32_f16 v[126:129], v[158:161], v[222:225], v[126:129]
	v_mfma_f32_16x16x32_f16 v[50:53], v[166:169], v[222:225], v[50:53]
	v_mfma_f32_16x16x32_f16 v[46:49], v[158:161], v[198:201], v[46:49]
	v_mfma_f32_16x16x32_f16 v[170:173], v[166:169], v[198:201], v[170:173]
	v_mfma_f32_16x16x32_f16 v[174:177], v[158:161], v[206:209], v[174:177]
	v_mfma_f32_16x16x32_f16 v[178:181], v[166:169], v[206:209], v[178:181]
	v_mfma_f32_16x16x32_f16 v[182:185], v[158:161], v[214:217], v[182:185]
	v_mfma_f32_16x16x32_f16 v[186:189], v[166:169], v[214:217], v[186:189]
	s_setprio 0
	s_barrier
	v_readfirstlane_b32 s5, v37
	v_lshl_add_u64 v[154:155], v[22:23], 0, s[0:1]
	s_mov_b32 m0, s5
	v_readfirstlane_b32 s4, v39
	global_load_lds_dwordx4 v[154:155], off
	v_lshl_add_u64 v[154:155], v[24:25], 0, s[0:1]
	s_mov_b32 m0, s4
	s_nop 0
	global_load_lds_dwordx4 v[154:155], off
	s_waitcnt vmcnt(6)
	s_barrier
	s_setprio 1
	v_mfma_f32_16x16x32_f16 v[82:85], v[234:237], v[194:197], v[82:85]
	v_mfma_f32_16x16x32_f16 v[130:133], v[226:229], v[202:205], v[130:133]
	v_mfma_f32_16x16x32_f16 v[142:145], v[234:237], v[202:205], v[142:145]
	v_mfma_f32_16x16x32_f16 v[146:149], v[226:229], v[210:213], v[146:149]
	v_mfma_f32_16x16x32_f16 v[150:153], v[234:237], v[210:213], v[150:153]
	v_mfma_f32_16x16x32_f16 v[118:121], v[226:229], v[218:221], v[118:121]
	v_mfma_f32_16x16x32_f16 v[122:125], v[234:237], v[218:221], v[122:125]
	v_mfma_f32_16x16x32_f16 v[54:57], v[226:229], v[194:197], v[54:57]
	v_mfma_f32_16x16x32_f16 v[82:85], v[238:241], v[198:201], v[82:85]
	v_mfma_f32_16x16x32_f16 v[130:133], v[230:233], v[206:209], v[130:133]
	v_mfma_f32_16x16x32_f16 v[142:145], v[238:241], v[206:209], v[142:145]
	v_mfma_f32_16x16x32_f16 v[146:149], v[230:233], v[214:217], v[146:149]
	v_mfma_f32_16x16x32_f16 v[150:153], v[238:241], v[214:217], v[150:153]
	v_mfma_f32_16x16x32_f16 v[118:121], v[230:233], v[222:225], v[118:121]
	v_mfma_f32_16x16x32_f16 v[122:125], v[238:241], v[222:225], v[122:125]
	v_mfma_f32_16x16x32_f16 v[54:57], v[230:233], v[198:201], v[54:57]
	s_setprio 0
	s_barrier
	ds_read_b128 v[154:157], v2
	ds_read_b128 v[158:161], v3
	ds_read_b128 v[162:165], v4
	ds_read_b128 v[166:169], v5
	v_readfirstlane_b32 s14, v38
	v_lshl_add_u64 v[190:191], v[18:19], 0, s[0:1]
	s_mov_b32 m0, s14
	v_readfirstlane_b32 s7, v40
	global_load_lds_dwordx4 v[190:191], off
	v_lshl_add_u64 v[38:39], v[20:21], 0, s[0:1]
	s_mov_b32 m0, s7
	s_nop 0
	global_load_lds_dwordx4 v[38:39], off
	ds_read_b128 v[190:193], v1
	ds_read_b128 v[194:197], v1 offset:1024
	ds_read_b128 v[198:201], v1 offset:2048
	ds_read_b128 v[202:205], v1 offset:3072
	ds_read_b128 v[206:209], v1 offset:4096
	ds_read_b128 v[210:213], v1 offset:5120
	ds_read_b128 v[214:217], v1 offset:6144
	ds_read_b128 v[218:221], v1 offset:7168
	s_waitcnt lgkmcnt(8)
	s_barrier
	s_waitcnt lgkmcnt(0)
	s_setprio 1
	s_waitcnt lgkmcnt(0)
	v_mfma_f32_16x16x32_f16 v[86:89], v[154:157], v[190:193], v[86:89]
	v_mfma_f32_16x16x32_f16 v[90:93], v[162:165], v[190:193], v[90:93]
	v_mfma_f32_16x16x32_f16 v[94:97], v[154:157], v[198:201], v[94:97]
	v_mfma_f32_16x16x32_f16 v[98:101], v[162:165], v[198:201], v[98:101]
	v_mfma_f32_16x16x32_f16 v[102:105], v[154:157], v[206:209], v[102:105]
	v_mfma_f32_16x16x32_f16 v[106:109], v[162:165], v[206:209], v[106:109]
	v_mfma_f32_16x16x32_f16 v[110:113], v[154:157], v[214:217], v[110:113]
	v_mfma_f32_16x16x32_f16 v[86:89], v[158:161], v[194:197], v[86:89]
	v_mfma_f32_16x16x32_f16 v[90:93], v[166:169], v[194:197], v[90:93]
	v_mfma_f32_16x16x32_f16 v[94:97], v[158:161], v[202:205], v[94:97]
	v_mfma_f32_16x16x32_f16 v[98:101], v[166:169], v[202:205], v[98:101]
	v_mfma_f32_16x16x32_f16 v[102:105], v[158:161], v[210:213], v[102:105]
	v_mfma_f32_16x16x32_f16 v[106:109], v[166:169], v[210:213], v[106:109]
	v_mfma_f32_16x16x32_f16 v[110:113], v[158:161], v[218:221], v[110:113]
	v_mfma_f32_16x16x32_f16 v[114:117], v[162:165], v[214:217], v[114:117]
	v_mfma_f32_16x16x32_f16 v[114:117], v[166:169], v[218:221], v[114:117]
	s_setprio 0
	s_barrier
	s_mov_b64 s[0:1], 0x300
	v_readfirstlane_b32 s15, v36
	v_lshl_add_u64 v[38:39], v[30:31], 0, s[0:1]
	s_mov_b32 m0, s15
	v_readfirstlane_b32 s15, v41
	ds_read_b128 v[222:225], v6
	ds_read_b128 v[226:229], v7
	ds_read_b128 v[230:233], v8
	ds_read_b128 v[234:237], v9
	global_load_lds_dwordx4 v[38:39], off
	v_lshl_add_u64 v[36:37], v[32:33], 0, s[0:1]
	s_mov_b32 m0, s15
	s_nop 0
	global_load_lds_dwordx4 v[36:37], off
	s_barrier
	s_waitcnt lgkmcnt(0)
	s_setprio 1
	s_waitcnt lgkmcnt(0)
	v_mfma_f32_16x16x32_f16 v[36:39], v[222:225], v[190:193], v[134:137]
	v_mfma_f32_16x16x32_f16 v[58:61], v[230:233], v[190:193], v[58:61]
	v_mfma_f32_16x16x32_f16 v[134:137], v[222:225], v[198:201], v[138:141]
	v_mfma_f32_16x16x32_f16 v[62:65], v[230:233], v[198:201], v[62:65]
	v_mfma_f32_16x16x32_f16 v[66:69], v[222:225], v[206:209], v[66:69]
	v_mfma_f32_16x16x32_f16 v[70:73], v[230:233], v[206:209], v[70:73]
	v_mfma_f32_16x16x32_f16 v[74:77], v[222:225], v[214:217], v[74:77]
	v_mfma_f32_16x16x32_f16 v[78:81], v[230:233], v[214:217], v[78:81]
	v_mfma_f32_16x16x32_f16 v[36:39], v[226:229], v[194:197], v[36:39]
	v_mfma_f32_16x16x32_f16 v[58:61], v[234:237], v[194:197], v[58:61]
	v_mfma_f32_16x16x32_f16 v[134:137], v[226:229], v[202:205], v[134:137]
	v_mfma_f32_16x16x32_f16 v[62:65], v[234:237], v[202:205], v[62:65]
	v_mfma_f32_16x16x32_f16 v[66:69], v[226:229], v[210:213], v[66:69]
	v_mfma_f32_16x16x32_f16 v[70:73], v[234:237], v[210:213], v[70:73]
	v_mfma_f32_16x16x32_f16 v[74:77], v[226:229], v[218:221], v[74:77]
	v_mfma_f32_16x16x32_f16 v[78:81], v[234:237], v[218:221], v[78:81]
	s_setprio 0
	v_readfirstlane_b32 s15, v35
	v_lshl_add_u64 v[40:41], v[26:27], 0, s[0:1]
	s_mov_b32 m0, s15
	v_readfirstlane_b32 s15, v42
	s_barrier
	ds_read_b128 v[138:141], v1 offset:16384
	ds_read_b128 v[190:193], v1 offset:17408
	ds_read_b128 v[194:197], v1 offset:18432
	ds_read_b128 v[198:201], v1 offset:19456
	ds_read_b128 v[202:205], v1 offset:20480
	ds_read_b128 v[206:209], v1 offset:21504
	ds_read_b128 v[210:213], v1 offset:22528
	ds_read_b128 v[214:217], v1 offset:23552
	global_load_lds_dwordx4 v[40:41], off
	v_lshl_add_u64 v[40:41], v[28:29], 0, s[0:1]
	s_mov_b32 m0, s15
	s_nop 0
	global_load_lds_dwordx4 v[40:41], off
	s_barrier
	s_waitcnt lgkmcnt(0)
	s_setprio 1
	s_waitcnt lgkmcnt(0)
	v_mfma_f32_16x16x32_f16 v[126:129], v[154:157], v[210:213], v[126:129]
	v_mfma_f32_16x16x32_f16 v[50:53], v[162:165], v[210:213], v[50:53]
	v_mfma_f32_16x16x32_f16 v[46:49], v[154:157], v[138:141], v[46:49]
	v_mfma_f32_16x16x32_f16 v[170:173], v[162:165], v[138:141], v[170:173]
	v_mfma_f32_16x16x32_f16 v[174:177], v[154:157], v[194:197], v[174:177]
	v_mfma_f32_16x16x32_f16 v[178:181], v[162:165], v[194:197], v[178:181]
	v_mfma_f32_16x16x32_f16 v[182:185], v[154:157], v[202:205], v[182:185]
	v_mfma_f32_16x16x32_f16 v[186:189], v[162:165], v[202:205], v[186:189]
	v_mfma_f32_16x16x32_f16 v[126:129], v[158:161], v[214:217], v[126:129]
	v_mfma_f32_16x16x32_f16 v[50:53], v[166:169], v[214:217], v[50:53]
	v_mfma_f32_16x16x32_f16 v[46:49], v[158:161], v[190:193], v[46:49]
	v_mfma_f32_16x16x32_f16 v[170:173], v[166:169], v[190:193], v[170:173]
	v_mfma_f32_16x16x32_f16 v[174:177], v[158:161], v[198:201], v[174:177]
	v_mfma_f32_16x16x32_f16 v[178:181], v[166:169], v[198:201], v[178:181]
	v_mfma_f32_16x16x32_f16 v[182:185], v[158:161], v[206:209], v[182:185]
	v_mfma_f32_16x16x32_f16 v[186:189], v[166:169], v[206:209], v[186:189]
	s_setprio 0
	s_barrier
	v_readfirstlane_b32 s15, v34
	v_lshl_add_u64 v[40:41], v[22:23], 0, s[0:1]
	s_mov_b32 m0, s15
	v_readfirstlane_b32 s15, v43
	global_load_lds_dwordx4 v[40:41], off
	v_lshl_add_u64 v[34:35], v[24:25], 0, s[0:1]
	s_mov_b32 m0, s15
	s_nop 0
	global_load_lds_dwordx4 v[34:35], off
	s_waitcnt vmcnt(6)
	s_barrier
	s_setprio 1
	v_mfma_f32_16x16x32_f16 v[40:43], v[222:225], v[138:141], v[54:57]
	v_mfma_f32_16x16x32_f16 v[54:57], v[230:233], v[138:141], v[82:85]
	v_mfma_f32_16x16x32_f16 v[82:85], v[222:225], v[194:197], v[130:133]
	v_mfma_f32_16x16x32_f16 v[130:133], v[230:233], v[194:197], v[142:145]
	v_mfma_f32_16x16x32_f16 v[138:141], v[222:225], v[202:205], v[146:149]
	v_mfma_f32_16x16x32_f16 v[142:145], v[230:233], v[202:205], v[150:153]
	v_mfma_f32_16x16x32_f16 v[118:121], v[222:225], v[210:213], v[118:121]
	v_mfma_f32_16x16x32_f16 v[122:125], v[230:233], v[210:213], v[122:125]
	v_mfma_f32_16x16x32_f16 v[82:85], v[226:229], v[198:201], v[82:85]
	v_mfma_f32_16x16x32_f16 v[130:133], v[234:237], v[198:201], v[130:133]
	v_mfma_f32_16x16x32_f16 v[138:141], v[226:229], v[206:209], v[138:141]
	v_mfma_f32_16x16x32_f16 v[142:145], v[234:237], v[206:209], v[142:145]
	v_mfma_f32_16x16x32_f16 v[118:121], v[226:229], v[214:217], v[118:121]
	v_mfma_f32_16x16x32_f16 v[122:125], v[234:237], v[214:217], v[122:125]
	v_mfma_f32_16x16x32_f16 v[40:43], v[226:229], v[190:193], v[40:43]
	v_mfma_f32_16x16x32_f16 v[54:57], v[234:237], v[190:193], v[54:57]
	s_setprio 0
	s_barrier
	ds_read_b128 v[146:149], v10
	ds_read_b128 v[150:153], v11
	ds_read_b128 v[154:157], v12
	ds_read_b128 v[158:161], v13
	v_readfirstlane_b32 s15, v44
	v_lshl_add_u64 v[34:35], v[18:19], 0, s[0:1]
	s_mov_b32 m0, s15
	ds_read_b128 v[162:165], v1 offset:32768
	ds_read_b128 v[166:169], v1 offset:33792
	ds_read_b128 v[190:193], v1 offset:34816
	ds_read_b128 v[194:197], v1 offset:35840
	ds_read_b128 v[198:201], v1 offset:36864
	ds_read_b128 v[202:205], v1 offset:37888
	ds_read_b128 v[206:209], v1 offset:38912
	ds_read_b128 v[210:213], v1 offset:39936
	global_load_lds_dwordx4 v[34:35], off
	v_lshl_add_u64 v[34:35], v[20:21], 0, s[0:1]
	v_readfirstlane_b32 s0, v45
	s_mov_b32 m0, s0
	s_nop 0
	global_load_lds_dwordx4 v[34:35], off
	s_waitcnt lgkmcnt(8)
	s_barrier
	s_waitcnt lgkmcnt(0)
	s_setprio 1
	s_waitcnt lgkmcnt(0)
	v_mfma_f32_16x16x32_f16 v[86:89], v[146:149], v[162:165], v[86:89]
	v_mfma_f32_16x16x32_f16 v[90:93], v[154:157], v[162:165], v[90:93]
	v_mfma_f32_16x16x32_f16 v[94:97], v[146:149], v[190:193], v[94:97]
	v_mfma_f32_16x16x32_f16 v[98:101], v[154:157], v[190:193], v[98:101]
	v_mfma_f32_16x16x32_f16 v[102:105], v[146:149], v[198:201], v[102:105]
	v_mfma_f32_16x16x32_f16 v[106:109], v[154:157], v[198:201], v[106:109]
	v_mfma_f32_16x16x32_f16 v[110:113], v[146:149], v[206:209], v[110:113]
	v_mfma_f32_16x16x32_f16 v[86:89], v[150:153], v[166:169], v[86:89]
	v_mfma_f32_16x16x32_f16 v[90:93], v[158:161], v[166:169], v[90:93]
	v_mfma_f32_16x16x32_f16 v[94:97], v[150:153], v[194:197], v[94:97]
	v_mfma_f32_16x16x32_f16 v[98:101], v[158:161], v[194:197], v[98:101]
	v_mfma_f32_16x16x32_f16 v[102:105], v[150:153], v[202:205], v[102:105]
	v_mfma_f32_16x16x32_f16 v[106:109], v[158:161], v[202:205], v[106:109]
	v_mfma_f32_16x16x32_f16 v[110:113], v[150:153], v[210:213], v[110:113]
	v_mfma_f32_16x16x32_f16 v[114:117], v[154:157], v[206:209], v[114:117]
	v_mfma_f32_16x16x32_f16 v[114:117], v[158:161], v[210:213], v[114:117]
	s_setprio 0
	s_barrier
	s_mov_b64 s[0:1], 0x380
	s_mov_b32 m0, s10
	v_lshl_add_u64 v[30:31], v[30:31], 0, s[0:1]
	ds_read_b128 v[214:217], v14
	ds_read_b128 v[218:221], v15
	ds_read_b128 v[222:225], v16
	ds_read_b128 v[226:229], v17
	global_load_lds_dwordx4 v[30:31], off
	v_lshl_add_u64 v[30:31], v[32:33], 0, s[0:1]
	s_mov_b32 m0, s2
	s_nop 0
	global_load_lds_dwordx4 v[30:31], off
	s_barrier
	s_waitcnt lgkmcnt(0)
	s_setprio 1
	s_waitcnt lgkmcnt(0)
	v_mfma_f32_16x16x32_f16 v[30:33], v[214:217], v[162:165], v[36:39]
	v_mfma_f32_16x16x32_f16 v[34:37], v[222:225], v[162:165], v[58:61]
	v_mfma_f32_16x16x32_f16 v[58:61], v[214:217], v[190:193], v[134:137]
	v_mfma_f32_16x16x32_f16 v[62:65], v[222:225], v[190:193], v[62:65]
	v_mfma_f32_16x16x32_f16 v[66:69], v[214:217], v[198:201], v[66:69]
	v_mfma_f32_16x16x32_f16 v[70:73], v[222:225], v[198:201], v[70:73]
	v_mfma_f32_16x16x32_f16 v[74:77], v[214:217], v[206:209], v[74:77]
	v_mfma_f32_16x16x32_f16 v[78:81], v[222:225], v[206:209], v[78:81]
	v_mfma_f32_16x16x32_f16 v[34:37], v[226:229], v[166:169], v[34:37]
	v_mfma_f32_16x16x32_f16 v[58:61], v[218:221], v[194:197], v[58:61]
	v_mfma_f32_16x16x32_f16 v[62:65], v[226:229], v[194:197], v[62:65]
	v_mfma_f32_16x16x32_f16 v[66:69], v[218:221], v[202:205], v[66:69]
	v_mfma_f32_16x16x32_f16 v[70:73], v[226:229], v[202:205], v[70:73]
	v_mfma_f32_16x16x32_f16 v[74:77], v[218:221], v[210:213], v[74:77]
	v_mfma_f32_16x16x32_f16 v[78:81], v[226:229], v[210:213], v[78:81]
	v_mfma_f32_16x16x32_f16 v[30:33], v[218:221], v[166:169], v[30:33]
	s_setprio 0
	s_mov_b32 m0, s11
	v_lshl_add_u64 v[26:27], v[26:27], 0, s[0:1]
	s_barrier
	ds_read_b128 v[134:137], v1 offset:49152
	ds_read_b128 v[162:165], v1 offset:50176
	ds_read_b128 v[166:169], v1 offset:51200
	ds_read_b128 v[190:193], v1 offset:52224
	ds_read_b128 v[194:197], v1 offset:53248
	ds_read_b128 v[198:201], v1 offset:54272
	ds_read_b128 v[202:205], v1 offset:55296
	ds_read_b128 v[206:209], v1 offset:56320
	global_load_lds_dwordx4 v[26:27], off
	v_lshl_add_u64 v[26:27], v[28:29], 0, s[0:1]
	s_mov_b32 m0, s3
	s_nop 0
	global_load_lds_dwordx4 v[26:27], off
	s_barrier
	s_waitcnt lgkmcnt(0)
	s_setprio 1
	s_waitcnt lgkmcnt(0)
	v_mfma_f32_16x16x32_f16 v[26:29], v[146:149], v[134:137], v[46:49]
	v_mfma_f32_16x16x32_f16 v[126:129], v[146:149], v[202:205], v[126:129]
	v_mfma_f32_16x16x32_f16 v[48:51], v[154:157], v[202:205], v[50:53]
	v_mfma_f32_16x16x32_f16 v[44:47], v[154:157], v[134:137], v[170:173]
	v_mfma_f32_16x16x32_f16 v[170:173], v[146:149], v[166:169], v[174:177]
	v_mfma_f32_16x16x32_f16 v[174:177], v[154:157], v[166:169], v[178:181]
	v_mfma_f32_16x16x32_f16 v[178:181], v[146:149], v[194:197], v[182:185]
	v_mfma_f32_16x16x32_f16 v[182:185], v[154:157], v[194:197], v[186:189]
	v_mfma_f32_16x16x32_f16 v[126:129], v[150:153], v[206:209], v[126:129]
	v_mfma_f32_16x16x32_f16 v[48:51], v[158:161], v[206:209], v[48:51]
	v_mfma_f32_16x16x32_f16 v[26:29], v[150:153], v[162:165], v[26:29]
	v_mfma_f32_16x16x32_f16 v[44:47], v[158:161], v[162:165], v[44:47]
	v_mfma_f32_16x16x32_f16 v[170:173], v[150:153], v[190:193], v[170:173]
	v_mfma_f32_16x16x32_f16 v[174:177], v[158:161], v[190:193], v[174:177]
	v_mfma_f32_16x16x32_f16 v[178:181], v[150:153], v[198:201], v[178:181]
	v_mfma_f32_16x16x32_f16 v[182:185], v[158:161], v[198:201], v[182:185]
	s_setprio 0
	s_barrier
	s_mov_b32 m0, s5
	v_lshl_add_u64 v[22:23], v[22:23], 0, s[0:1]
	global_load_lds_dwordx4 v[22:23], off
	v_lshl_add_u64 v[22:23], v[24:25], 0, s[0:1]
	s_mov_b32 m0, s4
	s_nop 0
	global_load_lds_dwordx4 v[22:23], off
	s_waitcnt vmcnt(6)
	s_barrier
	s_setprio 1
	v_mfma_f32_16x16x32_f16 v[22:25], v[214:217], v[134:137], v[40:43]
	v_mfma_f32_16x16x32_f16 v[38:41], v[222:225], v[134:137], v[54:57]
	v_mfma_f32_16x16x32_f16 v[52:55], v[214:217], v[166:169], v[82:85]
	v_mfma_f32_16x16x32_f16 v[82:85], v[222:225], v[166:169], v[130:133]
	v_mfma_f32_16x16x32_f16 v[130:133], v[214:217], v[194:197], v[138:141]
	v_mfma_f32_16x16x32_f16 v[134:137], v[222:225], v[194:197], v[142:145]
	v_mfma_f32_16x16x32_f16 v[118:121], v[214:217], v[202:205], v[118:121]
	v_mfma_f32_16x16x32_f16 v[122:125], v[222:225], v[202:205], v[122:125]
	v_mfma_f32_16x16x32_f16 v[52:55], v[218:221], v[190:193], v[52:55]
	v_mfma_f32_16x16x32_f16 v[82:85], v[226:229], v[190:193], v[82:85]
	v_mfma_f32_16x16x32_f16 v[130:133], v[218:221], v[198:201], v[130:133]
	v_mfma_f32_16x16x32_f16 v[134:137], v[226:229], v[198:201], v[134:137]
	v_mfma_f32_16x16x32_f16 v[118:121], v[218:221], v[206:209], v[118:121]
	v_mfma_f32_16x16x32_f16 v[122:125], v[226:229], v[206:209], v[122:125]
	v_mfma_f32_16x16x32_f16 v[22:25], v[218:221], v[162:165], v[22:25]
	v_mfma_f32_16x16x32_f16 v[38:41], v[226:229], v[162:165], v[38:41]
	s_setprio 0
	s_mov_b32 m0, s14
	v_lshl_add_u64 v[18:19], v[18:19], 0, s[0:1]
	s_barrier
	ds_read_b128 v[138:141], v2
	ds_read_b128 v[142:145], v3
	ds_read_b128 v[146:149], v4
	ds_read_b128 v[2:5], v5
	global_load_lds_dwordx4 v[18:19], off
	v_lshl_add_u64 v[18:19], v[20:21], 0, s[0:1]
	s_mov_b32 m0, s7
	s_nop 0
	global_load_lds_dwordx4 v[18:19], off
	ds_read_b128 v[18:21], v1
	ds_read_b128 v[150:153], v1 offset:1024
	ds_read_b128 v[154:157], v1 offset:2048
	ds_read_b128 v[158:161], v1 offset:3072
	ds_read_b128 v[162:165], v1 offset:4096
	ds_read_b128 v[166:169], v1 offset:5120
	ds_read_b128 v[186:189], v1 offset:6144
	ds_read_b128 v[190:193], v1 offset:7168
	s_barrier
	s_waitcnt lgkmcnt(0)
	s_setprio 1
	s_waitcnt lgkmcnt(0)
	v_mfma_f32_16x16x32_f16 v[86:89], v[138:141], v[18:21], v[86:89]
	v_mfma_f32_16x16x32_f16 v[90:93], v[146:149], v[18:21], v[90:93]
	v_mfma_f32_16x16x32_f16 v[94:97], v[138:141], v[154:157], v[94:97]
	v_mfma_f32_16x16x32_f16 v[98:101], v[146:149], v[154:157], v[98:101]
	v_mfma_f32_16x16x32_f16 v[102:105], v[138:141], v[162:165], v[102:105]
	v_mfma_f32_16x16x32_f16 v[106:109], v[146:149], v[162:165], v[106:109]
	v_mfma_f32_16x16x32_f16 v[110:113], v[138:141], v[186:189], v[110:113]
	v_mfma_f32_16x16x32_f16 v[86:89], v[142:145], v[150:153], v[86:89]
	v_mfma_f32_16x16x32_f16 v[90:93], v[2:5], v[150:153], v[90:93]
	v_mfma_f32_16x16x32_f16 v[94:97], v[142:145], v[158:161], v[94:97]
	v_mfma_f32_16x16x32_f16 v[98:101], v[2:5], v[158:161], v[98:101]
	v_mfma_f32_16x16x32_f16 v[102:105], v[142:145], v[166:169], v[102:105]
	v_mfma_f32_16x16x32_f16 v[106:109], v[2:5], v[166:169], v[106:109]
	v_mfma_f32_16x16x32_f16 v[110:113], v[142:145], v[190:193], v[110:113]
	v_mfma_f32_16x16x32_f16 v[114:117], v[146:149], v[186:189], v[114:117]
	v_mfma_f32_16x16x32_f16 v[114:117], v[2:5], v[190:193], v[114:117]
	s_setprio 0
	s_barrier
	ds_read_b128 v[194:197], v6
	ds_read_b128 v[198:201], v7
	ds_read_b128 v[202:205], v8
	ds_read_b128 v[6:9], v9
	s_barrier
	s_waitcnt lgkmcnt(0)
	s_setprio 1
	s_waitcnt lgkmcnt(0)
	v_mfma_f32_16x16x32_f16 v[30:33], v[194:197], v[18:21], v[30:33]
	v_mfma_f32_16x16x32_f16 v[18:21], v[202:205], v[18:21], v[34:37]
	v_mfma_f32_16x16x32_f16 v[34:37], v[194:197], v[154:157], v[58:61]
	v_mfma_f32_16x16x32_f16 v[56:59], v[202:205], v[154:157], v[62:65]
	v_mfma_f32_16x16x32_f16 v[60:63], v[194:197], v[162:165], v[66:69]
	v_mfma_f32_16x16x32_f16 v[64:67], v[202:205], v[162:165], v[70:73]
	v_mfma_f32_16x16x32_f16 v[68:71], v[194:197], v[186:189], v[74:77]
	v_mfma_f32_16x16x32_f16 v[72:75], v[202:205], v[186:189], v[78:81]
	v_mfma_f32_16x16x32_f16 v[34:37], v[198:201], v[158:161], v[34:37]
	v_mfma_f32_16x16x32_f16 v[56:59], v[6:9], v[158:161], v[56:59]
	v_mfma_f32_16x16x32_f16 v[60:63], v[198:201], v[166:169], v[60:63]
	v_mfma_f32_16x16x32_f16 v[64:67], v[6:9], v[166:169], v[64:67]
	v_mfma_f32_16x16x32_f16 v[68:71], v[198:201], v[190:193], v[68:71]
	v_mfma_f32_16x16x32_f16 v[72:75], v[6:9], v[190:193], v[72:75]
	v_mfma_f32_16x16x32_f16 v[30:33], v[198:201], v[150:153], v[30:33]
	v_mfma_f32_16x16x32_f16 v[18:21], v[6:9], v[150:153], v[18:21]
	s_setprio 0
	s_barrier
	ds_read_b128 v[76:79], v1 offset:16384
	ds_read_b128 v[150:153], v1 offset:17408
	ds_read_b128 v[154:157], v1 offset:18432
	ds_read_b128 v[158:161], v1 offset:19456
	ds_read_b128 v[162:165], v1 offset:20480
	ds_read_b128 v[166:169], v1 offset:21504
	ds_read_b128 v[186:189], v1 offset:22528
	ds_read_b128 v[190:193], v1 offset:23552
	s_waitcnt vmcnt(4)
	s_barrier
	s_waitcnt lgkmcnt(0)
	s_setprio 1
	s_waitcnt lgkmcnt(0)
	v_mfma_f32_16x16x32_f16 v[42:45], v[146:149], v[76:79], v[44:47]
	v_mfma_f32_16x16x32_f16 v[174:177], v[146:149], v[154:157], v[174:177]
	v_mfma_f32_16x16x32_f16 v[182:185], v[146:149], v[162:165], v[182:185]
	v_mfma_f32_16x16x32_f16 v[46:49], v[146:149], v[186:189], v[48:51]
	v_mfma_f32_16x16x32_f16 v[26:29], v[138:141], v[76:79], v[26:29]
	v_mfma_f32_16x16x32_f16 v[42:45], v[2:5], v[150:153], v[42:45]
	v_mfma_f32_16x16x32_f16 v[170:173], v[138:141], v[154:157], v[170:173]
	v_mfma_f32_16x16x32_f16 v[174:177], v[2:5], v[158:161], v[174:177]
	v_mfma_f32_16x16x32_f16 v[178:181], v[138:141], v[162:165], v[178:181]
	v_mfma_f32_16x16x32_f16 v[182:185], v[2:5], v[166:169], v[182:185]
	v_mfma_f32_16x16x32_f16 v[126:129], v[138:141], v[186:189], v[126:129]
	v_mfma_f32_16x16x32_f16 v[2:5], v[2:5], v[190:193], v[46:49]
	v_mfma_f32_16x16x32_f16 v[26:29], v[142:145], v[150:153], v[26:29]
	v_mfma_f32_16x16x32_f16 v[170:173], v[142:145], v[158:161], v[170:173]
	v_mfma_f32_16x16x32_f16 v[178:181], v[142:145], v[166:169], v[178:181]
	v_mfma_f32_16x16x32_f16 v[206:209], v[142:145], v[190:193], v[126:129]
	s_setprio 0
	s_setprio 1
	v_mfma_f32_16x16x32_f16 v[46:49], v[194:197], v[154:157], v[52:55]
	v_mfma_f32_16x16x32_f16 v[50:53], v[202:205], v[154:157], v[82:85]
	v_mfma_f32_16x16x32_f16 v[210:213], v[6:9], v[158:161], v[50:53]
	v_mfma_f32_16x16x32_f16 v[50:53], v[194:197], v[162:165], v[130:133]
	v_mfma_f32_16x16x32_f16 v[214:217], v[198:201], v[166:169], v[50:53]
	v_mfma_f32_16x16x32_f16 v[50:53], v[202:205], v[162:165], v[134:137]
	v_mfma_f32_16x16x32_f16 v[166:169], v[6:9], v[166:169], v[50:53]
	v_mfma_f32_16x16x32_f16 v[50:53], v[194:197], v[186:189], v[118:121]
	v_mfma_f32_16x16x32_f16 v[22:25], v[194:197], v[76:79], v[22:25]
	v_mfma_f32_16x16x32_f16 v[38:41], v[202:205], v[76:79], v[38:41]
	v_mfma_f32_16x16x32_f16 v[194:197], v[198:201], v[190:193], v[50:53]
	v_mfma_f32_16x16x32_f16 v[50:53], v[202:205], v[186:189], v[122:125]
	v_mfma_f32_16x16x32_f16 v[22:25], v[198:201], v[150:153], v[22:25]
	v_mfma_f32_16x16x32_f16 v[38:41], v[6:9], v[150:153], v[38:41]
	v_mfma_f32_16x16x32_f16 v[46:49], v[198:201], v[158:161], v[46:49]
	v_mfma_f32_16x16x32_f16 v[186:189], v[6:9], v[190:193], v[50:53]
	s_setprio 0
	s_barrier
	ds_read_b128 v[6:9], v10
	ds_read_b128 v[82:85], v11
	ds_read_b128 v[190:193], v12
	ds_read_b128 v[10:13], v13
	ds_read_b128 v[50:53], v1 offset:32768
	ds_read_b128 v[76:79], v1 offset:33792
	ds_read_b128 v[118:121], v1 offset:34816
	ds_read_b128 v[126:129], v1 offset:35840
	ds_read_b128 v[198:201], v1 offset:36864
	ds_read_b128 v[202:205], v1 offset:37888
	ds_read_b128 v[218:221], v1 offset:38912
	ds_read_b128 v[222:225], v1 offset:39936
	s_waitcnt vmcnt(2)
	s_barrier
	s_waitcnt lgkmcnt(0)
	s_setprio 1
	s_waitcnt lgkmcnt(0)
	v_mfma_f32_16x16x32_f16 v[86:89], v[6:9], v[50:53], v[86:89]
	v_mfma_f32_16x16x32_f16 v[162:165], v[82:85], v[76:79], v[86:89]
	v_mfma_f32_16x16x32_f16 v[86:89], v[190:193], v[50:53], v[90:93]
	v_mfma_f32_16x16x32_f16 v[154:157], v[10:13], v[76:79], v[86:89]
	v_mfma_f32_16x16x32_f16 v[86:89], v[6:9], v[118:121], v[94:97]
	v_mfma_f32_16x16x32_f16 v[146:149], v[82:85], v[126:129], v[86:89]
	v_mfma_f32_16x16x32_f16 v[86:89], v[190:193], v[118:121], v[98:101]
	v_mfma_f32_16x16x32_f16 v[138:141], v[10:13], v[126:129], v[86:89]
	v_mfma_f32_16x16x32_f16 v[86:89], v[6:9], v[198:201], v[102:105]
	v_mfma_f32_16x16x32_f16 v[130:133], v[82:85], v[202:205], v[86:89]
	v_mfma_f32_16x16x32_f16 v[86:89], v[190:193], v[198:201], v[106:109]
	v_mfma_f32_16x16x32_f16 v[122:125], v[10:13], v[202:205], v[86:89]
	v_mfma_f32_16x16x32_f16 v[86:89], v[6:9], v[218:221], v[110:113]
	v_mfma_f32_16x16x32_f16 v[110:113], v[82:85], v[222:225], v[86:89]
	v_mfma_f32_16x16x32_f16 v[86:89], v[190:193], v[218:221], v[114:117]
	v_mfma_f32_16x16x32_f16 v[102:105], v[10:13], v[222:225], v[86:89]
	s_setprio 0
	s_barrier
	ds_read_b128 v[114:117], v14
	ds_read_b128 v[226:229], v15
	ds_read_b128 v[230:233], v16
	ds_read_b128 v[234:237], v17
	s_waitcnt vmcnt(0)
	s_barrier
	s_waitcnt lgkmcnt(0)
	s_setprio 1
	s_waitcnt lgkmcnt(0)
	v_mfma_f32_16x16x32_f16 v[14:17], v[114:117], v[50:53], v[30:33]
	v_mfma_f32_16x16x32_f16 v[158:161], v[226:229], v[76:79], v[14:17]
	v_mfma_f32_16x16x32_f16 v[14:17], v[230:233], v[50:53], v[18:21]
	v_mfma_f32_16x16x32_f16 v[150:153], v[234:237], v[76:79], v[14:17]
	v_mfma_f32_16x16x32_f16 v[14:17], v[114:117], v[118:121], v[34:37]
	v_mfma_f32_16x16x32_f16 v[142:145], v[226:229], v[126:129], v[14:17]
	v_mfma_f32_16x16x32_f16 v[14:17], v[230:233], v[118:121], v[56:59]
	v_mfma_f32_16x16x32_f16 v[134:137], v[234:237], v[126:129], v[14:17]
	v_mfma_f32_16x16x32_f16 v[14:17], v[114:117], v[198:201], v[60:63]
	v_mfma_f32_16x16x32_f16 v[126:129], v[226:229], v[202:205], v[14:17]
	v_mfma_f32_16x16x32_f16 v[14:17], v[230:233], v[198:201], v[64:67]
	v_mfma_f32_16x16x32_f16 v[118:121], v[234:237], v[202:205], v[14:17]
	v_mfma_f32_16x16x32_f16 v[14:17], v[114:117], v[218:221], v[68:71]
	v_mfma_f32_16x16x32_f16 v[106:109], v[226:229], v[222:225], v[14:17]
	v_mfma_f32_16x16x32_f16 v[14:17], v[230:233], v[218:221], v[72:75]
	v_mfma_f32_16x16x32_f16 v[98:101], v[234:237], v[222:225], v[14:17]
	s_setprio 0
	s_barrier
	ds_read_b128 v[18:21], v1 offset:49152
	ds_read_b128 v[30:33], v1 offset:50176
	ds_read_b128 v[34:37], v1 offset:51200
	ds_read_b128 v[54:57], v1 offset:52224
	ds_read_b128 v[58:61], v1 offset:53248
	ds_read_b128 v[198:201], v1 offset:54272
	ds_read_b128 v[202:205], v1 offset:55296
	ds_read_b128 v[218:221], v1 offset:56320
	s_barrier
	s_waitcnt lgkmcnt(0)
	s_setprio 1
	s_waitcnt lgkmcnt(0)
	v_mfma_f32_16x16x32_f16 v[14:17], v[6:9], v[18:21], v[26:29]
	v_mfma_f32_16x16x32_f16 v[94:97], v[82:85], v[30:33], v[14:17]
	v_mfma_f32_16x16x32_f16 v[14:17], v[190:193], v[18:21], v[42:45]
	v_mfma_f32_16x16x32_f16 v[86:89], v[10:13], v[30:33], v[14:17]
	v_mfma_f32_16x16x32_f16 v[14:17], v[6:9], v[34:37], v[170:173]
	v_mfma_f32_16x16x32_f16 v[78:81], v[82:85], v[54:57], v[14:17]
	v_mfma_f32_16x16x32_f16 v[14:17], v[190:193], v[34:37], v[174:177]
	v_mfma_f32_16x16x32_f16 v[70:73], v[10:13], v[54:57], v[14:17]
	v_mfma_f32_16x16x32_f16 v[14:17], v[6:9], v[58:61], v[178:181]
	v_mfma_f32_16x16x32_f16 v[62:65], v[82:85], v[198:201], v[14:17]
	v_mfma_f32_16x16x32_f16 v[14:17], v[190:193], v[58:61], v[182:185]
	v_mfma_f32_16x16x32_f16 v[6:9], v[6:9], v[202:205], v[206:209]
	v_mfma_f32_16x16x32_f16 v[2:5], v[190:193], v[202:205], v[2:5]
	v_mfma_f32_16x16x32_f16 v[50:53], v[10:13], v[198:201], v[14:17]
	v_mfma_f32_16x16x32_f16 v[14:17], v[82:85], v[218:221], v[6:9]
	v_mfma_f32_16x16x32_f16 v[10:13], v[10:13], v[218:221], v[2:5]
	s_setprio 0
	s_setprio 1
	v_mfma_f32_16x16x32_f16 v[2:5], v[114:117], v[18:21], v[22:25]
	v_mfma_f32_16x16x32_f16 v[6:9], v[230:233], v[18:21], v[38:41]
	v_mfma_f32_16x16x32_f16 v[90:93], v[226:229], v[30:33], v[2:5]
	v_mfma_f32_16x16x32_f16 v[2:5], v[114:117], v[34:37], v[46:49]
	v_mfma_f32_16x16x32_f16 v[82:85], v[234:237], v[30:33], v[6:9]
	v_mfma_f32_16x16x32_f16 v[6:9], v[230:233], v[34:37], v[210:213]
	v_mfma_f32_16x16x32_f16 v[74:77], v[226:229], v[54:57], v[2:5]
	v_mfma_f32_16x16x32_f16 v[2:5], v[114:117], v[58:61], v[214:217]
	v_mfma_f32_16x16x32_f16 v[66:69], v[234:237], v[54:57], v[6:9]
	v_mfma_f32_16x16x32_f16 v[6:9], v[230:233], v[58:61], v[166:169]
	v_mfma_f32_16x16x32_f16 v[58:61], v[226:229], v[198:201], v[2:5]
	v_mfma_f32_16x16x32_f16 v[2:5], v[114:117], v[202:205], v[194:197]
	v_mfma_f32_16x16x32_f16 v[34:37], v[234:237], v[198:201], v[6:9]
	v_mfma_f32_16x16x32_f16 v[6:9], v[226:229], v[218:221], v[2:5]
	v_mfma_f32_16x16x32_f16 v[2:5], v[230:233], v[202:205], v[186:189]
	v_mfma_f32_16x16x32_f16 v[2:5], v[234:237], v[218:221], v[2:5]
	s_setprio 0
	s_barrier
	s_add_i32 s0, 0, 0x20800
	v_bfe_u32 v166, v0, 4, 2
	v_bfe_u32 v1, v0, 6, 2
	v_lshlrev_b32_e32 v18, 5, v166
	v_lshl_or_b32 v18, v1, 7, v18
	v_add_u32_e32 v19, s0, v18
	s_add_i32 s1, 0, 0x20c00
	v_add_u32_e32 v20, s1, v18
	ds_read_b128 v[54:57], v19
	ds_read_b128 v[46:49], v20
	v_or_b32_e32 v19, 16, v18
	v_add_u32_e32 v20, s0, v19
	v_add_u32_e32 v19, s1, v19
	ds_read_b128 v[42:45], v20
	ds_read_b128 v[38:41], v19
	v_or_b32_e32 v19, 0x200, v18
	v_add_u32_e32 v20, s0, v19
	v_add_u32_e32 v19, s1, v19
	v_or_b32_e32 v18, 0x210, v18
	ds_read_b128 v[30:33], v20
	ds_read_b128 v[26:29], v19
	v_add_u32_e32 v19, s0, v18
	v_and_b32_e32 v114, 15, v0
	v_ashrrev_i32_e32 v0, 2, v0
	s_movk_i32 s0, 0xffc0
	v_and_or_b32 v169, v0, s0, v114
	s_add_i32 s0, 0, 0x20000
	v_add_u32_e32 v18, s1, v18
	v_lshl_add_u32 v168, v169, 3, s0
	ds_read_b128 v[22:25], v19
	ds_read_b128 v[18:21], v18
	s_waitcnt vmcnt(0)
	ds_read2st64_b64 v[114:117], v168 offset1:2
	v_lshlrev_b32_e32 v0, 5, v1
	v_lshlrev_b32_e32 v1, 3, v166
	v_or3_b32 v166, v0, v1, s13
	v_add_u32_e32 v167, s12, v169
	s_waitcnt lgkmcnt(0)
	v_fma_f32 v154, -v114, v42, v154
	v_fma_f32 v154, v115, v154, v38
	v_fma_f32 v1, -v114, v54, v162
	v_fma_f32 v162, -v114, v55, v163
	v_fma_f32 v163, -v114, v56, v164
	v_fma_f32 v164, -v114, v57, v165
	v_max_f32_e32 v165, 0, v154
	v_fma_f32 v154, -v114, v43, v155
	v_fma_f32 v154, v115, v154, v39
	v_max_f32_e32 v170, 0, v154
	v_fma_f32 v154, -v114, v44, v156
	v_fma_f32 v154, v115, v154, v40
	v_max_f32_e32 v156, 0, v154
	v_fma_f32 v154, -v114, v45, v157
	v_fma_f32 v1, v115, v1, v46
	v_fma_f32 v162, v115, v162, v47
	v_fma_f32 v163, v115, v163, v48
	v_fma_f32 v164, v115, v164, v49
	v_fma_f32 v154, v115, v154, v41
	v_mul_lo_u32 v0, v167, s6
	v_max_f32_e32 v1, 0, v1
	v_max_f32_e32 v162, 0, v162
	v_max_f32_e32 v163, 0, v163
	v_max_f32_e32 v164, 0, v164
	v_max_f32_e32 v157, 0, v154
	s_and_b32 s9, s9, 0xffff
	s_mov_b32 s11, 0x20000
	s_mov_b32 s10, 0x7ffffff0
	v_cvt_pk_f16_f32 v155, v163, v164
	v_cvt_pk_f16_f32 v154, v1, v162
	v_cvt_pk_f16_f32 v157, v156, v157
	v_cvt_pk_f16_f32 v156, v165, v170
	v_add_lshl_u32 v0, v166, v0, 1
	buffer_store_dwordx4 v[154:157], v0, s[8:11], 0 offen sc1
	v_fma_f32 v1, -v114, v30, v158
	v_fma_f32 v150, -v114, v22, v150
	v_fma_f32 v154, -v114, v31, v159
	v_fma_f32 v155, -v114, v32, v160
	v_fma_f32 v156, -v114, v33, v161
	v_fma_f32 v151, -v114, v23, v151
	v_fma_f32 v152, -v114, v24, v152
	v_fma_f32 v114, -v114, v25, v153
	v_fma_f32 v1, v115, v1, v26
	v_fma_f32 v154, v115, v154, v27
	v_fma_f32 v155, v115, v155, v28
	v_fma_f32 v156, v115, v156, v29
	v_fma_f32 v150, v115, v150, v18
	v_fma_f32 v151, v115, v151, v19
	v_fma_f32 v152, v115, v152, v20
	v_fma_f32 v114, v115, v114, v21
	v_max_f32_e32 v1, 0, v1
	v_max_f32_e32 v154, 0, v154
	v_max_f32_e32 v155, 0, v155
	v_max_f32_e32 v156, 0, v156
	v_max_f32_e32 v150, 0, v150
	v_max_f32_e32 v151, 0, v151
	v_max_f32_e32 v152, 0, v152
	v_max_f32_e32 v114, 0, v114
	v_cvt_pk_f16_f32 v153, v152, v114
	v_cvt_pk_f16_f32 v152, v150, v151
	v_cvt_pk_f16_f32 v151, v155, v156
	v_cvt_pk_f16_f32 v150, v1, v154
	buffer_store_dwordx4 v[150:153], v0, s[8:11], 0 offen offset:256 sc1
	v_or_b32_e32 v0, 16, v169
	v_add_u32_e32 v114, s12, v0
	v_lshl_add_u32 v0, v0, 3, s0
	ds_read_b64 v[0:1], v0
	v_or_b32_e32 v155, 32, v169
	v_or_b32_e32 v156, 48, v169
	v_mul_lo_u32 v154, v114, s6
	v_lshl_add_u32 v114, v155, 3, s0
	s_waitcnt lgkmcnt(0)
	v_fma_f32 v146, -v0, v54, v146
	v_fma_f32 v147, -v0, v55, v147
	v_fma_f32 v148, -v0, v56, v148
	v_fma_f32 v149, -v0, v57, v149
	v_fma_f32 v138, -v0, v42, v138
	v_fma_f32 v139, -v0, v43, v139
	v_fma_f32 v140, -v0, v44, v140
	v_fma_f32 v141, -v0, v45, v141
	v_fma_f32 v146, v1, v146, v46
	v_fma_f32 v147, v1, v147, v47
	v_fma_f32 v148, v1, v148, v48
	v_fma_f32 v149, v1, v149, v49
	v_fma_f32 v138, v1, v138, v38
	v_fma_f32 v139, v1, v139, v39
	v_fma_f32 v140, v1, v140, v40
	v_fma_f32 v141, v1, v141, v41
	v_lshl_add_u32 v115, v156, 3, s0
	v_max_f32_e32 v146, 0, v146
	v_max_f32_e32 v147, 0, v147
	v_max_f32_e32 v148, 0, v148
	v_max_f32_e32 v149, 0, v149
	v_max_f32_e32 v138, 0, v138
	v_max_f32_e32 v139, 0, v139
	v_max_f32_e32 v140, 0, v140
	v_max_f32_e32 v141, 0, v141
	ds_read_b64 v[152:153], v114
	ds_read_b64 v[114:115], v115
	ds_read_b64 v[150:151], v168 offset:1408
	v_cvt_pk_f16_f32 v141, v140, v141
	v_cvt_pk_f16_f32 v140, v138, v139
	v_cvt_pk_f16_f32 v139, v148, v149
	v_cvt_pk_f16_f32 v138, v146, v147
	v_add_lshl_u32 v146, v166, v154, 1
	buffer_store_dwordx4 v[138:141], v146, s[8:11], 0 offen sc1
	s_and_saveexec_b64 s[24:25], vcc
	s_cbranch_execz .LBB8_8
	s_barrier
.LBB8_8:
	s_or_b64 exec, exec, s[24:25]
	v_fma_f32 v134, -v0, v22, v134
	v_fma_f32 v135, -v0, v23, v135
	v_fma_f32 v138, -v0, v30, v142
	v_fma_f32 v139, -v0, v31, v143
	v_fma_f32 v140, -v0, v32, v144
	v_fma_f32 v141, -v0, v33, v145
	v_fma_f32 v136, -v0, v24, v136
	v_fma_f32 v0, -v0, v25, v137
	v_fma_f32 v136, v1, v136, v20
	v_fma_f32 v0, v1, v0, v21
	v_fma_f32 v138, v1, v138, v26
	v_fma_f32 v139, v1, v139, v27
	v_fma_f32 v140, v1, v140, v28
	v_fma_f32 v141, v1, v141, v29
	v_fma_f32 v134, v1, v134, v18
	v_fma_f32 v135, v1, v135, v19
	v_max_f32_e32 v136, 0, v136
	v_max_f32_e32 v0, 0, v0
	s_waitcnt lgkmcnt(2)
	v_fma_f32 v1, -v152, v54, v130
	v_fma_f32 v130, -v152, v55, v131
	v_fma_f32 v131, -v152, v56, v132
	v_fma_f32 v132, -v152, v57, v133
	v_fma_f32 v122, -v152, v42, v122
	v_fma_f32 v123, -v152, v43, v123
	v_fma_f32 v124, -v152, v44, v124
	v_fma_f32 v125, -v152, v45, v125
	v_cvt_pk_f16_f32 v137, v136, v0
	v_add_u32_e32 v0, s12, v155
	v_fma_f32 v1, v153, v1, v46
	v_fma_f32 v130, v153, v130, v47
	v_fma_f32 v131, v153, v131, v48
	v_fma_f32 v132, v153, v132, v49
	v_fma_f32 v122, v153, v122, v38
	v_fma_f32 v123, v153, v123, v39
	v_fma_f32 v124, v153, v124, v40
	v_fma_f32 v125, v153, v125, v41
	v_max_f32_e32 v138, 0, v138
	v_max_f32_e32 v139, 0, v139
	v_max_f32_e32 v140, 0, v140
	v_max_f32_e32 v141, 0, v141
	v_max_f32_e32 v134, 0, v134
	v_max_f32_e32 v135, 0, v135
	v_mul_lo_u32 v0, v0, s6
	v_max_f32_e32 v1, 0, v1
	v_max_f32_e32 v130, 0, v130
	v_max_f32_e32 v131, 0, v131
	v_max_f32_e32 v132, 0, v132
	v_max_f32_e32 v122, 0, v122
	v_max_f32_e32 v123, 0, v123
	v_max_f32_e32 v124, 0, v124
	v_max_f32_e32 v125, 0, v125
	v_cvt_pk_f16_f32 v136, v134, v135
	v_cvt_pk_f16_f32 v135, v140, v141
	v_cvt_pk_f16_f32 v134, v138, v139
	v_cvt_pk_f16_f32 v125, v124, v125
	v_cvt_pk_f16_f32 v124, v122, v123
	v_cvt_pk_f16_f32 v123, v131, v132
	v_cvt_pk_f16_f32 v122, v1, v130
	v_add_lshl_u32 v0, v166, v0, 1
	buffer_store_dwordx4 v[134:137], v146, s[8:11], 0 offen offset:256 sc1
	buffer_store_dwordx4 v[122:125], v0, s[8:11], 0 offen sc1
	v_fma_f32 v1, -v152, v30, v126
	v_fma_f32 v118, -v152, v22, v118
	v_fma_f32 v122, -v152, v31, v127
	v_fma_f32 v123, -v152, v32, v128
	v_fma_f32 v124, -v152, v33, v129
	v_fma_f32 v119, -v152, v23, v119
	v_fma_f32 v120, -v152, v24, v120
	v_fma_f32 v121, -v152, v25, v121
	v_fma_f32 v1, v153, v1, v26
	v_fma_f32 v122, v153, v122, v27
	v_fma_f32 v123, v153, v123, v28
	v_fma_f32 v124, v153, v124, v29
	v_fma_f32 v118, v153, v118, v18
	v_fma_f32 v119, v153, v119, v19
	v_fma_f32 v120, v153, v120, v20
	v_fma_f32 v121, v153, v121, v21
	v_max_f32_e32 v1, 0, v1
	v_max_f32_e32 v122, 0, v122
	v_max_f32_e32 v123, 0, v123
	v_max_f32_e32 v124, 0, v124
	v_max_f32_e32 v118, 0, v118
	v_max_f32_e32 v119, 0, v119
	v_max_f32_e32 v120, 0, v120
	v_max_f32_e32 v121, 0, v121
	v_cvt_pk_f16_f32 v121, v120, v121
	v_cvt_pk_f16_f32 v120, v118, v119
	v_cvt_pk_f16_f32 v119, v123, v124
	v_cvt_pk_f16_f32 v118, v1, v122
	s_waitcnt lgkmcnt(1)
	v_fma_f32 v1, -v114, v54, v110
	v_fma_f32 v110, -v114, v55, v111
	v_fma_f32 v111, -v114, v56, v112
	v_fma_f32 v112, -v114, v57, v113
	v_fma_f32 v102, -v114, v42, v102
	v_fma_f32 v103, -v114, v43, v103
	v_fma_f32 v104, -v114, v44, v104
	v_fma_f32 v105, -v114, v45, v105
	buffer_store_dwordx4 v[118:121], v0, s[8:11], 0 offen offset:256 sc1
	v_add_u32_e32 v0, s12, v156
	v_fma_f32 v1, v115, v1, v46
	v_fma_f32 v110, v115, v110, v47
	v_fma_f32 v111, v115, v111, v48
	v_fma_f32 v112, v115, v112, v49
	v_fma_f32 v102, v115, v102, v38
	v_fma_f32 v103, v115, v103, v39
	v_fma_f32 v104, v115, v104, v40
	v_fma_f32 v105, v115, v105, v41
	v_mul_lo_u32 v0, v0, s6
	v_max_f32_e32 v1, 0, v1
	v_max_f32_e32 v110, 0, v110
	v_max_f32_e32 v111, 0, v111
	v_max_f32_e32 v112, 0, v112
	v_max_f32_e32 v102, 0, v102
	v_max_f32_e32 v103, 0, v103
	v_max_f32_e32 v104, 0, v104
	v_max_f32_e32 v105, 0, v105
	v_cvt_pk_f16_f32 v105, v104, v105
	v_cvt_pk_f16_f32 v104, v102, v103
	v_cvt_pk_f16_f32 v103, v111, v112
	v_cvt_pk_f16_f32 v102, v1, v110
	v_add_lshl_u32 v0, v166, v0, 1
	buffer_store_dwordx4 v[102:105], v0, s[8:11], 0 offen sc1
	v_fma_f32 v1, -v114, v30, v106
	v_fma_f32 v98, -v114, v22, v98
	v_fma_f32 v102, -v114, v31, v107
	v_fma_f32 v103, -v114, v32, v108
	v_fma_f32 v104, -v114, v33, v109
	v_fma_f32 v99, -v114, v23, v99
	v_fma_f32 v100, -v114, v24, v100
	v_fma_f32 v101, -v114, v25, v101
	v_fma_f32 v1, v115, v1, v26
	v_fma_f32 v102, v115, v102, v27
	v_fma_f32 v103, v115, v103, v28
	v_fma_f32 v104, v115, v104, v29
	v_fma_f32 v98, v115, v98, v18
	v_fma_f32 v99, v115, v99, v19
	v_fma_f32 v100, v115, v100, v20
	v_fma_f32 v101, v115, v101, v21
	v_max_f32_e32 v1, 0, v1
	v_max_f32_e32 v102, 0, v102
	v_max_f32_e32 v103, 0, v103
	v_max_f32_e32 v104, 0, v104
	v_max_f32_e32 v98, 0, v98
	v_max_f32_e32 v99, 0, v99
	v_max_f32_e32 v100, 0, v100
	v_max_f32_e32 v101, 0, v101
	v_cvt_pk_f16_f32 v101, v100, v101
	v_cvt_pk_f16_f32 v100, v98, v99
	v_cvt_pk_f16_f32 v99, v103, v104
	v_cvt_pk_f16_f32 v98, v1, v102
	v_fma_f32 v1, -v116, v54, v94
	v_fma_f32 v94, -v116, v55, v95
	v_fma_f32 v95, -v116, v56, v96
	v_fma_f32 v96, -v116, v57, v97
	v_fma_f32 v86, -v116, v42, v86
	v_fma_f32 v87, -v116, v43, v87
	v_fma_f32 v88, -v116, v44, v88
	v_fma_f32 v89, -v116, v45, v89
	buffer_store_dwordx4 v[98:101], v0, s[8:11], 0 offen offset:256 sc1
	v_add_u32_e32 v0, 0x80, v167
	v_fma_f32 v1, v117, v1, v46
	v_fma_f32 v94, v117, v94, v47
	v_fma_f32 v95, v117, v95, v48
	v_fma_f32 v96, v117, v96, v49
	v_fma_f32 v86, v117, v86, v38
	v_fma_f32 v87, v117, v87, v39
	v_fma_f32 v88, v117, v88, v40
	v_fma_f32 v89, v117, v89, v41
	v_mul_lo_u32 v0, v0, s6
	v_max_f32_e32 v1, 0, v1
	v_max_f32_e32 v94, 0, v94
	v_max_f32_e32 v95, 0, v95
	v_max_f32_e32 v96, 0, v96
	v_max_f32_e32 v86, 0, v86
	v_max_f32_e32 v87, 0, v87
	v_max_f32_e32 v88, 0, v88
	v_max_f32_e32 v89, 0, v89
	v_cvt_pk_f16_f32 v89, v88, v89
	v_cvt_pk_f16_f32 v88, v86, v87
	v_cvt_pk_f16_f32 v87, v95, v96
	v_cvt_pk_f16_f32 v86, v1, v94
	v_add_lshl_u32 v0, v166, v0, 1
	buffer_store_dwordx4 v[86:89], v0, s[8:11], 0 offen sc1
	v_fma_f32 v1, -v116, v30, v90
	v_fma_f32 v82, -v116, v22, v82
	v_fma_f32 v86, -v116, v31, v91
	v_fma_f32 v86, v117, v86, v27
	v_max_f32_e32 v90, 0, v86
	v_fma_f32 v86, -v116, v32, v92
	v_fma_f32 v87, -v116, v33, v93
	v_fma_f32 v83, -v116, v23, v83
	v_fma_f32 v84, -v116, v24, v84
	v_fma_f32 v85, -v116, v25, v85
	v_fma_f32 v86, v117, v86, v28
	v_fma_f32 v87, v117, v87, v29
	v_fma_f32 v82, v117, v82, v18
	v_fma_f32 v83, v117, v83, v19
	v_fma_f32 v84, v117, v84, v20
	v_fma_f32 v85, v117, v85, v21
	v_max_f32_e32 v86, 0, v86
	v_max_f32_e32 v87, 0, v87
	v_max_f32_e32 v82, 0, v82
	v_max_f32_e32 v83, 0, v83
	v_max_f32_e32 v84, 0, v84
	v_max_f32_e32 v85, 0, v85
	v_cvt_pk_f16_f32 v85, v84, v85
	v_cvt_pk_f16_f32 v84, v82, v83
	v_cvt_pk_f16_f32 v83, v86, v87
	ds_read2_b64 v[86:89], v168 offset0:144 offset1:160
	v_fma_f32 v1, v117, v1, v26
	v_max_f32_e32 v1, 0, v1
	v_cvt_pk_f16_f32 v82, v1, v90
	buffer_store_dwordx4 v[82:85], v0, s[8:11], 0 offen offset:256 sc1
	s_waitcnt lgkmcnt(0)
	v_fma_f32 v1, -v86, v54, v78
	v_fma_f32 v78, -v86, v55, v79
	v_fma_f32 v79, -v86, v56, v80
	v_fma_f32 v80, -v86, v57, v81
	v_fma_f32 v70, -v86, v42, v70
	v_fma_f32 v71, -v86, v43, v71
	v_fma_f32 v72, -v86, v44, v72
	v_fma_f32 v73, -v86, v45, v73
	v_add_u32_e32 v0, 0x90, v167
	v_fma_f32 v1, v87, v1, v46
	v_fma_f32 v78, v87, v78, v47
	v_fma_f32 v79, v87, v79, v48
	v_fma_f32 v80, v87, v80, v49
	v_fma_f32 v70, v87, v70, v38
	v_fma_f32 v71, v87, v71, v39
	v_fma_f32 v72, v87, v72, v40
	v_fma_f32 v73, v87, v73, v41
	v_mul_lo_u32 v0, v0, s6
	v_max_f32_e32 v1, 0, v1
	v_max_f32_e32 v78, 0, v78
	v_max_f32_e32 v79, 0, v79
	v_max_f32_e32 v80, 0, v80
	v_max_f32_e32 v70, 0, v70
	v_max_f32_e32 v71, 0, v71
	v_max_f32_e32 v72, 0, v72
	v_max_f32_e32 v73, 0, v73
	v_cvt_pk_f16_f32 v73, v72, v73
	v_cvt_pk_f16_f32 v72, v70, v71
	v_cvt_pk_f16_f32 v71, v79, v80
	v_cvt_pk_f16_f32 v70, v1, v78
	v_add_lshl_u32 v0, v166, v0, 1
	buffer_store_dwordx4 v[70:73], v0, s[8:11], 0 offen sc1
	v_fma_f32 v1, -v86, v30, v74
	v_fma_f32 v66, -v86, v22, v66
	v_fma_f32 v70, -v86, v31, v75
	v_fma_f32 v71, -v86, v32, v76
	v_fma_f32 v72, -v86, v33, v77
	v_fma_f32 v67, -v86, v23, v67
	v_fma_f32 v68, -v86, v24, v68
	v_fma_f32 v69, -v86, v25, v69
	v_fma_f32 v1, v87, v1, v26
	v_fma_f32 v70, v87, v70, v27
	v_fma_f32 v71, v87, v71, v28
	v_fma_f32 v72, v87, v72, v29
	v_fma_f32 v66, v87, v66, v18
	v_fma_f32 v67, v87, v67, v19
	v_fma_f32 v68, v87, v68, v20
	v_fma_f32 v69, v87, v69, v21
	v_max_f32_e32 v1, 0, v1
	v_max_f32_e32 v70, 0, v70
	v_max_f32_e32 v71, 0, v71
	v_max_f32_e32 v72, 0, v72
	v_max_f32_e32 v66, 0, v66
	v_max_f32_e32 v67, 0, v67
	v_max_f32_e32 v68, 0, v68
	v_max_f32_e32 v69, 0, v69
	v_cvt_pk_f16_f32 v69, v68, v69
	v_cvt_pk_f16_f32 v68, v66, v67
	v_cvt_pk_f16_f32 v67, v71, v72
	v_cvt_pk_f16_f32 v66, v1, v70
	v_fma_f32 v1, -v88, v54, v62
	v_fma_f32 v62, -v88, v55, v63
	v_fma_f32 v63, -v88, v56, v64
	v_fma_f32 v64, -v88, v57, v65
	v_fma_f32 v50, -v88, v42, v50
	v_fma_f32 v51, -v88, v43, v51
	v_fma_f32 v52, -v88, v44, v52
	v_fma_f32 v53, -v88, v45, v53
	buffer_store_dwordx4 v[66:69], v0, s[8:11], 0 offen offset:256 sc1
	v_add_u32_e32 v0, 0xa0, v167
	v_fma_f32 v1, v89, v1, v46
	v_fma_f32 v62, v89, v62, v47
	v_fma_f32 v63, v89, v63, v48
	v_fma_f32 v64, v89, v64, v49
	v_fma_f32 v50, v89, v50, v38
	v_fma_f32 v51, v89, v51, v39
	v_fma_f32 v52, v89, v52, v40
	v_fma_f32 v53, v89, v53, v41
	v_mul_lo_u32 v0, v0, s6
	v_max_f32_e32 v1, 0, v1
	v_max_f32_e32 v62, 0, v62
	v_max_f32_e32 v63, 0, v63
	v_max_f32_e32 v64, 0, v64
	v_max_f32_e32 v50, 0, v50
	v_max_f32_e32 v51, 0, v51
	v_max_f32_e32 v52, 0, v52
	v_max_f32_e32 v53, 0, v53
	v_cvt_pk_f16_f32 v53, v52, v53
	v_cvt_pk_f16_f32 v52, v50, v51
	v_cvt_pk_f16_f32 v51, v63, v64
	v_cvt_pk_f16_f32 v50, v1, v62
	v_add_lshl_u32 v0, v166, v0, 1
	buffer_store_dwordx4 v[50:53], v0, s[8:11], 0 offen sc1
	v_fma_f32 v1, -v88, v30, v58
	v_fma_f32 v34, -v88, v22, v34
	v_fma_f32 v50, -v88, v31, v59
	v_fma_f32 v35, -v88, v23, v35
	v_fma_f32 v36, -v88, v24, v36
	v_fma_f32 v37, -v88, v25, v37
	v_fma_f32 v1, v89, v1, v26
	v_fma_f32 v50, v89, v50, v27
	v_fma_f32 v34, v89, v34, v18
	v_fma_f32 v35, v89, v35, v19
	v_fma_f32 v36, v89, v36, v20
	v_fma_f32 v37, v89, v37, v21
	v_max_f32_e32 v1, 0, v1
	v_max_f32_e32 v50, 0, v50
	v_fma_f32 v51, -v88, v32, v60
	v_fma_f32 v52, -v88, v33, v61
	v_max_f32_e32 v34, 0, v34
	v_max_f32_e32 v35, 0, v35
	v_max_f32_e32 v36, 0, v36
	v_max_f32_e32 v37, 0, v37
	v_fma_f32 v51, v89, v51, v28
	v_fma_f32 v52, v89, v52, v29
	v_cvt_pk_f16_f32 v37, v36, v37
	v_cvt_pk_f16_f32 v36, v34, v35
	v_cvt_pk_f16_f32 v34, v1, v50
	v_fma_f32 v1, -v150, v54, v14
	v_fma_f32 v14, -v150, v55, v15
	v_fma_f32 v10, -v150, v42, v10
	v_fma_f32 v11, -v150, v43, v11
	v_fma_f32 v12, -v150, v44, v12
	v_fma_f32 v13, -v150, v45, v13
	v_max_f32_e32 v51, 0, v51
	v_max_f32_e32 v52, 0, v52
	v_fma_f32 v1, v151, v1, v46
	v_fma_f32 v14, v151, v14, v47
	v_fma_f32 v10, v151, v10, v38
	v_fma_f32 v11, v151, v11, v39
	v_fma_f32 v12, v151, v12, v40
	v_fmac_f32_e32 v41, v151, v13
	v_cvt_pk_f16_f32 v35, v51, v52
	v_max_f32_e32 v1, 0, v1
	v_max_f32_e32 v14, 0, v14
	v_max_f32_e32 v10, 0, v10
	v_max_f32_e32 v11, 0, v11
	v_max_f32_e32 v12, 0, v12
	v_max_f32_e32 v13, 0, v41
	buffer_store_dwordx4 v[34:37], v0, s[8:11], 0 offen offset:256 sc1
	v_add_u32_e32 v0, 0xb0, v167
	v_cvt_pk_f16_f32 v13, v12, v13
	v_cvt_pk_f16_f32 v12, v10, v11
	v_cvt_pk_f16_f32 v10, v1, v14
	v_fma_f32 v1, -v150, v31, v7
	v_fma_f32 v3, -v150, v23, v3
	v_mul_lo_u32 v0, v0, s6
	v_fma_f32 v1, v151, v1, v27
	v_fma_f32 v3, v151, v3, v19
	v_fma_f32 v15, -v150, v56, v16
	v_fma_f32 v16, -v150, v57, v17
	v_add_lshl_u32 v14, v166, v0, 1
	v_fma_f32 v0, -v150, v30, v6
	v_max_f32_e32 v6, 0, v1
	v_fma_f32 v1, -v150, v32, v8
	v_fma_f32 v7, -v150, v33, v9
	v_fma_f32 v2, -v150, v22, v2
	v_max_f32_e32 v8, 0, v3
	v_fma_f32 v3, -v150, v24, v4
	v_fma_f32 v4, -v150, v25, v5
	v_fma_f32 v15, v151, v15, v48
	v_fmac_f32_e32 v49, v151, v16
	v_fma_f32 v0, v151, v0, v26
	v_fma_f32 v1, v151, v1, v28
	v_fmac_f32_e32 v29, v151, v7
	v_fma_f32 v2, v151, v2, v18
	v_fma_f32 v3, v151, v3, v20
	v_fmac_f32_e32 v21, v151, v4
	v_max_f32_e32 v15, 0, v15
	v_max_f32_e32 v16, 0, v49
	v_max_f32_e32 v0, 0, v0
	v_max_f32_e32 v1, 0, v1
	v_max_f32_e32 v7, 0, v29
	v_max_f32_e32 v2, 0, v2
	v_max_f32_e32 v3, 0, v3
	v_max_f32_e32 v4, 0, v21
	v_cvt_pk_f16_f32 v11, v15, v16
	v_cvt_pk_f16_f32 v3, v3, v4
	v_cvt_pk_f16_f32 v2, v2, v8
	v_cvt_pk_f16_f32 v1, v1, v7
	v_cvt_pk_f16_f32 v0, v0, v6
	buffer_store_dwordx4 v[10:13], v14, s[8:11], 0 offen sc1
	buffer_store_dwordx4 v[0:3], v14, s[8:11], 0 offen offset:256 sc1
	s_endpgm
